# __shfl_xor butterflies (norm1, prep kk-norm, post, norm2/router wave sums, final): ds_bpermute_b32 round trips replaced by DPP row moves (quad_perm / row_half_mirror / row_mirror), bit-identical sums
# speedup vs baseline: 1.0063x; 1.0041x over previous
.LBB0_256:
	s_add_u32 s4, s46, s29
	s_addc_u32 s5, s47, s52
	global_load_dwordx4 v[126:129], v1, s[4:5] nt
	v_lshl_add_u64 v[124:125], s[46:47], 0, v[88:89]
	v_add_co_u32_e32 v150, vcc, 0x11100000, v124
	v_lshl_add_u64 v[122:123], s[46:47], 0, v[86:87]
	s_nop 0
	v_addc_co_u32_e32 v151, vcc, 0, v125, vcc
	global_load_dwordx2 v[124:125], v[150:151], off nt
	global_load_dwordx2 v[202:203], v[150:151], off offset:512 nt
	global_load_dwordx2 v[204:205], v[150:151], off offset:1024 nt
	global_load_dwordx2 v[206:207], v[150:151], off offset:1536 nt
	global_load_dwordx2 v[208:209], v[150:151], off offset:2048 nt
	global_load_dwordx2 v[210:211], v[150:151], off offset:2560 nt
	global_load_dwordx2 v[212:213], v[150:151], off offset:3072 nt
	global_load_dwordx2 v[214:215], v[150:151], off offset:3584 nt
	s_mov_b32 s4, 0x3e000000
	v_add_co_u32_e64 v122, s[38:39], s80, v122
	s_add_i32 s25, s25, s66
	s_nop 0
	v_addc_co_u32_e64 v123, s[38:39], 0, v123, s[38:39]
	v_lshl_add_u64 v[86:87], v[86:87], 0, s[22:23]
	v_lshl_add_u64 v[88:89], v[88:89], 0, s[94:95]
	s_waitcnt vmcnt(8)
	v_readfirstlane_b32 s5, v126
	v_readfirstlane_b32 s6, v127
	s_nop 0
	v_pk_mul_f32 v[126:127], v[128:129], s[4:5] op_sel_hi:[1,0]
	s_lshr_b32 s4, s5, 18
	s_lshl_b32 s5, s5, 11
	s_lshr_b32 s7, s6, 18
	s_and_b32 s4, s4, 0x3ffc
	s_and_b32 s20, s5, 0x7ffff800
	s_and_b32 s5, s7, 0x3ffc
	s_add_i32 s4, s81, s4
	s_add_i32 s5, s81, s5
	v_mov_b32_e32 v128, s4
	v_mov_b32_e32 v129, s5
	ds_read_b32 v128, v128
	ds_read_b32 v130, v129
	s_lshl_b32 s6, s6, 11
	s_waitcnt lgkmcnt(1)
	v_ashrrev_i32_e32 v129, 31, v128
	v_lshlrev_b64 v[128:129], 19, v[128:129]
	v_lshl_add_u64 v[128:129], s[48:49], 0, v[128:129]
	v_lshl_add_u64 v[128:129], v[128:129], 0, s[20:21]
	s_waitcnt lgkmcnt(0)
	v_ashrrev_i32_e32 v131, 31, v130
	v_readfirstlane_b32 s4, v128
	v_readfirstlane_b32 s5, v129
	v_lshlrev_b64 v[130:131], 19, v[130:131]
	v_lshl_add_u64 v[130:131], s[48:49], 0, v[130:131]
	s_and_b32 s20, s6, 0x7ffff800
	v_lshl_add_u64 v[130:131], v[130:131], 0, s[20:21]
	s_add_u32 s29, s29, s68
	global_load_dword v129, v170, s[4:5] nt
	v_readfirstlane_b32 s6, v130
	v_readfirstlane_b32 s7, v131
	global_load_dword v131, v170, s[4:5] offset:256 nt
	global_load_dword v145, v170, s[4:5] offset:512 nt
	global_load_dword v154, v170, s[4:5] offset:768 nt
	global_load_dword v156, v170, s[4:5] offset:1024 nt
	global_load_dword v158, v170, s[4:5] offset:1280 nt
	global_load_dword v159, v170, s[4:5] offset:1536 nt
	global_load_dword v160, v170, s[4:5] offset:1792 nt
	global_load_dword v133, v170, s[6:7] nt
	global_load_dword v141, v170, s[6:7] offset:256 nt
	global_load_dword v149, v170, s[6:7] offset:512 nt
	global_load_dword v157, v170, s[6:7] offset:768 nt
	global_load_dword v161, v170, s[6:7] offset:1024 nt
	global_load_dword v162, v170, s[6:7] offset:1280 nt
	global_load_dword v163, v170, s[6:7] offset:1536 nt
	global_load_dword v171, v170, s[6:7] offset:1792 nt
	s_addc_u32 s52, s52, s69
	s_cmp_ge_i32 s25, s28
	s_waitcnt vmcnt(14)
	v_cvt_f32_fp8_e32 v136, v131
	v_cvt_f32_fp8_sdwa v138, v131 src0_sel:BYTE_1
	v_cvt_f32_fp8_sdwa v140, v131 src0_sel:BYTE_2
	v_cvt_f32_fp8_sdwa v142, v131 src0_sel:BYTE_3
	s_waitcnt vmcnt(13)
	v_cvt_f32_fp8_sdwa v146, v145 src0_sel:BYTE_1
	v_cvt_f32_fp8_e32 v144, v145
	v_cvt_f32_fp8_sdwa v148, v145 src0_sel:BYTE_2
	s_waitcnt vmcnt(7)
	v_cvt_f32_fp8_e32 v131, v133
	v_cvt_f32_fp8_sdwa v135, v133 src0_sel:BYTE_2
	s_waitcnt vmcnt(6)
	v_cvt_f32_fp8_e32 v139, v141
	v_cvt_f32_fp8_sdwa v137, v141 src0_sel:BYTE_1
	v_cvt_f32_fp8_sdwa v130, v129 src0_sel:BYTE_1
	v_cvt_f32_fp8_sdwa v134, v129 src0_sel:BYTE_3
	v_cvt_f32_fp8_e32 v128, v129
	v_cvt_f32_fp8_sdwa v132, v129 src0_sel:BYTE_2
	v_cvt_f32_fp8_sdwa v129, v133 src0_sel:BYTE_1
	v_cvt_f32_fp8_sdwa v133, v133 src0_sel:BYTE_3
	s_waitcnt vmcnt(5)
	v_cvt_f32_fp8_e32 v147, v149
	v_cvt_f32_fp8_sdwa v143, v141 src0_sel:BYTE_2
	v_cvt_f32_fp8_sdwa v152, v145 src0_sel:BYTE_3
	v_cvt_f32_fp8_sdwa v145, v149 src0_sel:BYTE_1
	v_cvt_f32_fp8_sdwa v141, v141 src0_sel:BYTE_3
	v_pk_mul_f32 v[130:131], v[126:127], v[130:131]
	v_pk_mul_f32 v[134:135], v[126:127], v[134:135]
	v_pk_mul_f32 v[138:139], v[126:127], v[138:139]
	v_pk_fma_f32 v[128:129], v[126:127], v[128:129], v[130:131] op_sel:[0,0,1] op_sel_hi:[1,1,0]
	v_cvt_f32_fp8_e32 v130, v154
	v_pk_fma_f32 v[132:133], v[126:127], v[132:133], v[134:135] op_sel:[0,0,1] op_sel_hi:[1,1,0]
	v_cvt_f32_fp8_sdwa v134, v154 src0_sel:BYTE_1
	v_pk_fma_f32 v[136:137], v[126:127], v[136:137], v[138:139] op_sel:[0,0,1] op_sel_hi:[1,1,0]
	v_cvt_f32_fp8_sdwa v138, v154 src0_sel:BYTE_2
	v_cvt_f32_fp8_sdwa v154, v154 src0_sel:BYTE_3
	s_waitcnt vmcnt(4)
	v_cvt_f32_fp8_sdwa v155, v157 src0_sel:BYTE_2
	v_pk_mul_f32 v[146:147], v[126:127], v[146:147]
	v_cvt_f32_fp8_e32 v135, v157
	v_cvt_f32_fp8_sdwa v139, v157 src0_sel:BYTE_3
	v_pk_mul_f32 v[142:143], v[126:127], v[142:143]
	v_pk_fma_f32 v[144:145], v[126:127], v[144:145], v[146:147] op_sel:[0,0,1] op_sel_hi:[1,1,0]
	v_cvt_f32_fp8_sdwa v146, v156 src0_sel:BYTE_1
	v_cvt_f32_fp8_sdwa v131, v157 src0_sel:BYTE_1
	s_waitcnt vmcnt(3)
	v_cvt_f32_fp8_e32 v147, v161
	v_cvt_f32_fp8_sdwa v153, v149 src0_sel:BYTE_2
	v_pk_fma_f32 v[140:141], v[126:127], v[140:141], v[142:143] op_sel:[0,0,1] op_sel_hi:[1,1,0]
	v_cvt_f32_fp8_e32 v142, v156
	v_cvt_f32_fp8_sdwa v143, v161 src0_sel:BYTE_1
	v_cvt_f32_fp8_sdwa v149, v149 src0_sel:BYTE_3
	v_pk_mul_f32 v[154:155], v[126:127], v[154:155]
	v_pk_mul_f32 v[134:135], v[126:127], v[134:135]
	v_pk_fma_f32 v[172:173], v[126:127], v[138:139], v[154:155] op_sel:[0,0,1] op_sel_hi:[1,1,0]
	v_cvt_f32_fp8_sdwa v138, v158 src0_sel:BYTE_1
	s_waitcnt vmcnt(2)
	v_cvt_f32_fp8_e32 v139, v162
	v_pk_fma_f32 v[134:135], v[126:127], v[130:131], v[134:135] op_sel:[0,0,1] op_sel_hi:[1,1,0]
	v_cvt_f32_fp8_e32 v130, v158
	v_pk_mul_f32 v[146:147], v[126:127], v[146:147]
	v_cvt_f32_fp8_sdwa v154, v158 src0_sel:BYTE_3
	v_cvt_f32_fp8_sdwa v131, v162 src0_sel:BYTE_1
	v_cvt_f32_fp8_sdwa v155, v162 src0_sel:BYTE_2
	v_pk_mul_f32 v[152:153], v[126:127], v[152:153]
	v_pk_fma_f32 v[146:147], v[126:127], v[142:143], v[146:147] op_sel:[0,0,1] op_sel_hi:[1,1,0]
	v_cvt_f32_fp8_sdwa v142, v158 src0_sel:BYTE_2
	v_cvt_f32_fp8_sdwa v143, v162 src0_sel:BYTE_3
	v_pk_fma_f32 v[148:149], v[126:127], v[148:149], v[152:153] op_sel:[0,0,1] op_sel_hi:[1,1,0]
	v_cvt_f32_fp8_sdwa v152, v156 src0_sel:BYTE_2
	v_cvt_f32_fp8_sdwa v156, v156 src0_sel:BYTE_3
	v_cvt_f32_fp8_sdwa v157, v161 src0_sel:BYTE_2
	v_cvt_f32_fp8_sdwa v153, v161 src0_sel:BYTE_3
	v_pk_mul_f32 v[138:139], v[126:127], v[138:139]
	v_pk_mul_f32 v[156:157], v[126:127], v[156:157]
	v_pk_fma_f32 v[176:177], v[126:127], v[130:131], v[138:139] op_sel:[0,0,1] op_sel_hi:[1,1,0]
	v_pk_mul_f32 v[138:139], v[126:127], v[154:155]
	v_cvt_f32_fp8_sdwa v130, v159 src0_sel:BYTE_1
	v_pk_fma_f32 v[178:179], v[126:127], v[142:143], v[138:139] op_sel:[0,0,1] op_sel_hi:[1,1,0]
	v_cvt_f32_fp8_sdwa v142, v159 src0_sel:BYTE_3
	s_waitcnt vmcnt(1)
	v_cvt_f32_fp8_sdwa v143, v163 src0_sel:BYTE_2
	v_cvt_f32_fp8_sdwa v138, v159 src0_sel:BYTE_2
	v_cvt_f32_fp8_e32 v131, v163
	v_cvt_f32_fp8_sdwa v139, v163 src0_sel:BYTE_3
	v_pk_fma_f32 v[174:175], v[126:127], v[152:153], v[156:157] op_sel:[0,0,1] op_sel_hi:[1,1,0]
	v_cvt_f32_fp8_e32 v152, v159
	v_cvt_f32_fp8_sdwa v153, v163 src0_sel:BYTE_1
	v_pk_mul_f32 v[142:143], v[126:127], v[142:143]
	v_pk_mul_f32 v[130:131], v[126:127], v[130:131]
	v_pk_fma_f32 v[180:181], v[126:127], v[138:139], v[142:143] op_sel:[0,0,1] op_sel_hi:[1,1,0]
	v_cvt_f32_fp8_sdwa v138, v160 src0_sel:BYTE_1
	s_waitcnt vmcnt(0)
	v_cvt_f32_fp8_e32 v139, v171
	v_pk_fma_f32 v[154:155], v[126:127], v[152:153], v[130:131] op_sel:[0,0,1] op_sel_hi:[1,1,0]
	v_cvt_f32_fp8_e32 v130, v160
	v_cvt_f32_fp8_sdwa v131, v171 src0_sel:BYTE_1
	v_pk_mul_f32 v[138:139], v[126:127], v[138:139]
	v_lshlrev_b32_e32 v142, 16, v124
	v_and_b32_e32 v143, 0xffff0000, v124
	v_pk_fma_f32 v[152:153], v[126:127], v[130:131], v[138:139] op_sel:[0,0,1] op_sel_hi:[1,1,0]
	v_cvt_f32_fp8_sdwa v138, v160 src0_sel:BYTE_3
	v_cvt_f32_fp8_sdwa v139, v171 src0_sel:BYTE_2
	v_cvt_f32_fp8_sdwa v130, v160 src0_sel:BYTE_2
	v_cvt_f32_fp8_sdwa v131, v171 src0_sel:BYTE_3
	v_lshlrev_b32_e32 v124, 16, v125
	v_pk_mul_f32 v[138:139], v[126:127], v[138:139]
	v_and_b32_e32 v125, 0xffff0000, v125
	v_pk_fma_f32 v[156:157], v[126:127], v[130:131], v[138:139] op_sel:[0,0,1] op_sel_hi:[1,1,0]
	v_pk_fma_f32 v[124:125], v[8:9], v[132:133], v[124:125]
	v_and_b32_e32 v171, 64, v226
	v_lshlrev_b32_e32 v182, 16, v202
	v_and_b32_e32 v183, 0xffff0000, v202
	v_lshlrev_b32_e32 v186, 16, v206
	v_and_b32_e32 v187, 0xffff0000, v206
	v_lshlrev_b32_e32 v188, 16, v207
	v_and_b32_e32 v189, 0xffff0000, v207
	v_lshlrev_b32_e32 v126, 16, v203
	v_and_b32_e32 v127, 0xffff0000, v203
	v_lshlrev_b32_e32 v184, 16, v204
	v_and_b32_e32 v185, 0xffff0000, v204
	v_lshlrev_b32_e32 v130, 16, v205
	v_and_b32_e32 v131, 0xffff0000, v205
	v_pk_fma_f32 v[126:127], v[16:17], v[140:141], v[126:127]
	v_pk_fma_f32 v[140:141], v[14:15], v[136:137], v[182:183]
	v_lshlrev_b32_e32 v192, 16, v208
	v_lshlrev_b32_e32 v196, 16, v210
	v_and_b32_e32 v197, 0xffff0000, v210
	v_lshlrev_b32_e32 v198, 16, v211
	v_and_b32_e32 v199, 0xffff0000, v211
	v_lshlrev_b32_e32 v158, 16, v214
	v_and_b32_e32 v159, 0xffff0000, v214
	v_and_b32_e32 v193, 0xffff0000, v208
	v_lshlrev_b32_e32 v194, 16, v209
	v_and_b32_e32 v195, 0xffff0000, v209
	v_pk_fma_f32 v[138:139], v[6:7], v[128:129], v[142:143]
	v_pk_fma_f32 v[158:159], v[62:63], v[152:153], v[158:159]
	v_cvt_pk_bf16_f32 v152, v138, v139
	v_cvt_pk_bf16_f32 v153, v124, v125
	global_store_dwordx2 v[150:151], v[152:153], off
	v_cvt_pk_bf16_f32 v152, v140, v141
	v_cvt_pk_bf16_f32 v153, v126, v127
	v_pk_fma_f32 v[128:129], v[24:25], v[148:149], v[130:131]
	v_pk_fma_f32 v[142:143], v[22:23], v[144:145], v[184:185]
	global_store_dwordx2 v[150:151], v[152:153], off offset:512
	v_cvt_pk_bf16_f32 v152, v142, v143
	v_cvt_pk_bf16_f32 v153, v128, v129
	v_pk_fma_f32 v[130:131], v[32:33], v[172:173], v[188:189]
	v_pk_fma_f32 v[144:145], v[30:31], v[134:135], v[186:187]
	global_store_dwordx2 v[150:151], v[152:153], off offset:1024
	v_cvt_pk_bf16_f32 v152, v144, v145
	v_cvt_pk_bf16_f32 v153, v130, v131
	v_pk_fma_f32 v[132:133], v[40:41], v[174:175], v[194:195]
	v_pk_fma_f32 v[146:147], v[38:39], v[146:147], v[192:193]
	global_store_dwordx2 v[150:151], v[152:153], off offset:1536
	v_cvt_pk_bf16_f32 v152, v146, v147
	v_cvt_pk_bf16_f32 v153, v132, v133
	v_lshlrev_b32_e32 v162, 16, v212
	v_and_b32_e32 v163, 0xffff0000, v212
	v_lshlrev_b32_e32 v200, 16, v213
	v_and_b32_e32 v201, 0xffff0000, v213
	v_lshlrev_b32_e32 v160, 16, v215
	v_and_b32_e32 v161, 0xffff0000, v215
	v_pk_fma_f32 v[134:135], v[48:49], v[178:179], v[198:199]
	v_pk_fma_f32 v[148:149], v[46:47], v[176:177], v[196:197]
	global_store_dwordx2 v[150:151], v[152:153], off offset:2048
	v_cvt_pk_bf16_f32 v152, v148, v149
	v_cvt_pk_bf16_f32 v153, v134, v135
	v_pk_fma_f32 v[136:137], v[56:57], v[180:181], v[200:201]
	v_pk_fma_f32 v[154:155], v[54:55], v[154:155], v[162:163]
	v_xor_b32_e32 v163, 1, v226
	v_xor_b32_e32 v172, 2, v226
	v_pk_fma_f32 v[156:157], v[64:65], v[156:157], v[160:161]
	v_xor_b32_e32 v173, 4, v226
	v_xor_b32_e32 v174, 8, v226
	v_add_u32_e32 v160, 64, v171
	global_store_dwordx2 v[150:151], v[152:153], off offset:2560
	v_cvt_pk_bf16_f32 v152, v154, v155
	v_cvt_pk_bf16_f32 v153, v136, v137
	v_cmp_lt_i32_e32 vcc, v163, v160
	v_cmp_lt_i32_e64 s[38:39], v172, v160
	v_cmp_lt_i32_e64 s[40:41], v173, v160
	v_cmp_lt_i32_e64 s[42:43], v174, v160
	v_mul_f32_e32 v160, v139, v139
	global_store_dwordx2 v[150:151], v[152:153], off offset:3072
	v_cvt_pk_bf16_f32 v152, v158, v159
	v_cvt_pk_bf16_f32 v153, v156, v157
	global_store_dwordx2 v[150:151], v[152:153], off offset:3584
	v_mul_f32_e32 v150, v125, v125
	v_fmac_f32_e32 v160, v138, v138
	v_fmac_f32_e32 v150, v124, v124
	v_mul_f32_e32 v151, v141, v141
	v_mul_f32_e32 v152, v127, v127
	v_mul_f32_e32 v153, v143, v143
	v_add_f32_e32 v150, v160, v150
	v_mul_f32_e32 v160, v129, v129
	v_fmac_f32_e32 v151, v140, v140
	v_fmac_f32_e32 v152, v126, v126
	v_fmac_f32_e32 v153, v142, v142
	v_fmac_f32_e32 v160, v128, v128
	v_add_f32_e32 v151, v151, v152
	v_mul_f32_e32 v152, v145, v145
	v_add_f32_e32 v153, v153, v160
	v_mul_f32_e32 v160, v131, v131
	v_fmac_f32_e32 v152, v144, v144
	v_fmac_f32_e32 v160, v130, v130
	v_add_f32_e32 v152, v152, v160
	v_mul_f32_e32 v160, v147, v147
	v_mul_f32_e32 v161, v133, v133
	v_fmac_f32_e32 v160, v146, v146
	v_fmac_f32_e32 v161, v132, v132
	v_add_f32_e32 v160, v160, v161
	v_mul_f32_e32 v161, v149, v149
	v_mul_f32_e32 v162, v135, v135
	v_fmac_f32_e32 v161, v148, v148
	v_fmac_f32_e32 v162, v134, v134
	v_add_f32_e32 v150, v150, v151
	v_add_f32_e32 v161, v161, v162
	v_mul_f32_e32 v162, v155, v155
	v_mul_f32_e32 v171, v137, v137
	v_add_f32_e32 v150, v150, v153
	v_fmac_f32_e32 v162, v154, v154
	v_fmac_f32_e32 v171, v136, v136
	v_add_f32_e32 v150, v150, v152
	v_add_f32_e32 v162, v162, v171
	v_mul_f32_e32 v171, v159, v159
	v_mul_f32_e32 v175, v157, v157
	v_add_f32_e32 v150, v150, v160
	v_fmac_f32_e32 v171, v158, v158
	v_fmac_f32_e32 v175, v156, v156
	v_add_f32_e32 v150, v150, v161
	v_add_f32_e32 v171, v171, v175
	v_add_f32_e32 v150, v150, v162
	v_cndmask_b32_e32 v151, v226, v163, vcc
	v_lshlrev_b32_e32 v151, 2, v151
	v_add_f32_e32 v150, v150, v171
	s_nop 1
	v_mov_b32_dpp v151, v150 quad_perm:[1,0,3,2] row_mask:0xf bank_mask:0xf
	v_cndmask_b32_e64 v152, v226, v172, s[38:39]
	v_lshlrev_b32_e32 v152, 2, v152
	v_cndmask_b32_e64 v153, v226, v173, s[40:41]
	v_lshlrev_b32_e32 v153, 2, v153
	s_waitcnt lgkmcnt(0)
	v_add_f32_e32 v150, v150, v151
	s_nop 1
	v_mov_b32_dpp v151, v150 quad_perm:[2,3,0,1] row_mask:0xf bank_mask:0xf
	v_cndmask_b32_e64 v163, v226, v174, s[42:43]
	v_lshlrev_b32_e32 v163, 2, v163
	v_mov_b32_e32 v160, 0
	v_mov_b32_e32 v161, 0
	s_waitcnt lgkmcnt(0)
	v_add_f32_e32 v150, v150, v151
	s_nop 1
	v_mov_b32_dpp v151, v150 row_half_mirror row_mask:0xf bank_mask:0xf
	v_mov_b32_e32 v162, 0
	v_mov_b32_e32 v173, 0
	s_waitcnt lgkmcnt(0)
	v_add_f32_e32 v150, v150, v151
	s_nop 1
	v_mov_b32_dpp v151, v150 row_mirror row_mask:0xf bank_mask:0xf
	s_waitcnt lgkmcnt(0)
	v_add_f32_e32 v150, v150, v151
	v_mov_b32_e32 v151, v150
	s_nop 1
	v_permlane16_swap_b32_e32 v150, v151
	v_add_f32_e32 v150, v150, v151
	v_mov_b32_e32 v151, v150
	s_nop 1
	v_permlane32_swap_b32_e32 v150, v151
	v_add_f32_e32 v150, v150, v151
	v_fmamk_f32 v150, v150, 0x3a000000, v228
	v_mul_f32_e32 v151, 0x4f800000, v150
	v_cmp_gt_f32_e32 vcc, s82, v150
	s_nop 1
	v_cndmask_b32_e32 v150, v150, v151, vcc
	v_sqrt_f32_e32 v151, v150
	s_nop 0
	v_add_u32_e32 v152, -1, v151
	v_add_u32_e32 v153, 1, v151
	v_fma_f32 v163, -v152, v151, v150
	v_fma_f32 v171, -v153, v151, v150
	v_cmp_ge_f32_e64 s[38:39], 0, v163
	s_nop 1
	v_cndmask_b32_e64 v151, v151, v152, s[38:39]
	v_cmp_lt_f32_e64 s[38:39], 0, v171
	v_mov_b32_e32 v171, 0
	s_nop 0
	v_cndmask_b32_e64 v151, v151, v153, s[38:39]
	v_mul_f32_e32 v152, 0x37800000, v151
	v_cndmask_b32_e32 v151, v151, v152, vcc
	v_cmp_class_f32_e32 vcc, v150, v229
	s_nop 1
	v_cndmask_b32_e32 v150, v151, v150, vcc
	v_div_scale_f32 v151, s[4:5], v150, v150, 1.0
	v_rcp_f32_e32 v153, v151
	v_div_scale_f32 v152, vcc, 1.0, v150, 1.0
	v_fma_f32 v163, -v151, v153, 1.0
	v_fmac_f32_e32 v153, v163, v153
	v_mul_f32_e32 v172, v152, v153
	v_fma_f32 v163, -v151, v172, v152
	v_fmac_f32_e32 v172, v163, v153
	v_fma_f32 v151, -v151, v172, v152
	v_div_fmas_f32 v151, v151, v153, v172
	v_div_fixup_f32 v174, v151, v150, 1.0
	v_pk_mul_f32 v[138:139], v[138:139], v[174:175] op_sel_hi:[1,0]
	v_pk_mul_f32 v[150:151], v[124:125], v[174:175] op_sel_hi:[1,0]
	v_pk_mul_f32 v[124:125], v[140:141], v[174:175] op_sel_hi:[1,0]
	v_pk_fma_f32 v[138:139], v[92:93], v[138:139], v[2:3]
	v_pk_mul_f32 v[140:141], v[126:127], v[174:175] op_sel_hi:[1,0]
	v_pk_mul_f32 v[126:127], v[142:143], v[174:175] op_sel_hi:[1,0]
	v_pk_fma_f32 v[124:125], v[96:97], v[124:125], v[10:11]
	v_med3_f32 v138, v138, s33, v233
	v_med3_f32 v139, v139, s33, v233
	v_pk_mul_f32 v[142:143], v[128:129], v[174:175] op_sel_hi:[1,0]
	v_pk_mul_f32 v[128:129], v[144:145], v[174:175] op_sel_hi:[1,0]
	v_pk_fma_f32 v[126:127], v[100:101], v[126:127], v[18:19]
	v_med3_f32 v124, v124, s33, v233
	v_med3_f32 v125, v125, s33, v233
	v_cvt_pk_fp8_f32 v160, v138, v139
	v_pk_mul_f32 v[144:145], v[130:131], v[174:175] op_sel_hi:[1,0]
	v_pk_mul_f32 v[130:131], v[146:147], v[174:175] op_sel_hi:[1,0]
	v_pk_mul_f32 v[146:147], v[132:133], v[174:175] op_sel_hi:[1,0]
	v_pk_mul_f32 v[132:133], v[148:149], v[174:175] op_sel_hi:[1,0]
	v_pk_mul_f32 v[148:149], v[134:135], v[174:175] op_sel_hi:[1,0]
	v_pk_mul_f32 v[134:135], v[154:155], v[174:175] op_sel_hi:[1,0]
	v_pk_mul_f32 v[152:153], v[136:137], v[174:175] op_sel_hi:[1,0]
	v_pk_mul_f32 v[136:137], v[158:159], v[174:175] op_sel_hi:[1,0]
	v_pk_fma_f32 v[128:129], v[104:105], v[128:129], v[26:27]
	v_med3_f32 v126, v126, s33, v233
	v_med3_f32 v127, v127, s33, v233
	v_cvt_pk_fp8_f32 v161, v124, v125
	v_mov_b32_e32 v163, 0
	v_pk_fma_f32 v[150:151], v[90:91], v[150:151], v[4:5]
	v_pk_fma_f32 v[130:131], v[108:109], v[130:131], v[34:35]
	v_pk_fma_f32 v[132:133], v[112:113], v[132:133], v[42:43]
	v_pk_fma_f32 v[134:135], v[116:117], v[134:135], v[50:51]
	v_pk_fma_f32 v[136:137], v[120:121], v[136:137], v[58:59]
	v_med3_f32 v128, v128, s33, v233
	v_med3_f32 v129, v129, s33, v233
	v_cvt_pk_fp8_f32 v162, v126, v127
	v_mov_b32_e32 v172, 0
	v_pk_mul_f32 v[154:155], v[156:157], v[174:175] op_sel_hi:[1,0]
	v_mov_b32_e32 v156, 0
	v_pk_fma_f32 v[140:141], v[94:95], v[140:141], v[12:13]
	v_med3_f32 v150, v150, s33, v233
	v_med3_f32 v151, v151, s33, v233
	v_med3_f32 v130, v130, s33, v233
	v_med3_f32 v131, v131, s33, v233
	v_med3_f32 v132, v132, s33, v233
	v_med3_f32 v133, v133, s33, v233
	v_med3_f32 v134, v134, s33, v233
	v_med3_f32 v135, v135, s33, v233
	v_med3_f32 v136, v136, s33, v233
	v_med3_f32 v137, v137, s33, v233
	v_cvt_pk_fp8_f32 v163, v128, v129
	v_pk_fma_f32 v[142:143], v[98:99], v[142:143], v[20:21]
	v_med3_f32 v140, v140, s33, v233
	v_med3_f32 v141, v141, s33, v233
	v_cvt_pk_fp8_f32 v171, v130, v131
	v_cvt_pk_fp8_f32 v172, v132, v133
	v_cvt_pk_fp8_f32 v173, v134, v135
	v_cvt_pk_fp8_f32 v156, v136, v137
	v_cvt_pk_fp8_f32 v160, v150, v151 op_sel:[0,0,1]
	v_pk_fma_f32 v[144:145], v[102:103], v[144:145], v[28:29]
	v_med3_f32 v142, v142, s33, v233
	v_med3_f32 v143, v143, s33, v233
	v_cvt_pk_fp8_f32 v161, v140, v141 op_sel:[0,0,1]
	v_pk_fma_f32 v[146:147], v[106:107], v[146:147], v[36:37]
	v_pk_fma_f32 v[148:149], v[110:111], v[148:149], v[44:45]
	v_pk_fma_f32 v[152:153], v[114:115], v[152:153], v[52:53]
	v_pk_fma_f32 v[154:155], v[118:119], v[154:155], v[60:61]
	v_med3_f32 v144, v144, s33, v233
	v_med3_f32 v145, v145, s33, v233
	v_cvt_pk_fp8_f32 v162, v142, v143 op_sel:[0,0,1]
	v_med3_f32 v146, v146, s33, v233
	v_med3_f32 v147, v147, s33, v233
	v_med3_f32 v148, v148, s33, v233
	v_med3_f32 v149, v149, s33, v233
	v_med3_f32 v152, v152, s33, v233
	v_med3_f32 v153, v153, s33, v233
	v_med3_f32 v154, v154, s33, v233
	v_med3_f32 v155, v155, s33, v233
	v_cvt_pk_fp8_f32 v163, v144, v145 op_sel:[0,0,1]
	v_cvt_pk_fp8_f32 v171, v146, v147 op_sel:[0,0,1]
	v_cvt_pk_fp8_f32 v172, v148, v149 op_sel:[0,0,1]
	v_cvt_pk_fp8_f32 v173, v152, v153 op_sel:[0,0,1]
	v_cvt_pk_fp8_f32 v156, v154, v155 op_sel:[0,0,1]
	global_store_dword v[122:123], v160, off
	global_store_dword v[122:123], v161, off offset:256
	global_store_dword v[122:123], v162, off offset:512
	global_store_dword v[122:123], v163, off offset:768
	global_store_dword v[122:123], v171, off offset:1024
	global_store_dword v[122:123], v172, off offset:1280
	global_store_dword v[122:123], v173, off offset:1536
	global_store_dword v[122:123], v156, off offset:1792
	s_cbranch_scc0 .LBB0_256
	s_branch .LBB0_253

.LBB0_274:
	v_add_co_u32_e32 v34, vcc, 0xfffff000, v108
	s_add_i32 s24, s24, s66
	s_nop 0
	v_addc_co_u32_e32 v35, vcc, -1, v109, vcc
	global_load_dwordx4 v[126:129], v[34:35], off offset:-3072 nt
	global_load_dwordx4 v[58:61], v[34:35], off offset:-2048 nt
	global_load_dwordx4 v[54:57], v[34:35], off offset:-1024 nt
	global_load_dwordx4 v[50:53], v[108:109], off offset:-4096 nt
	global_load_dwordx4 v[46:49], v[108:109], off offset:-3072 nt
	global_load_dwordx4 v[42:45], v[108:109], off offset:-2048 nt
	global_load_dwordx4 v[38:41], v[108:109], off offset:-1024 nt
	s_nop 0
	global_load_dwordx4 v[34:37], v[108:109], off nt
	v_lshl_add_u64 v[108:109], v[108:109], 0, s[28:29]
	s_cmp_ge_i32 s24, s25
	s_waitcnt vmcnt(7)
	v_mul_f32_e32 v110, v127, v127
	v_mul_f32_e32 v112, v129, v129
	v_fmac_f32_e32 v110, v126, v126
	v_fmac_f32_e32 v112, v128, v128
	v_add_f32_e32 v110, v110, v112
	s_waitcnt vmcnt(6)
	v_mul_f32_e32 v112, v59, v59
	v_mul_f32_e32 v113, v61, v61
	v_fmac_f32_e32 v112, v58, v58
	v_fmac_f32_e32 v113, v60, v60
	v_add_f32_e32 v112, v112, v113
	v_add_f32_e32 v110, v110, v112
	s_waitcnt vmcnt(5)
	v_mul_f32_e32 v112, v55, v55
	v_mul_f32_e32 v113, v57, v57
	v_fmac_f32_e32 v112, v54, v54
	v_fmac_f32_e32 v113, v56, v56
	v_add_f32_e32 v112, v112, v113
	v_add_f32_e32 v110, v110, v112
	s_waitcnt vmcnt(4)
	v_mul_f32_e32 v112, v51, v51
	v_mul_f32_e32 v113, v53, v53
	v_fmac_f32_e32 v112, v50, v50
	v_fmac_f32_e32 v113, v52, v52
	v_add_f32_e32 v112, v112, v113
	v_add_f32_e32 v110, v110, v112
	s_waitcnt vmcnt(3)
	v_mul_f32_e32 v112, v47, v47
	v_mul_f32_e32 v113, v49, v49
	v_fmac_f32_e32 v112, v46, v46
	v_fmac_f32_e32 v113, v48, v48
	v_add_f32_e32 v112, v112, v113
	v_add_f32_e32 v110, v110, v112
	s_waitcnt vmcnt(2)
	v_mul_f32_e32 v112, v43, v43
	v_mul_f32_e32 v113, v45, v45
	v_fmac_f32_e32 v112, v42, v42
	v_fmac_f32_e32 v113, v44, v44
	v_add_f32_e32 v112, v112, v113
	v_add_f32_e32 v110, v110, v112
	s_waitcnt vmcnt(1)
	v_mul_f32_e32 v112, v39, v39
	v_mul_f32_e32 v113, v41, v41
	v_fmac_f32_e32 v112, v38, v38
	v_fmac_f32_e32 v113, v40, v40
	v_add_f32_e32 v112, v112, v113
	v_add_f32_e32 v110, v110, v112
	s_waitcnt vmcnt(0)
	v_mul_f32_e32 v112, v35, v35
	v_mul_f32_e32 v113, v37, v37
	v_fmac_f32_e32 v112, v34, v34
	v_fmac_f32_e32 v113, v36, v36
	v_add_f32_e32 v112, v112, v113
	v_add_f32_e32 v110, v110, v112
	s_nop 1
	v_mov_b32_dpp v112, v110 quad_perm:[1,0,3,2] row_mask:0xf bank_mask:0xf
	s_waitcnt lgkmcnt(0)
	v_add_f32_e32 v110, v110, v112
	s_nop 1
	v_mov_b32_dpp v112, v110 quad_perm:[2,3,0,1] row_mask:0xf bank_mask:0xf
	s_waitcnt lgkmcnt(0)
	v_add_f32_e32 v110, v110, v112
	s_nop 1
	v_mov_b32_dpp v112, v110 row_half_mirror row_mask:0xf bank_mask:0xf
	s_waitcnt lgkmcnt(0)
	v_add_f32_e32 v110, v110, v112
	s_nop 1
	v_mov_b32_dpp v112, v110 row_mirror row_mask:0xf bank_mask:0xf
	s_waitcnt lgkmcnt(0)
	v_add_f32_e32 v110, v110, v112
	v_mov_b32_e32 v112, v110
	s_nop 1
	v_permlane16_swap_b32_e32 v110, v112
	v_add_f32_e32 v110, v110, v112
	v_mov_b32_e32 v112, v110
	s_nop 1
	v_permlane32_swap_b32_e32 v110, v112
	v_add_f32_e32 v110, v110, v112
	v_fmamk_f32 v110, v110, 0x3a000000, v228
	v_cmp_gt_f32_e32 vcc, s82, v110
	v_mul_f32_e32 v112, 0x4f800000, v110
	s_nop 0
	v_cndmask_b32_e32 v110, v110, v112, vcc
	v_sqrt_f32_e32 v112, v110
	s_nop 0
	v_add_u32_e32 v113, -1, v112
	v_fma_f32 v125, -v113, v112, v110
	v_cmp_ge_f32_e64 s[38:39], 0, v125
	v_add_u32_e32 v125, 1, v112
	s_nop 0
	v_cndmask_b32_e64 v113, v112, v113, s[38:39]
	v_fma_f32 v112, -v125, v112, v110
	v_cmp_lt_f32_e64 s[38:39], 0, v112
	s_nop 1
	v_cndmask_b32_e64 v112, v113, v125, s[38:39]
	v_mul_f32_e32 v113, 0x37800000, v112
	v_cndmask_b32_e32 v112, v112, v113, vcc
	v_cmp_class_f32_e32 vcc, v110, v229
	s_nop 1
	v_cndmask_b32_e32 v110, v112, v110, vcc
	v_div_scale_f32 v112, s[4:5], v110, v110, 1.0
	v_rcp_f32_e32 v113, v112
	s_nop 0
	v_fma_f32 v125, -v112, v113, 1.0
	v_fmac_f32_e32 v113, v125, v113
	v_div_scale_f32 v125, vcc, 1.0, v110, 1.0
	v_mul_f32_e32 v130, v125, v113
	v_fma_f32 v131, -v112, v130, v125
	v_fmac_f32_e32 v130, v131, v113
	v_fma_f32 v112, -v112, v130, v125
	v_div_fmas_f32 v112, v112, v113, v130
	v_div_fixup_f32 v110, v112, v110, 1.0
	v_pk_mul_f32 v[126:127], v[126:127], v[110:111] op_sel_hi:[1,0]
	v_pk_mul_f32 v[112:113], v[128:129], v[110:111] op_sel_hi:[1,0]
	v_pk_fma_f32 v[126:127], v[78:79], v[126:127], v[2:3]
	v_pk_fma_f32 v[112:113], v[76:77], v[112:113], v[4:5]
	v_med3_f32 v125, v126, s33, v233
	v_med3_f32 v126, v127, s33, v233
	v_mov_b32_e32 v127, 0
	v_cvt_pk_fp8_f32 v127, v125, v126
	v_pk_mul_f32 v[58:59], v[58:59], v[110:111] op_sel_hi:[1,0]
	v_med3_f32 v112, v112, s33, v233
	v_med3_f32 v113, v113, s33, v233
	v_pk_fma_f32 v[58:59], v[82:83], v[58:59], v[6:7]
	v_cvt_pk_fp8_f32 v127, v112, v113 op_sel:[0,0,1]
	v_med3_f32 v58, v58, s33, v233
	v_med3_f32 v59, v59, s33, v233
	v_mov_b32_e32 v112, 0
	v_cvt_pk_fp8_f32 v112, v58, v59
	v_pk_mul_f32 v[60:61], v[60:61], v[110:111] op_sel_hi:[1,0]
	v_pk_mul_f32 v[54:55], v[54:55], v[110:111] op_sel_hi:[1,0]
	v_pk_fma_f32 v[60:61], v[80:81], v[60:61], v[8:9]
	v_pk_fma_f32 v[54:55], v[86:87], v[54:55], v[10:11]
	v_med3_f32 v58, v60, s33, v233
	v_med3_f32 v59, v61, s33, v233
	v_cvt_pk_fp8_f32 v112, v58, v59 op_sel:[0,0,1]
	v_med3_f32 v54, v54, s33, v233
	v_med3_f32 v55, v55, s33, v233
	v_mov_b32_e32 v58, 0
	v_cvt_pk_fp8_f32 v58, v54, v55
	v_pk_mul_f32 v[56:57], v[56:57], v[110:111] op_sel_hi:[1,0]
	v_pk_mul_f32 v[50:51], v[50:51], v[110:111] op_sel_hi:[1,0]
	v_pk_fma_f32 v[56:57], v[84:85], v[56:57], v[12:13]
	v_pk_fma_f32 v[50:51], v[90:91], v[50:51], v[14:15]
	v_med3_f32 v54, v56, s33, v233
	v_med3_f32 v55, v57, s33, v233
	v_cvt_pk_fp8_f32 v58, v54, v55 op_sel:[0,0,1]
	v_med3_f32 v50, v50, s33, v233
	v_med3_f32 v51, v51, s33, v233
	v_mov_b32_e32 v54, 0
	v_cvt_pk_fp8_f32 v54, v50, v51
	v_pk_mul_f32 v[52:53], v[52:53], v[110:111] op_sel_hi:[1,0]
	v_pk_mul_f32 v[46:47], v[46:47], v[110:111] op_sel_hi:[1,0]
	v_pk_fma_f32 v[52:53], v[88:89], v[52:53], v[16:17]
	v_pk_fma_f32 v[46:47], v[94:95], v[46:47], v[18:19]
	v_med3_f32 v50, v52, s33, v233
	v_med3_f32 v51, v53, s33, v233
	v_cvt_pk_fp8_f32 v54, v50, v51 op_sel:[0,0,1]
	v_med3_f32 v46, v46, s33, v233
	v_med3_f32 v47, v47, s33, v233
	v_mov_b32_e32 v50, 0
	v_cvt_pk_fp8_f32 v50, v46, v47
	v_pk_mul_f32 v[48:49], v[48:49], v[110:111] op_sel_hi:[1,0]
	v_pk_mul_f32 v[42:43], v[42:43], v[110:111] op_sel_hi:[1,0]
	v_pk_fma_f32 v[48:49], v[92:93], v[48:49], v[20:21]
	v_pk_fma_f32 v[42:43], v[98:99], v[42:43], v[22:23]
	v_med3_f32 v46, v48, s33, v233
	v_med3_f32 v47, v49, s33, v233
	v_cvt_pk_fp8_f32 v50, v46, v47 op_sel:[0,0,1]
	v_med3_f32 v42, v42, s33, v233
	v_med3_f32 v43, v43, s33, v233
	v_mov_b32_e32 v46, 0
	v_cvt_pk_fp8_f32 v46, v42, v43
	v_pk_mul_f32 v[44:45], v[44:45], v[110:111] op_sel_hi:[1,0]
	v_pk_mul_f32 v[38:39], v[38:39], v[110:111] op_sel_hi:[1,0]
	v_pk_fma_f32 v[44:45], v[96:97], v[44:45], v[24:25]
	v_pk_fma_f32 v[38:39], v[102:103], v[38:39], v[26:27]
	v_med3_f32 v42, v44, s33, v233
	v_med3_f32 v43, v45, s33, v233
	v_cvt_pk_fp8_f32 v46, v42, v43 op_sel:[0,0,1]
	v_med3_f32 v38, v38, s33, v233
	v_med3_f32 v39, v39, s33, v233
	v_mov_b32_e32 v42, 0
	v_cvt_pk_fp8_f32 v42, v38, v39
	v_pk_mul_f32 v[40:41], v[40:41], v[110:111] op_sel_hi:[1,0]
	v_pk_mul_f32 v[34:35], v[34:35], v[110:111] op_sel_hi:[1,0]
	v_pk_fma_f32 v[40:41], v[100:101], v[40:41], v[28:29]
	v_pk_fma_f32 v[34:35], v[106:107], v[34:35], v[30:31]
	v_med3_f32 v38, v40, s33, v233
	v_med3_f32 v39, v41, s33, v233
	v_cvt_pk_fp8_f32 v42, v38, v39 op_sel:[0,0,1]
	v_med3_f32 v34, v34, s33, v233
	v_med3_f32 v35, v35, s33, v233
	v_mov_b32_e32 v38, 0
	v_cvt_pk_fp8_f32 v38, v34, v35
	v_pk_mul_f32 v[36:37], v[36:37], v[110:111] op_sel_hi:[1,0]
	global_store_dword v[74:75], v127, off offset:-1792
	v_pk_fma_f32 v[36:37], v[104:105], v[36:37], v[32:33]
	global_store_dword v[74:75], v112, off offset:-1536
	v_med3_f32 v34, v36, s33, v233
	v_med3_f32 v35, v37, s33, v233
	v_cvt_pk_fp8_f32 v38, v34, v35 op_sel:[0,0,1]
	global_store_dword v[74:75], v58, off offset:-1280
	global_store_dword v[74:75], v54, off offset:-1024
	global_store_dword v[74:75], v50, off offset:-768
	global_store_dword v[74:75], v46, off offset:-512
	global_store_dword v[74:75], v42, off offset:-256
	global_store_dword v[74:75], v38, off
	v_lshl_add_u64 v[74:75], v[74:75], 0, s[22:23]
	s_cbranch_scc0 .LBB0_274
	s_branch .LBB0_271

.LBB0_491:
	v_cndmask_b32_e64 v90, 0, 1, s[58:59]
	s_and_b64 vcc, exec, s[4:5]
	v_lshl_add_u64 v[62:63], s[50:51], 0, v[86:87]
	v_cmp_ne_u32_e64 s[42:43], 1, v90
	s_cbranch_vccz .LBB0_494
	v_add_co_u32_e32 v90, vcc, 0x2e200000, v62
	v_cvt_pk_bf16_f32 v124, v120, v121
	v_cvt_pk_bf16_f32 v125, v122, v123
	v_cvt_pk_bf16_f32 v126, v98, v99
	v_cvt_pk_bf16_f32 v127, v64, v65
	s_nop 1
	v_addc_co_u32_e32 v91, vcc, 0, v63, vcc
	s_and_b64 vcc, exec, s[42:43]
	global_store_dwordx4 v[90:91], v[124:127], off sc1
	s_cbranch_vccnz .LBB0_494
	v_mul_f32_e32 v121, v103, v121
	v_mul_f32_e32 v120, v104, v120
	v_mul_f32_e32 v124, v121, v121
	v_fmac_f32_e32 v124, v120, v120
	v_mul_f32_e32 v122, v110, v122
	v_fmac_f32_e32 v124, v122, v122
	v_mul_f32_e32 v123, v109, v123
	v_pk_mul_f32 v[90:91], v[72:73], v[98:99]
	v_fmac_f32_e32 v124, v123, v123
	v_pk_mul_f32 v[98:99], v[90:91], v[90:91]
	v_pk_mul_f32 v[64:65], v[78:79], v[64:65]
	v_add_f32_e32 v98, v98, v124
	v_add_f32_e32 v124, v99, v98
	v_pk_mul_f32 v[98:99], v[64:65], v[64:65]
	s_nop 0
	v_add_f32_e32 v98, v98, v124
	v_and_b32_e32 v124, 64, v226
	v_add_f32_e32 v98, v99, v98
	v_xor_b32_e32 v99, 1, v226
	v_add_u32_e32 v124, 64, v124
	v_cmp_lt_i32_e32 vcc, v99, v124
	s_nop 1
	v_cndmask_b32_e32 v99, v226, v99, vcc
	v_lshlrev_b32_e32 v99, 2, v99
	v_mov_b32_dpp v99, v98 quad_perm:[1,0,3,2] row_mask:0xf bank_mask:0xf
	s_waitcnt lgkmcnt(0)
	v_add_f32_e32 v98, v98, v99
	v_xor_b32_e32 v99, 2, v226
	v_cmp_lt_i32_e32 vcc, v99, v124
	s_nop 1
	v_cndmask_b32_e32 v99, v226, v99, vcc
	v_lshlrev_b32_e32 v99, 2, v99
	v_mov_b32_dpp v99, v98 quad_perm:[2,3,0,1] row_mask:0xf bank_mask:0xf
	s_waitcnt lgkmcnt(0)
	v_add_f32_e32 v98, v98, v99
	v_xor_b32_e32 v99, 4, v226
	v_cmp_lt_i32_e32 vcc, v99, v124
	s_nop 1
	v_cndmask_b32_e32 v99, v226, v99, vcc
	v_lshlrev_b32_e32 v99, 2, v99
	v_mov_b32_dpp v99, v98 row_half_mirror row_mask:0xf bank_mask:0xf
	s_waitcnt lgkmcnt(0)
	v_add_f32_e32 v98, v98, v99
	v_mul_f32_e32 v99, 0x4f800000, v98
	v_cmp_gt_f32_e32 vcc, s82, v98
	s_nop 1
	v_cndmask_b32_e32 v98, v98, v99, vcc
	v_sqrt_f32_e32 v99, v98
	s_nop 0
	v_add_u32_e32 v124, -1, v99
	v_fma_f32 v125, -v124, v99, v98
	v_cmp_ge_f32_e64 s[46:47], 0, v125
	v_add_u32_e32 v125, 1, v99
	s_nop 0
	v_cndmask_b32_e64 v124, v99, v124, s[46:47]
	v_fma_f32 v99, -v125, v99, v98
	v_cmp_lt_f32_e64 s[46:47], 0, v99
	s_nop 1
	v_cndmask_b32_e64 v99, v124, v125, s[46:47]
	v_mul_f32_e32 v124, 0x37800000, v99
	v_cndmask_b32_e32 v99, v99, v124, vcc
	v_cmp_class_f32_e32 vcc, v98, v229
	s_nop 1
	v_cndmask_b32_e32 v98, v99, v98, vcc
	v_max_f32_e32 v98, 0x2b8cbccc, v98
	v_div_scale_f32 v99, s[4:5], v98, v98, 1.0
	v_rcp_f32_e32 v124, v99
	s_nop 0
	v_fma_f32 v125, -v99, v124, 1.0
	v_fmac_f32_e32 v124, v125, v124
	v_div_scale_f32 v125, vcc, 1.0, v98, 1.0
	v_mul_f32_e32 v126, v125, v124
	v_fma_f32 v127, -v99, v126, v125
	v_fmac_f32_e32 v126, v127, v124
	v_fma_f32 v99, -v99, v126, v125
	v_div_fmas_f32 v99, v99, v124, v126
	v_div_fixup_f32 v98, v99, v98, 1.0
	v_mul_f32_e32 v99, v120, v98
	v_mul_f32_e32 v120, v121, v98
	v_mul_f32_e32 v121, v122, v98
	v_mul_f32_e32 v122, v123, v98
	v_mul_f32_e32 v64, v64, v98
	v_mul_f32_e32 v65, v65, v98
	v_mul_f32_e32 v90, v90, v98
	v_mul_f32_e32 v91, v91, v98
	v_cvt_pk_bf16_f32 v120, v99, v120
	v_cvt_pk_bf16_f32 v121, v121, v122
	v_cvt_pk_bf16_f32 v122, v90, v91
	v_cvt_pk_bf16_f32 v123, v64, v65
	v_lshl_add_u64 v[64:65], s[50:51], 0, v[84:85]
	v_add_co_u32_e32 v64, vcc, 0x2e201000, v64
	s_nop 1
	v_addc_co_u32_e32 v65, vcc, 0, v65, vcc
	global_store_dwordx4 v[64:65], v[120:123], off offset:2048 sc1

.LBB0_528:
	s_and_b64 vcc, exec, s[4:5]
	s_cbranch_vccz .LBB0_531
	v_add_co_u32_e32 v122, vcc, 0x2e202000, v62
	v_cvt_pk_bf16_f32 v92, v115, v114
	v_cvt_pk_bf16_f32 v93, v113, v0
	v_cvt_pk_bf16_f32 v94, v58, v59
	v_cvt_pk_bf16_f32 v95, v60, v61
	s_nop 1
	v_addc_co_u32_e32 v123, vcc, 0, v63, vcc
	s_and_b64 vcc, exec, s[42:43]
	global_store_dwordx4 v[122:123], v[92:95], off sc1
	s_cbranch_vccnz .LBB0_531
	s_nop 0
	v_mul_f32_e32 v95, v103, v114
	v_mul_f32_e32 v94, v104, v115
	v_mul_f32_e32 v114, v95, v95
	v_fmac_f32_e32 v114, v94, v94
	v_mul_f32_e32 v113, v110, v113
	v_fmac_f32_e32 v114, v113, v113
	v_mul_f32_e32 v0, v109, v0
	v_pk_mul_f32 v[58:59], v[72:73], v[58:59]
	v_fmac_f32_e32 v114, v0, v0
	v_pk_mul_f32 v[92:93], v[58:59], v[58:59]
	v_pk_mul_f32 v[60:61], v[78:79], v[60:61]
	v_add_f32_e32 v92, v92, v114
	v_add_f32_e32 v114, v93, v92
	v_pk_mul_f32 v[92:93], v[60:61], v[60:61]
	s_nop 0
	v_add_f32_e32 v92, v92, v114
	v_and_b32_e32 v114, 64, v226
	v_add_f32_e32 v92, v93, v92
	v_xor_b32_e32 v93, 1, v226
	v_add_u32_e32 v114, 64, v114
	v_cmp_lt_i32_e32 vcc, v93, v114
	s_nop 1
	v_cndmask_b32_e32 v93, v226, v93, vcc
	v_lshlrev_b32_e32 v93, 2, v93
	v_mov_b32_dpp v93, v92 quad_perm:[1,0,3,2] row_mask:0xf bank_mask:0xf
	s_waitcnt lgkmcnt(0)
	v_add_f32_e32 v92, v92, v93
	v_xor_b32_e32 v93, 2, v226
	v_cmp_lt_i32_e32 vcc, v93, v114
	s_nop 1
	v_cndmask_b32_e32 v93, v226, v93, vcc
	v_lshlrev_b32_e32 v93, 2, v93
	v_mov_b32_dpp v93, v92 quad_perm:[2,3,0,1] row_mask:0xf bank_mask:0xf
	s_waitcnt lgkmcnt(0)
	v_add_f32_e32 v92, v92, v93
	v_xor_b32_e32 v93, 4, v226
	v_cmp_lt_i32_e32 vcc, v93, v114
	s_nop 1
	v_cndmask_b32_e32 v93, v226, v93, vcc
	v_lshlrev_b32_e32 v93, 2, v93
	v_mov_b32_dpp v93, v92 row_half_mirror row_mask:0xf bank_mask:0xf
	s_waitcnt lgkmcnt(0)
	v_add_f32_e32 v92, v92, v93
	v_mul_f32_e32 v93, 0x4f800000, v92
	v_cmp_gt_f32_e32 vcc, s82, v92
	s_nop 1
	v_cndmask_b32_e32 v92, v92, v93, vcc
	v_sqrt_f32_e32 v93, v92
	s_nop 0
	v_add_u32_e32 v114, -1, v93
	v_fma_f32 v115, -v114, v93, v92
	v_cmp_ge_f32_e64 s[46:47], 0, v115
	v_add_u32_e32 v115, 1, v93
	s_nop 0
	v_cndmask_b32_e64 v114, v93, v114, s[46:47]
	v_fma_f32 v93, -v115, v93, v92
	v_cmp_lt_f32_e64 s[46:47], 0, v93
	s_nop 1
	v_cndmask_b32_e64 v93, v114, v115, s[46:47]
	v_mul_f32_e32 v114, 0x37800000, v93
	v_cndmask_b32_e32 v93, v93, v114, vcc
	v_cmp_class_f32_e32 vcc, v92, v229
	s_nop 1
	v_cndmask_b32_e32 v92, v93, v92, vcc
	v_max_f32_e32 v92, 0x2b8cbccc, v92
	v_div_scale_f32 v93, s[4:5], v92, v92, 1.0
	v_rcp_f32_e32 v114, v93
	s_nop 0
	v_fma_f32 v115, -v93, v114, 1.0
	v_fmac_f32_e32 v114, v115, v114
	v_div_scale_f32 v115, vcc, 1.0, v92, 1.0
	v_mul_f32_e32 v122, v115, v114
	v_fma_f32 v123, -v93, v122, v115
	v_fmac_f32_e32 v122, v123, v114
	v_fma_f32 v93, -v93, v122, v115
	v_div_fmas_f32 v93, v93, v114, v122
	v_div_fixup_f32 v92, v93, v92, 1.0
	v_mul_f32_e32 v93, v94, v92
	v_mul_f32_e32 v94, v95, v92
	v_mul_f32_e32 v95, v113, v92
	v_mul_f32_e32 v0, v0, v92
	v_mul_f32_e32 v113, v58, v92
	v_mul_f32_e32 v114, v59, v92
	v_mul_f32_e32 v115, v60, v92
	v_mul_f32_e32 v61, v61, v92
	v_cvt_pk_bf16_f32 v58, v93, v94
	v_lshl_add_u64 v[92:93], s[50:51], 0, v[84:85]
	v_add_co_u32_e32 v92, vcc, 0x2e203000, v92
	v_cvt_pk_bf16_f32 v59, v95, v0
	v_cvt_pk_bf16_f32 v60, v113, v114
	v_cvt_pk_bf16_f32 v61, v115, v61
	s_nop 1
	v_addc_co_u32_e32 v93, vcc, 0, v93, vcc
	global_store_dwordx4 v[92:93], v[58:61], off offset:2048 sc1

.LBB0_565:
	s_and_b64 vcc, exec, s[4:5]
	s_cbranch_vccz .LBB0_568
	v_add_co_u32_e32 v88, vcc, 0x2e204000, v62
	v_cvt_pk_bf16_f32 v116, v94, v113
	v_cvt_pk_bf16_f32 v117, v114, v115
	v_cvt_pk_bf16_f32 v118, v54, v55
	v_cvt_pk_bf16_f32 v119, v56, v57
	s_nop 1
	v_addc_co_u32_e32 v89, vcc, 0, v63, vcc
	s_and_b64 vcc, exec, s[42:43]
	global_store_dwordx4 v[88:89], v[116:119], off sc1
	s_cbranch_vccnz .LBB0_568
	v_mul_f32_e32 v96, v103, v113
	v_mul_f32_e32 v94, v104, v94
	v_mul_f32_e32 v97, v96, v96
	v_fmac_f32_e32 v97, v94, v94
	v_mul_f32_e32 v113, v110, v114
	v_fmac_f32_e32 v97, v113, v113
	v_mul_f32_e32 v114, v109, v115
	v_pk_mul_f32 v[54:55], v[72:73], v[54:55]
	v_fmac_f32_e32 v97, v114, v114
	v_pk_mul_f32 v[88:89], v[54:55], v[54:55]
	v_pk_mul_f32 v[56:57], v[78:79], v[56:57]
	v_add_f32_e32 v88, v88, v97
	v_add_f32_e32 v97, v89, v88
	v_pk_mul_f32 v[88:89], v[56:57], v[56:57]
	s_nop 0
	v_add_f32_e32 v88, v88, v97
	v_and_b32_e32 v97, 64, v226
	v_add_f32_e32 v88, v89, v88
	v_xor_b32_e32 v89, 1, v226
	v_add_u32_e32 v97, 64, v97
	v_cmp_lt_i32_e32 vcc, v89, v97
	s_nop 1
	v_cndmask_b32_e32 v89, v226, v89, vcc
	v_lshlrev_b32_e32 v89, 2, v89
	v_mov_b32_dpp v89, v88 quad_perm:[1,0,3,2] row_mask:0xf bank_mask:0xf
	s_waitcnt lgkmcnt(0)
	v_add_f32_e32 v88, v88, v89
	v_xor_b32_e32 v89, 2, v226
	v_cmp_lt_i32_e32 vcc, v89, v97
	s_nop 1
	v_cndmask_b32_e32 v89, v226, v89, vcc
	v_lshlrev_b32_e32 v89, 2, v89
	v_mov_b32_dpp v89, v88 quad_perm:[2,3,0,1] row_mask:0xf bank_mask:0xf
	s_waitcnt lgkmcnt(0)
	v_add_f32_e32 v88, v88, v89
	v_xor_b32_e32 v89, 4, v226
	v_cmp_lt_i32_e32 vcc, v89, v97
	s_nop 1
	v_cndmask_b32_e32 v89, v226, v89, vcc
	v_lshlrev_b32_e32 v89, 2, v89
	v_mov_b32_dpp v89, v88 row_half_mirror row_mask:0xf bank_mask:0xf
	s_waitcnt lgkmcnt(0)
	v_add_f32_e32 v88, v88, v89
	v_mul_f32_e32 v89, 0x4f800000, v88
	v_cmp_gt_f32_e32 vcc, s82, v88
	s_nop 1
	v_cndmask_b32_e32 v88, v88, v89, vcc
	v_sqrt_f32_e32 v89, v88
	s_nop 0
	v_add_u32_e32 v97, -1, v89
	v_fma_f32 v115, -v97, v89, v88
	v_cmp_ge_f32_e64 s[46:47], 0, v115
	v_add_u32_e32 v115, 1, v89
	s_nop 0
	v_cndmask_b32_e64 v97, v89, v97, s[46:47]
	v_fma_f32 v89, -v115, v89, v88
	v_cmp_lt_f32_e64 s[46:47], 0, v89
	s_nop 1
	v_cndmask_b32_e64 v89, v97, v115, s[46:47]
	v_mul_f32_e32 v97, 0x37800000, v89
	v_cndmask_b32_e32 v89, v89, v97, vcc
	v_cmp_class_f32_e32 vcc, v88, v229
	s_nop 1
	v_cndmask_b32_e32 v88, v89, v88, vcc
	v_max_f32_e32 v88, 0x2b8cbccc, v88
	v_div_scale_f32 v89, s[4:5], v88, v88, 1.0
	v_rcp_f32_e32 v97, v89
	s_nop 0
	v_fma_f32 v115, -v89, v97, 1.0
	v_fmac_f32_e32 v97, v115, v97
	v_div_scale_f32 v115, vcc, 1.0, v88, 1.0
	v_mul_f32_e32 v116, v115, v97
	v_fma_f32 v117, -v89, v116, v115
	v_fmac_f32_e32 v116, v117, v97
	v_fma_f32 v89, -v89, v116, v115
	v_div_fmas_f32 v89, v89, v97, v116
	v_div_fixup_f32 v88, v89, v88, 1.0
	v_mul_f32_e32 v89, v94, v88
	v_mul_f32_e32 v94, v96, v88
	v_mul_f32_e32 v96, v113, v88
	v_mul_f32_e32 v97, v114, v88
	v_mul_f32_e32 v113, v54, v88
	v_mul_f32_e32 v114, v55, v88
	v_mul_f32_e32 v115, v56, v88
	v_mul_f32_e32 v57, v57, v88
	v_cvt_pk_bf16_f32 v54, v89, v94
	v_lshl_add_u64 v[88:89], s[50:51], 0, v[84:85]
	v_add_co_u32_e32 v88, vcc, 0x2e205000, v88
	v_cvt_pk_bf16_f32 v55, v96, v97
	v_cvt_pk_bf16_f32 v56, v113, v114
	v_cvt_pk_bf16_f32 v57, v115, v57
	s_nop 1
	v_addc_co_u32_e32 v89, vcc, 0, v89, vcc
	global_store_dwordx4 v[88:89], v[54:57], off offset:2048 sc1

.LBB0_602:
	s_and_b64 vcc, exec, s[4:5]
	s_cbranch_vccz .LBB0_605
	v_add_co_u32_e32 v64, vcc, 0x2e206000, v62
	v_cvt_pk_bf16_f32 v114, v97, v113
	v_cvt_pk_bf16_f32 v115, v99, v98
	v_cvt_pk_bf16_f32 v116, v50, v51
	v_cvt_pk_bf16_f32 v117, v52, v53
	s_nop 1
	v_addc_co_u32_e32 v65, vcc, 0, v63, vcc
	s_and_b64 vcc, exec, s[42:43]
	global_store_dwordx4 v[64:65], v[114:117], off sc1
	s_cbranch_vccnz .LBB0_605
	v_mul_f32_e32 v91, v103, v113
	v_mul_f32_e32 v90, v104, v97
	v_mul_f32_e32 v97, v91, v91
	v_fmac_f32_e32 v97, v90, v90
	v_mul_f32_e32 v99, v110, v99
	v_fmac_f32_e32 v97, v99, v99
	v_mul_f32_e32 v98, v109, v98
	v_pk_mul_f32 v[50:51], v[72:73], v[50:51]
	v_fmac_f32_e32 v97, v98, v98
	v_pk_mul_f32 v[64:65], v[50:51], v[50:51]
	v_pk_mul_f32 v[52:53], v[78:79], v[52:53]
	v_add_f32_e32 v64, v64, v97
	v_add_f32_e32 v97, v65, v64
	v_pk_mul_f32 v[64:65], v[52:53], v[52:53]
	s_nop 0
	v_add_f32_e32 v64, v64, v97
	v_and_b32_e32 v97, 64, v226
	v_add_f32_e32 v64, v65, v64
	v_xor_b32_e32 v65, 1, v226
	v_add_u32_e32 v97, 64, v97
	v_cmp_lt_i32_e32 vcc, v65, v97
	s_nop 1
	v_cndmask_b32_e32 v65, v226, v65, vcc
	v_lshlrev_b32_e32 v65, 2, v65
	v_mov_b32_dpp v65, v64 quad_perm:[1,0,3,2] row_mask:0xf bank_mask:0xf
	s_waitcnt lgkmcnt(0)
	v_add_f32_e32 v64, v64, v65
	v_xor_b32_e32 v65, 2, v226
	v_cmp_lt_i32_e32 vcc, v65, v97
	s_nop 1
	v_cndmask_b32_e32 v65, v226, v65, vcc
	v_lshlrev_b32_e32 v65, 2, v65
	v_mov_b32_dpp v65, v64 quad_perm:[2,3,0,1] row_mask:0xf bank_mask:0xf
	s_waitcnt lgkmcnt(0)
	v_add_f32_e32 v64, v64, v65
	v_xor_b32_e32 v65, 4, v226
	v_cmp_lt_i32_e32 vcc, v65, v97
	s_nop 1
	v_cndmask_b32_e32 v65, v226, v65, vcc
	v_lshlrev_b32_e32 v65, 2, v65
	v_mov_b32_dpp v65, v64 row_half_mirror row_mask:0xf bank_mask:0xf
	s_waitcnt lgkmcnt(0)
	v_add_f32_e32 v64, v64, v65
	v_mul_f32_e32 v65, 0x4f800000, v64
	v_cmp_gt_f32_e32 vcc, s82, v64
	s_nop 1
	v_cndmask_b32_e32 v64, v64, v65, vcc
	v_sqrt_f32_e32 v65, v64
	s_nop 0
	v_add_u32_e32 v97, -1, v65
	v_fma_f32 v113, -v97, v65, v64
	v_cmp_ge_f32_e64 s[46:47], 0, v113
	v_add_u32_e32 v113, 1, v65
	s_nop 0
	v_cndmask_b32_e64 v97, v65, v97, s[46:47]
	v_fma_f32 v65, -v113, v65, v64
	v_cmp_lt_f32_e64 s[46:47], 0, v65
	s_nop 1
	v_cndmask_b32_e64 v65, v97, v113, s[46:47]
	v_mul_f32_e32 v97, 0x37800000, v65
	v_cndmask_b32_e32 v65, v65, v97, vcc
	v_cmp_class_f32_e32 vcc, v64, v229
	s_nop 1
	v_cndmask_b32_e32 v64, v65, v64, vcc
	v_max_f32_e32 v64, 0x2b8cbccc, v64
	v_div_scale_f32 v65, s[4:5], v64, v64, 1.0
	v_rcp_f32_e32 v97, v65
	s_nop 0
	v_fma_f32 v113, -v65, v97, 1.0
	v_fmac_f32_e32 v97, v113, v97
	v_div_scale_f32 v113, vcc, 1.0, v64, 1.0
	v_mul_f32_e32 v114, v113, v97
	v_fma_f32 v115, -v65, v114, v113
	v_fmac_f32_e32 v114, v115, v97
	v_fma_f32 v65, -v65, v114, v113
	v_div_fmas_f32 v65, v65, v97, v114
	v_div_fixup_f32 v64, v65, v64, 1.0
	v_mul_f32_e32 v65, v90, v64
	v_mul_f32_e32 v90, v91, v64
	v_mul_f32_e32 v91, v99, v64
	v_mul_f32_e32 v97, v98, v64
	v_mul_f32_e32 v98, v50, v64
	v_mul_f32_e32 v99, v51, v64
	v_mul_f32_e32 v113, v52, v64
	v_mul_f32_e32 v53, v53, v64
	v_cvt_pk_bf16_f32 v50, v65, v90
	v_lshl_add_u64 v[64:65], s[50:51], 0, v[84:85]
	v_add_co_u32_e32 v64, vcc, 0x2e207000, v64
	v_cvt_pk_bf16_f32 v51, v91, v97
	v_cvt_pk_bf16_f32 v52, v98, v99
	v_cvt_pk_bf16_f32 v53, v113, v53
	s_nop 1
	v_addc_co_u32_e32 v65, vcc, 0, v65, vcc
	global_store_dwordx4 v[64:65], v[50:53], off offset:2048 sc1

.LBB0_639:
	s_and_b64 vcc, exec, s[4:5]
	s_cbranch_vccz .LBB0_642
	v_add_co_u32_e32 v98, vcc, 0x2e208000, v62
	v_cvt_pk_bf16_f32 v58, v95, v93
	v_cvt_pk_bf16_f32 v59, v92, v0
	v_cvt_pk_bf16_f32 v60, v46, v47
	v_cvt_pk_bf16_f32 v61, v48, v49
	s_nop 1
	v_addc_co_u32_e32 v99, vcc, 0, v63, vcc
	s_and_b64 vcc, exec, s[42:43]
	global_store_dwordx4 v[98:99], v[58:61], off sc1
	s_cbranch_vccnz .LBB0_642
	s_nop 0
	v_mul_f32_e32 v61, v103, v93
	v_mul_f32_e32 v60, v104, v95
	v_mul_f32_e32 v93, v61, v61
	v_fmac_f32_e32 v93, v60, v60
	v_mul_f32_e32 v92, v110, v92
	v_fmac_f32_e32 v93, v92, v92
	v_mul_f32_e32 v0, v109, v0
	v_pk_mul_f32 v[46:47], v[72:73], v[46:47]
	v_fmac_f32_e32 v93, v0, v0
	v_pk_mul_f32 v[58:59], v[46:47], v[46:47]
	v_pk_mul_f32 v[48:49], v[78:79], v[48:49]
	v_add_f32_e32 v58, v58, v93
	v_add_f32_e32 v93, v59, v58
	v_pk_mul_f32 v[58:59], v[48:49], v[48:49]
	s_nop 0
	v_add_f32_e32 v58, v58, v93
	v_and_b32_e32 v93, 64, v226
	v_add_f32_e32 v58, v59, v58
	v_xor_b32_e32 v59, 1, v226
	v_add_u32_e32 v93, 64, v93
	v_cmp_lt_i32_e32 vcc, v59, v93
	s_nop 1
	v_cndmask_b32_e32 v59, v226, v59, vcc
	v_lshlrev_b32_e32 v59, 2, v59
	v_mov_b32_dpp v59, v58 quad_perm:[1,0,3,2] row_mask:0xf bank_mask:0xf
	s_waitcnt lgkmcnt(0)
	v_add_f32_e32 v58, v58, v59
	v_xor_b32_e32 v59, 2, v226
	v_cmp_lt_i32_e32 vcc, v59, v93
	s_nop 1
	v_cndmask_b32_e32 v59, v226, v59, vcc
	v_lshlrev_b32_e32 v59, 2, v59
	v_mov_b32_dpp v59, v58 quad_perm:[2,3,0,1] row_mask:0xf bank_mask:0xf
	s_waitcnt lgkmcnt(0)
	v_add_f32_e32 v58, v58, v59
	v_xor_b32_e32 v59, 4, v226
	v_cmp_lt_i32_e32 vcc, v59, v93
	s_nop 1
	v_cndmask_b32_e32 v59, v226, v59, vcc
	v_lshlrev_b32_e32 v59, 2, v59
	v_mov_b32_dpp v59, v58 row_half_mirror row_mask:0xf bank_mask:0xf
	s_waitcnt lgkmcnt(0)
	v_add_f32_e32 v58, v58, v59
	v_mul_f32_e32 v59, 0x4f800000, v58
	v_cmp_gt_f32_e32 vcc, s82, v58
	s_nop 1
	v_cndmask_b32_e32 v58, v58, v59, vcc
	v_sqrt_f32_e32 v59, v58
	s_nop 0
	v_add_u32_e32 v93, -1, v59
	v_fma_f32 v95, -v93, v59, v58
	v_cmp_ge_f32_e64 s[46:47], 0, v95
	v_add_u32_e32 v95, 1, v59
	s_nop 0
	v_cndmask_b32_e64 v93, v59, v93, s[46:47]
	v_fma_f32 v59, -v95, v59, v58
	v_cmp_lt_f32_e64 s[46:47], 0, v59
	s_nop 1
	v_cndmask_b32_e64 v59, v93, v95, s[46:47]
	v_mul_f32_e32 v93, 0x37800000, v59
	v_cndmask_b32_e32 v59, v59, v93, vcc
	v_cmp_class_f32_e32 vcc, v58, v229
	s_nop 1
	v_cndmask_b32_e32 v58, v59, v58, vcc
	v_max_f32_e32 v58, 0x2b8cbccc, v58
	v_div_scale_f32 v59, s[4:5], v58, v58, 1.0
	v_rcp_f32_e32 v93, v59
	s_nop 0
	v_fma_f32 v95, -v59, v93, 1.0
	v_fmac_f32_e32 v93, v95, v93
	v_div_scale_f32 v95, vcc, 1.0, v58, 1.0
	v_mul_f32_e32 v97, v95, v93
	v_fma_f32 v98, -v59, v97, v95
	v_fmac_f32_e32 v97, v98, v93
	v_fma_f32 v59, -v59, v97, v95
	v_div_fmas_f32 v59, v59, v93, v97
	v_div_fixup_f32 v58, v59, v58, 1.0
	v_mul_f32_e32 v59, v60, v58
	v_mul_f32_e32 v60, v61, v58
	v_mul_f32_e32 v61, v92, v58
	v_mul_f32_e32 v0, v0, v58
	v_mul_f32_e32 v92, v46, v58
	v_mul_f32_e32 v93, v47, v58
	v_mul_f32_e32 v95, v48, v58
	v_mul_f32_e32 v49, v49, v58
	v_cvt_pk_bf16_f32 v46, v59, v60
	v_lshl_add_u64 v[58:59], s[50:51], 0, v[84:85]
	v_add_co_u32_e32 v58, vcc, 0x2e209000, v58
	v_cvt_pk_bf16_f32 v47, v61, v0
	v_cvt_pk_bf16_f32 v48, v92, v93
	v_cvt_pk_bf16_f32 v49, v95, v49
	s_nop 1
	v_addc_co_u32_e32 v59, vcc, 0, v59, vcc
	global_store_dwordx4 v[58:59], v[46:49], off offset:2048 sc1

.LBB0_676:
	s_and_b64 vcc, exec, s[4:5]
	s_cbranch_vccz .LBB0_679
	v_add_co_u32_e32 v94, vcc, 0x2e20a000, v62
	v_cvt_pk_bf16_f32 v54, v0, v92
	v_cvt_pk_bf16_f32 v55, v89, v88
	v_cvt_pk_bf16_f32 v56, v48, v49
	v_cvt_pk_bf16_f32 v57, v44, v45
	s_nop 1
	v_addc_co_u32_e32 v95, vcc, 0, v63, vcc
	s_and_b64 vcc, exec, s[42:43]
	global_store_dwordx4 v[94:95], v[54:57], off sc1
	s_cbranch_vccnz .LBB0_679
	s_nop 0
	v_mul_f32_e32 v56, v103, v92
	v_mul_f32_e32 v0, v104, v0
	v_mul_f32_e32 v57, v56, v56
	v_fmac_f32_e32 v57, v0, v0
	v_mul_f32_e32 v89, v110, v89
	v_fmac_f32_e32 v57, v89, v89
	v_mul_f32_e32 v88, v109, v88
	v_pk_mul_f32 v[48:49], v[72:73], v[48:49]
	v_fmac_f32_e32 v57, v88, v88
	v_pk_mul_f32 v[54:55], v[48:49], v[48:49]
	v_pk_mul_f32 v[44:45], v[78:79], v[44:45]
	v_add_f32_e32 v54, v54, v57
	v_add_f32_e32 v57, v55, v54
	v_pk_mul_f32 v[54:55], v[44:45], v[44:45]
	s_nop 0
	v_add_f32_e32 v54, v54, v57
	v_and_b32_e32 v57, 64, v226
	v_add_f32_e32 v54, v55, v54
	v_xor_b32_e32 v55, 1, v226
	v_add_u32_e32 v57, 64, v57
	v_cmp_lt_i32_e32 vcc, v55, v57
	s_nop 1
	v_cndmask_b32_e32 v55, v226, v55, vcc
	v_lshlrev_b32_e32 v55, 2, v55
	v_mov_b32_dpp v55, v54 quad_perm:[1,0,3,2] row_mask:0xf bank_mask:0xf
	s_waitcnt lgkmcnt(0)
	v_add_f32_e32 v54, v54, v55
	v_xor_b32_e32 v55, 2, v226
	v_cmp_lt_i32_e32 vcc, v55, v57
	s_nop 1
	v_cndmask_b32_e32 v55, v226, v55, vcc
	v_lshlrev_b32_e32 v55, 2, v55
	v_mov_b32_dpp v55, v54 quad_perm:[2,3,0,1] row_mask:0xf bank_mask:0xf
	s_waitcnt lgkmcnt(0)
	v_add_f32_e32 v54, v54, v55
	v_xor_b32_e32 v55, 4, v226
	v_cmp_lt_i32_e32 vcc, v55, v57
	s_nop 1
	v_cndmask_b32_e32 v55, v226, v55, vcc
	v_lshlrev_b32_e32 v55, 2, v55
	v_mov_b32_dpp v55, v54 row_half_mirror row_mask:0xf bank_mask:0xf
	s_waitcnt lgkmcnt(0)
	v_add_f32_e32 v54, v54, v55
	v_mul_f32_e32 v55, 0x4f800000, v54
	v_cmp_gt_f32_e32 vcc, s82, v54
	s_nop 1
	v_cndmask_b32_e32 v54, v54, v55, vcc
	v_sqrt_f32_e32 v55, v54
	s_nop 0
	v_add_u32_e32 v57, -1, v55
	v_fma_f32 v92, -v57, v55, v54
	v_cmp_ge_f32_e64 s[46:47], 0, v92
	v_add_u32_e32 v92, 1, v55
	s_nop 0
	v_cndmask_b32_e64 v57, v55, v57, s[46:47]
	v_fma_f32 v55, -v92, v55, v54
	v_cmp_lt_f32_e64 s[46:47], 0, v55
	s_nop 1
	v_cndmask_b32_e64 v55, v57, v92, s[46:47]
	v_mul_f32_e32 v57, 0x37800000, v55
	v_cndmask_b32_e32 v55, v55, v57, vcc
	v_cmp_class_f32_e32 vcc, v54, v229
	s_nop 1
	v_cndmask_b32_e32 v54, v55, v54, vcc
	v_max_f32_e32 v54, 0x2b8cbccc, v54
	v_div_scale_f32 v55, s[4:5], v54, v54, 1.0
	v_rcp_f32_e32 v57, v55
	s_nop 0
	v_fma_f32 v92, -v55, v57, 1.0
	v_fmac_f32_e32 v57, v92, v57
	v_div_scale_f32 v92, vcc, 1.0, v54, 1.0
	v_mul_f32_e32 v93, v92, v57
	v_fma_f32 v94, -v55, v93, v92
	v_fmac_f32_e32 v93, v94, v57
	v_fma_f32 v55, -v55, v93, v92
	v_div_fmas_f32 v55, v55, v57, v93
	v_div_fixup_f32 v54, v55, v54, 1.0
	v_mul_f32_e32 v55, v56, v54
	v_mul_f32_e32 v56, v89, v54
	v_mul_f32_e32 v57, v88, v54
	v_mul_f32_e32 v44, v44, v54
	v_mul_f32_e32 v45, v45, v54
	v_mul_f32_e32 v0, v0, v54
	v_mul_f32_e32 v48, v48, v54
	v_mul_f32_e32 v49, v49, v54
	v_cvt_pk_bf16_f32 v54, v0, v55
	v_cvt_pk_bf16_f32 v55, v56, v57
	v_cvt_pk_bf16_f32 v56, v48, v49
	v_cvt_pk_bf16_f32 v57, v44, v45
	v_lshl_add_u64 v[44:45], s[50:51], 0, v[84:85]
	v_add_co_u32_e32 v44, vcc, 0x2e20b000, v44
	s_nop 1
	v_addc_co_u32_e32 v45, vcc, 0, v45, vcc
	global_store_dwordx4 v[44:45], v[54:57], off offset:2048 sc1

.LBB0_713:
	s_and_b64 vcc, exec, s[4:5]
	s_cbranch_vccz .LBB0_716
	v_add_co_u32_e32 v54, vcc, 0x2e20c000, v62
	v_cvt_pk_bf16_f32 v50, v0, v44
	v_cvt_pk_bf16_f32 v51, v45, v48
	v_cvt_pk_bf16_f32 v52, v38, v39
	v_cvt_pk_bf16_f32 v53, v40, v41
	s_nop 1
	v_addc_co_u32_e32 v55, vcc, 0, v63, vcc
	s_and_b64 vcc, exec, s[42:43]
	global_store_dwordx4 v[54:55], v[50:53], off sc1
	s_cbranch_vccnz .LBB0_716
	v_mul_f32_e32 v49, v103, v44
	v_mul_f32_e32 v0, v104, v0
	v_mul_f32_e32 v50, v49, v49
	v_fmac_f32_e32 v50, v0, v0
	v_mul_f32_e32 v51, v110, v45
	v_fmac_f32_e32 v50, v51, v51
	v_mul_f32_e32 v48, v109, v48
	v_pk_mul_f32 v[38:39], v[72:73], v[38:39]
	v_fmac_f32_e32 v50, v48, v48
	v_pk_mul_f32 v[44:45], v[38:39], v[38:39]
	v_pk_mul_f32 v[40:41], v[78:79], v[40:41]
	v_add_f32_e32 v44, v44, v50
	v_add_f32_e32 v50, v45, v44
	v_pk_mul_f32 v[44:45], v[40:41], v[40:41]
	s_nop 0
	v_add_f32_e32 v44, v44, v50
	v_and_b32_e32 v50, 64, v226
	v_add_f32_e32 v44, v45, v44
	v_xor_b32_e32 v45, 1, v226
	v_add_u32_e32 v50, 64, v50
	v_cmp_lt_i32_e32 vcc, v45, v50
	s_nop 1
	v_cndmask_b32_e32 v45, v226, v45, vcc
	v_lshlrev_b32_e32 v45, 2, v45
	v_mov_b32_dpp v45, v44 quad_perm:[1,0,3,2] row_mask:0xf bank_mask:0xf
	s_waitcnt lgkmcnt(0)
	v_add_f32_e32 v44, v44, v45
	v_xor_b32_e32 v45, 2, v226
	v_cmp_lt_i32_e32 vcc, v45, v50
	s_nop 1
	v_cndmask_b32_e32 v45, v226, v45, vcc
	v_lshlrev_b32_e32 v45, 2, v45
	v_mov_b32_dpp v45, v44 quad_perm:[2,3,0,1] row_mask:0xf bank_mask:0xf
	s_waitcnt lgkmcnt(0)
	v_add_f32_e32 v44, v44, v45
	v_xor_b32_e32 v45, 4, v226
	v_cmp_lt_i32_e32 vcc, v45, v50
	s_nop 1
	v_cndmask_b32_e32 v45, v226, v45, vcc
	v_lshlrev_b32_e32 v45, 2, v45
	v_mov_b32_dpp v45, v44 row_half_mirror row_mask:0xf bank_mask:0xf
	s_waitcnt lgkmcnt(0)
	v_add_f32_e32 v44, v44, v45
	v_mul_f32_e32 v45, 0x4f800000, v44
	v_cmp_gt_f32_e32 vcc, s82, v44
	s_nop 1
	v_cndmask_b32_e32 v44, v44, v45, vcc
	v_sqrt_f32_e32 v45, v44
	s_nop 0
	v_add_u32_e32 v50, -1, v45
	v_fma_f32 v52, -v50, v45, v44
	v_cmp_ge_f32_e64 s[46:47], 0, v52
	v_add_u32_e32 v52, 1, v45
	s_nop 0
	v_cndmask_b32_e64 v50, v45, v50, s[46:47]
	v_fma_f32 v45, -v52, v45, v44
	v_cmp_lt_f32_e64 s[46:47], 0, v45
	s_nop 1
	v_cndmask_b32_e64 v45, v50, v52, s[46:47]
	v_mul_f32_e32 v50, 0x37800000, v45
	v_cndmask_b32_e32 v45, v45, v50, vcc
	v_cmp_class_f32_e32 vcc, v44, v229
	s_nop 1
	v_cndmask_b32_e32 v44, v45, v44, vcc
	v_max_f32_e32 v44, 0x2b8cbccc, v44
	v_div_scale_f32 v45, s[4:5], v44, v44, 1.0
	v_rcp_f32_e32 v50, v45
	s_nop 0
	v_fma_f32 v52, -v45, v50, 1.0
	v_fmac_f32_e32 v50, v52, v50
	v_div_scale_f32 v52, vcc, 1.0, v44, 1.0
	v_mul_f32_e32 v53, v52, v50
	v_fma_f32 v54, -v45, v53, v52
	v_fmac_f32_e32 v53, v54, v50
	v_fma_f32 v45, -v45, v53, v52
	v_div_fmas_f32 v45, v45, v50, v53
	v_div_fixup_f32 v44, v45, v44, 1.0
	v_mul_f32_e32 v45, v49, v44
	v_mul_f32_e32 v0, v0, v44
	v_mul_f32_e32 v49, v51, v44
	v_mul_f32_e32 v48, v48, v44
	v_mul_f32_e32 v50, v38, v44
	v_mul_f32_e32 v51, v39, v44
	v_mul_f32_e32 v52, v40, v44
	v_mul_f32_e32 v41, v41, v44
	v_cvt_pk_bf16_f32 v38, v0, v45
	v_lshl_add_u64 v[44:45], s[50:51], 0, v[84:85]
	v_add_co_u32_e32 v44, vcc, 0x2e20d000, v44
	v_cvt_pk_bf16_f32 v39, v49, v48
	v_cvt_pk_bf16_f32 v40, v50, v51
	v_cvt_pk_bf16_f32 v41, v52, v41
	s_nop 1
	v_addc_co_u32_e32 v45, vcc, 0, v45, vcc
	global_store_dwordx4 v[44:45], v[38:41], off offset:2048 sc1

.LBB0_750:
	s_and_b64 vcc, exec, s[4:5]
	s_cbranch_vccz .LBB0_454
	v_add_co_u32_e32 v46, vcc, 0x2e20e000, v62
	v_cvt_pk_bf16_f32 v42, v38, v39
	v_cvt_pk_bf16_f32 v43, v40, v41
	v_cvt_pk_bf16_f32 v44, v34, v35
	v_cvt_pk_bf16_f32 v45, v36, v37
	s_nop 1
	v_addc_co_u32_e32 v47, vcc, 0, v63, vcc
	s_and_b64 vcc, exec, s[42:43]
	global_store_dwordx4 v[46:47], v[42:45], off sc1
	s_cbranch_vccnz .LBB0_454
	s_nop 0
	v_mul_f32_e32 v43, v103, v39
	v_mul_f32_e32 v42, v104, v38
	v_mul_f32_e32 v44, v43, v43
	v_fmac_f32_e32 v44, v42, v42
	v_mul_f32_e32 v40, v110, v40
	v_fmac_f32_e32 v44, v40, v40
	v_mul_f32_e32 v41, v109, v41
	v_pk_mul_f32 v[34:35], v[72:73], v[34:35]
	v_fmac_f32_e32 v44, v41, v41
	v_pk_mul_f32 v[38:39], v[34:35], v[34:35]
	v_pk_mul_f32 v[36:37], v[78:79], v[36:37]
	v_add_f32_e32 v38, v38, v44
	v_add_f32_e32 v44, v39, v38
	v_pk_mul_f32 v[38:39], v[36:37], v[36:37]
	s_nop 0
	v_add_f32_e32 v38, v38, v44
	v_and_b32_e32 v44, 64, v226
	v_add_f32_e32 v38, v39, v38
	v_xor_b32_e32 v39, 1, v226
	v_add_u32_e32 v44, 64, v44
	v_cmp_lt_i32_e32 vcc, v39, v44
	s_nop 1
	v_cndmask_b32_e32 v39, v226, v39, vcc
	v_lshlrev_b32_e32 v39, 2, v39
	v_mov_b32_dpp v39, v38 quad_perm:[1,0,3,2] row_mask:0xf bank_mask:0xf
	s_waitcnt lgkmcnt(0)
	v_add_f32_e32 v38, v38, v39
	v_xor_b32_e32 v39, 2, v226
	v_cmp_lt_i32_e32 vcc, v39, v44
	s_nop 1
	v_cndmask_b32_e32 v39, v226, v39, vcc
	v_lshlrev_b32_e32 v39, 2, v39
	v_mov_b32_dpp v39, v38 quad_perm:[2,3,0,1] row_mask:0xf bank_mask:0xf
	s_waitcnt lgkmcnt(0)
	v_add_f32_e32 v38, v38, v39
	v_xor_b32_e32 v39, 4, v226
	v_cmp_lt_i32_e32 vcc, v39, v44
	s_nop 1
	v_cndmask_b32_e32 v39, v226, v39, vcc
	v_lshlrev_b32_e32 v39, 2, v39
	v_mov_b32_dpp v39, v38 row_half_mirror row_mask:0xf bank_mask:0xf
	s_waitcnt lgkmcnt(0)
	v_add_f32_e32 v38, v38, v39
	v_mul_f32_e32 v39, 0x4f800000, v38
	v_cmp_gt_f32_e32 vcc, s82, v38
	s_nop 1
	v_cndmask_b32_e32 v38, v38, v39, vcc
	v_sqrt_f32_e32 v39, v38
	s_nop 0
	v_add_u32_e32 v44, -1, v39
	v_fma_f32 v45, -v44, v39, v38
	v_cmp_ge_f32_e64 s[42:43], 0, v45
	v_add_u32_e32 v45, 1, v39
	s_nop 0
	v_cndmask_b32_e64 v44, v39, v44, s[42:43]
	v_fma_f32 v39, -v45, v39, v38
	v_cmp_lt_f32_e64 s[42:43], 0, v39
	s_nop 1
	v_cndmask_b32_e64 v39, v44, v45, s[42:43]
	v_mul_f32_e32 v44, 0x37800000, v39
	v_cndmask_b32_e32 v39, v39, v44, vcc
	v_cmp_class_f32_e32 vcc, v38, v229
	s_nop 1
	v_cndmask_b32_e32 v38, v39, v38, vcc
	v_max_f32_e32 v38, 0x2b8cbccc, v38
	v_div_scale_f32 v39, s[4:5], v38, v38, 1.0
	v_rcp_f32_e32 v44, v39
	s_nop 0
	v_fma_f32 v45, -v39, v44, 1.0
	v_fmac_f32_e32 v44, v45, v44
	v_div_scale_f32 v45, vcc, 1.0, v38, 1.0
	v_mul_f32_e32 v46, v45, v44
	v_fma_f32 v47, -v39, v46, v45
	v_fmac_f32_e32 v46, v47, v44
	v_fma_f32 v39, -v39, v46, v45
	v_div_fmas_f32 v39, v39, v44, v46
	v_div_fixup_f32 v38, v39, v38, 1.0
	v_mul_f32_e32 v39, v42, v38
	v_mul_f32_e32 v42, v43, v38
	v_mul_f32_e32 v40, v40, v38
	v_mul_f32_e32 v41, v41, v38
	v_mul_f32_e32 v43, v34, v38
	v_mul_f32_e32 v44, v35, v38
	v_mul_f32_e32 v45, v36, v38
	v_mul_f32_e32 v37, v37, v38
	v_cvt_pk_bf16_f32 v34, v39, v42
	v_lshl_add_u64 v[38:39], s[50:51], 0, v[84:85]
	v_add_co_u32_e32 v38, vcc, 0x2e20f000, v38
	v_cvt_pk_bf16_f32 v35, v40, v41
	v_cvt_pk_bf16_f32 v36, v43, v44
	v_cvt_pk_bf16_f32 v37, v45, v37
	s_nop 1
	v_addc_co_u32_e32 v39, vcc, 0, v39, vcc
	global_store_dwordx4 v[38:39], v[34:37], off offset:2048 sc1
	s_branch .LBB0_454

.LBB0_1141:
	s_waitcnt lgkmcnt(0)
	v_lshl_add_u64 v[50:51], s[40:41], 0, v[80:81]
	s_mov_b64 s[4:5], 0x40e00000
	v_lshl_add_u64 v[46:47], v[50:51], 0, s[4:5]
	v_add_co_u32_e32 v48, vcc, 0x40e00000, v50
	s_mov_b64 s[4:5], 0x42e00000
	s_nop 0
	v_addc_co_u32_e32 v49, vcc, 0, v51, vcc
	v_lshl_add_u64 v[52:53], v[50:51], 0, s[4:5]
	s_mov_b32 s4, 0x42e00000
	v_add_co_u32_e32 v50, vcc, s4, v50
	global_load_dwordx4 v[54:57], v[48:49], off nt
	s_nop 0
	global_load_dwordx4 v[46:49], v[46:47], off offset:16 nt
	v_addc_co_u32_e32 v51, vcc, 0, v51, vcc
	global_load_dwordx4 v[58:61], v[50:51], off nt
	s_nop 0
	global_load_dwordx4 v[50:53], v[52:53], off offset:16 nt
	v_lshl_add_u64 v[108:109], s[40:41], 0, v[76:77]
	s_mov_b64 s[4:5], 0x2e200000
	v_lshl_add_u64 v[156:157], s[40:41], 0, v[74:75]
	s_add_i32 s48, s48, s66
	v_lshl_add_u64 v[74:75], v[74:75], 0, s[6:7]
	v_lshl_add_u64 v[76:77], v[76:77], 0, s[10:11]
	v_lshl_add_u64 v[80:81], v[80:81], 0, s[22:23]
	s_cmpk_lt_i32 s48, 0x4000
	s_waitcnt vmcnt(3)
	v_lshlrev_b32_e32 v2, 16, v54
	v_and_b32_e32 v82, 0xffff0000, v54
	v_lshlrev_b32_e32 v86, 16, v55
	v_and_b32_e32 v127, 0xffff0000, v55
	v_lshl_add_u64 v[54:55], v[108:109], 0, s[4:5]
	s_mov_b32 s4, 0x2e200000
	s_waitcnt vmcnt(1)
	v_lshlrev_b32_e32 v4, 16, v58
	v_and_b32_e32 v72, 0xffff0000, v58
	v_add_co_u32_e32 v58, vcc, s4, v108
	v_lshlrev_b32_e32 v123, 16, v59
	v_and_b32_e32 v125, 0xffff0000, v59
	v_addc_co_u32_e32 v59, vcc, 0, v109, vcc
	s_mov_b32 s4, 0x2e201000
	v_add_co_u32_e32 v110, vcc, s4, v108
	s_mov_b64 s[4:5], 0x2e200800
	v_lshlrev_b32_e32 v131, 16, v60
	v_and_b32_e32 v133, 0xffff0000, v60
	v_lshlrev_b32_e32 v137, 16, v61
	v_and_b32_e32 v136, 0xffff0000, v61
	v_addc_co_u32_e32 v111, vcc, 0, v109, vcc
	v_lshl_add_u64 v[60:61], v[108:109], 0, s[4:5]
	s_mov_b64 s[4:5], 0x2e201000
	v_lshlrev_b32_e32 v135, 16, v57
	v_lshlrev_b32_e32 v129, 16, v56
	v_and_b32_e32 v134, 0xffff0000, v56
	v_and_b32_e32 v164, 0xffff0000, v57
	global_load_dwordx4 v[62:65], v[110:111], off offset:-4096 nt
	s_nop 0
	global_load_dwordx4 v[54:57], v[54:55], off offset:16 nt
	s_nop 0
	global_load_dwordx4 v[66:69], v[58:59], off offset:2048 nt
	s_nop 0
	global_load_dwordx4 v[58:61], v[60:61], off offset:16 nt
	v_lshl_add_u64 v[112:113], v[108:109], 0, s[4:5]
	global_load_dwordx4 v[108:111], v[110:111], off nt
	s_nop 0
	global_load_dwordx4 v[140:143], v[112:113], off offset:16 nt
	s_mov_b64 s[4:5], 0x36e01000
	v_lshl_add_u64 v[144:145], v[156:157], 0, s[4:5]
	s_mov_b32 s4, 0x36e01000
	v_add_co_u32_e32 v148, vcc, s4, v156
	s_mov_b32 s4, 0x36e02000
	s_nop 0
	v_addc_co_u32_e32 v149, vcc, 0, v157, vcc
	v_add_co_u32_e32 v158, vcc, s4, v156
	s_mov_b64 s[4:5], 0x36e01800
	s_nop 0
	v_addc_co_u32_e32 v159, vcc, 0, v157, vcc
	v_lshl_add_u64 v[152:153], v[156:157], 0, s[4:5]
	s_mov_b64 s[4:5], 0x36e02000
	v_lshl_add_u64 v[160:161], v[156:157], 0, s[4:5]
	v_add_f32_e32 v82, v72, v82
	v_add_f32_e32 v4, v4, v2
	v_add_f32_e32 v2, 0, v4
	v_add_f32_e32 v2, v82, v2
	v_add_f32_e32 v86, v123, v86
	v_add_f32_e32 v2, v86, v2
	v_add_f32_e32 v123, v125, v127
	v_add_f32_e32 v2, v123, v2
	v_add_f32_e32 v125, v131, v129
	v_add_f32_e32 v2, v125, v2
	s_waitcnt vmcnt(5)
	v_lshlrev_b32_e32 v165, 16, v62
	v_and_b32_e32 v166, 0xffff0000, v62
	s_waitcnt vmcnt(3)
	v_lshlrev_b32_e32 v169, 16, v66
	v_and_b32_e32 v170, 0xffff0000, v66
	s_waitcnt vmcnt(1)
	v_lshlrev_b32_e32 v132, 16, v108
	v_and_b32_e32 v130, 0xffff0000, v108
	v_lshlrev_b32_e32 v124, 16, v110
	v_and_b32_e32 v122, 0xffff0000, v110
	s_waitcnt vmcnt(0)
	v_lshlrev_b32_e32 v118, 16, v140
	v_and_b32_e32 v116, 0xffff0000, v140
	v_lshlrev_b32_e32 v114, 16, v141
	v_and_b32_e32 v112, 0xffff0000, v141
	v_lshlrev_b32_e32 v110, 16, v142
	v_and_b32_e32 v108, 0xffff0000, v142
	v_lshlrev_b32_e32 v66, 16, v143
	v_and_b32_e32 v62, 0xffff0000, v143
	global_load_dwordx4 v[140:143], v[158:159], off offset:-4096 nt
	s_nop 0
	global_load_dwordx4 v[144:147], v[144:145], off offset:16 nt
	s_nop 0
	global_load_dwordx4 v[148:151], v[148:149], off offset:2048 nt
	s_nop 0
	global_load_dwordx4 v[152:155], v[152:153], off offset:16 nt
	s_nop 0
	global_load_dwordx4 v[156:159], v[158:159], off nt
	s_nop 0
	global_load_dwordx4 v[160:163], v[160:161], off offset:16 nt
	v_lshlrev_b32_e32 v128, 16, v109
	v_and_b32_e32 v126, 0xffff0000, v109
	v_lshlrev_b32_e32 v84, 16, v111
	v_and_b32_e32 v120, 0xffff0000, v111
	v_lshlrev_b32_e32 v171, 16, v67
	v_lshlrev_b32_e32 v167, 16, v63
	v_and_b32_e32 v168, 0xffff0000, v57
	v_and_b32_e32 v172, 0xffff0000, v61
	s_waitcnt vmcnt(5)
	v_lshlrev_b32_e32 v173, 16, v140
	s_waitcnt vmcnt(3)
	v_lshlrev_b32_e32 v175, 16, v148
	v_and_b32_e32 v140, 0xffff0000, v140
	v_and_b32_e32 v148, 0xffff0000, v148
	s_waitcnt vmcnt(1)
	v_lshlrev_b32_e32 v179, 16, v156
	v_and_b32_e32 v180, 0xffff0000, v156
	v_add_f32_e32 v156, v173, v175
	v_add_f32_e32 v156, -2.0, v156
	v_add_f32_e32 v72, v140, v148
	v_fma_f32 v156, v14, v156, 2.0
	v_add_f32_e32 v72, -2.0, v72
	v_mul_f32_e32 v156, v156, v169
	v_fma_f32 v72, v15, v72, 2.0
	v_lshlrev_b32_e32 v174, 16, v141
	s_waitcnt vmcnt(0)
	v_lshlrev_b32_e32 v115, 16, v160
	v_and_b32_e32 v113, 0xffff0000, v160
	v_lshlrev_b32_e32 v111, 16, v161
	v_and_b32_e32 v109, 0xffff0000, v161
	v_mul_f32_e32 v156, v156, v165
	v_mul_f32_e32 v72, v72, v170
	v_lshlrev_b32_e32 v161, 16, v142
	v_and_b32_e32 v160, 0xffff0000, v141
	v_lshlrev_b32_e32 v141, 16, v150
	v_and_b32_e32 v140, 0xffff0000, v149
	v_lshlrev_b32_e32 v176, 16, v149
	v_lshlrev_b32_e32 v20, 16, v162
	v_and_b32_e32 v17, 0xffff0000, v162
	v_fma_f32 v162, v6, v156, 0
	v_mul_f32_e32 v72, v72, v166
	v_pk_add_f32 v[140:141], v[160:161], v[140:141]
	v_fmac_f32_e32 v162, v7, v72
	v_add_f32_e32 v72, v174, v176
	v_pk_add_f32 v[140:141], v[140:141], -2.0 op_sel_hi:[1,0]
	v_lshlrev_b32_e32 v70, 16, v158
	v_and_b32_e32 v121, 0xffff0000, v158
	v_lshlrev_b32_e32 v119, 16, v159
	v_and_b32_e32 v117, 0xffff0000, v159
	v_add_f32_e32 v72, -2.0, v72
	v_lshlrev_b32_e32 v159, 16, v68
	v_and_b32_e32 v158, 0xffff0000, v67
	v_pk_fma_f32 v[140:141], v[98:99], v[140:141], 2.0 op_sel_hi:[1,1,0]
	v_lshlrev_b32_e32 v181, 16, v157
	v_and_b32_e32 v182, 0xffff0000, v157
	v_fma_f32 v72, v16, v72, 2.0
	v_lshlrev_b32_e32 v157, 16, v64
	v_and_b32_e32 v156, 0xffff0000, v63
	v_pk_mul_f32 v[140:141], v[140:141], v[158:159]
	v_mul_f32_e32 v72, v72, v171
	v_pk_mul_f32 v[140:141], v[140:141], v[156:157]
	v_lshlrev_b32_e32 v157, 16, v143
	v_and_b32_e32 v156, 0xffff0000, v142
	v_lshlrev_b32_e32 v159, 16, v151
	v_and_b32_e32 v158, 0xffff0000, v150
	v_mul_f32_e32 v72, v72, v167
	v_pk_add_f32 v[156:157], v[156:157], v[158:159]
	v_fmac_f32_e32 v162, v8, v72
	v_pk_mul_f32 v[140:141], v[88:89], v[140:141]
	v_pk_add_f32 v[156:157], v[156:157], -2.0 op_sel_hi:[1,0]
	v_add_f32_e32 v63, v140, v162
	v_lshlrev_b32_e32 v149, 16, v69
	v_and_b32_e32 v148, 0xffff0000, v68
	v_pk_fma_f32 v[156:157], v[100:101], v[156:157], 2.0 op_sel_hi:[1,1,0]
	v_add_f32_e32 v63, v141, v63
	v_lshlrev_b32_e32 v141, 16, v65
	v_and_b32_e32 v140, 0xffff0000, v64
	v_pk_mul_f32 v[148:149], v[156:157], v[148:149]
	v_and_b32_e32 v64, 0xffff0000, v69
	v_lshlrev_b32_e32 v69, 16, v144
	v_and_b32_e32 v68, 0xffff0000, v143
	v_lshlrev_b32_e32 v143, 16, v152
	v_and_b32_e32 v142, 0xffff0000, v151
	v_pk_mul_f32 v[140:141], v[148:149], v[140:141]
	v_pk_add_f32 v[68:69], v[68:69], v[142:143]
	v_pk_mul_f32 v[140:141], v[90:91], v[140:141]
	v_pk_add_f32 v[68:69], v[68:69], -2.0 op_sel_hi:[1,0]
	v_add_f32_e32 v63, v140, v63
	v_and_b32_e32 v140, 0xffff0000, v65
	v_lshlrev_b32_e32 v65, 16, v58
	v_pk_fma_f32 v[68:69], v[102:103], v[68:69], 2.0 op_sel_hi:[1,1,0]
	v_add_f32_e32 v63, v141, v63
	v_lshlrev_b32_e32 v141, 16, v54
	v_pk_mul_f32 v[64:65], v[68:69], v[64:65]
	v_lshlrev_b32_e32 v143, 16, v145
	v_pk_mul_f32 v[64:65], v[64:65], v[140:141]
	v_and_b32_e32 v142, 0xffff0000, v144
	v_lshlrev_b32_e32 v149, 16, v153
	v_and_b32_e32 v148, 0xffff0000, v152
	v_pk_mul_f32 v[64:65], v[92:93], v[64:65]
	v_pk_add_f32 v[142:143], v[142:143], v[148:149]
	v_add_f32_e32 v63, v64, v63
	v_pk_add_f32 v[142:143], v[142:143], -2.0 op_sel_hi:[1,0]
	v_add_f32_e32 v63, v65, v63
	v_and_b32_e32 v64, 0xffff0000, v46
	v_lshlrev_b32_e32 v65, 16, v46
	v_and_b32_e32 v68, 0xffff0000, v50
	v_lshlrev_b32_e32 v69, 16, v50
	v_lshlrev_b32_e32 v141, 16, v59
	v_and_b32_e32 v140, 0xffff0000, v58
	v_pk_fma_f32 v[142:143], v[104:105], v[142:143], 2.0 op_sel_hi:[1,1,0]
	v_pk_add_f32 v[64:65], v[64:65], v[68:69]
	v_lshlrev_b32_e32 v69, 16, v55
	v_and_b32_e32 v68, 0xffff0000, v54
	v_pk_mul_f32 v[140:141], v[142:143], v[140:141]
	v_and_b32_e32 v54, 0xffff0000, v59
	v_pk_mul_f32 v[68:69], v[140:141], v[68:69]
	v_lshlrev_b32_e32 v59, 16, v146
	v_pk_mul_f32 v[68:69], v[94:95], v[68:69]
	v_and_b32_e32 v58, 0xffff0000, v145
	v_add_f32_e32 v46, v68, v63
	v_add_f32_e32 v63, v69, v46
	v_lshlrev_b32_e32 v69, 16, v154
	v_and_b32_e32 v68, 0xffff0000, v153
	v_pk_add_f32 v[58:59], v[58:59], v[68:69]
	v_and_b32_e32 v46, 0xffff0000, v47
	v_lshlrev_b32_e32 v47, 16, v47
	v_and_b32_e32 v50, 0xffff0000, v51
	v_lshlrev_b32_e32 v51, 16, v51
	v_pk_add_f32 v[58:59], v[58:59], -2.0 op_sel_hi:[1,0]
	v_pk_add_f32 v[50:51], v[46:47], v[50:51]
	v_and_b32_e32 v46, 0xffff0000, v55
	v_lshlrev_b32_e32 v55, 16, v60
	v_pk_fma_f32 v[58:59], v[106:107], v[58:59], 2.0 op_sel_hi:[1,1,0]
	v_lshlrev_b32_e32 v47, 16, v56
	v_pk_mul_f32 v[54:55], v[58:59], v[54:55]
	v_and_b32_e32 v177, 0xffff0000, v155
	v_pk_mul_f32 v[46:47], v[54:55], v[46:47]
	v_and_b32_e32 v54, 0xffff0000, v52
	v_pk_mul_f32 v[46:47], v[96:97], v[46:47]
	v_lshlrev_b32_e32 v55, 16, v52
	v_add_f32_e32 v46, v46, v63
	v_add_f32_e32 v63, v47, v46
	v_and_b32_e32 v46, 0xffff0000, v48
	v_lshlrev_b32_e32 v47, 16, v48
	v_pk_add_f32 v[58:59], v[46:47], v[54:55]
	v_lshlrev_b32_e32 v47, 16, v57
	v_and_b32_e32 v46, 0xffff0000, v56
	v_lshlrev_b32_e32 v55, 16, v61
	v_and_b32_e32 v54, 0xffff0000, v60
	v_lshlrev_b32_e32 v57, 16, v147
	v_and_b32_e32 v56, 0xffff0000, v146
	v_lshlrev_b32_e32 v61, 16, v155
	v_and_b32_e32 v60, 0xffff0000, v154
	v_pk_add_f32 v[56:57], v[56:57], v[60:61]
	v_and_b32_e32 v178, 0xffff0000, v147
	v_pk_add_f32 v[56:57], v[56:57], -2.0 op_sel_hi:[1,0]
	v_add_f32_e32 v150, v136, v164
	v_pk_fma_f32 v[56:57], v[18:19], v[56:57], 2.0 op_sel_hi:[1,1,0]
	v_and_b32_e32 v48, 0xffff0000, v53
	v_pk_mul_f32 v[54:55], v[56:57], v[54:55]
	v_add_f32_e32 v67, v133, v134
	v_pk_mul_f32 v[46:47], v[54:55], v[46:47]
	v_add_f32_e32 v2, v67, v2
	v_pk_mul_f32 v[46:47], v[10:11], v[46:47]
	v_lshlrev_b32_e32 v12, 16, v163
	v_add_f32_e32 v46, v46, v63
	v_add_f32_e32 v136, v47, v46
	v_and_b32_e32 v46, 0xffff0000, v49
	v_lshlrev_b32_e32 v47, 16, v49
	v_lshlrev_b32_e32 v49, 16, v53
	v_pk_add_f32 v[48:49], v[46:47], v[48:49]
	v_add_f32_e32 v46, v177, v178
	v_add_f32_e32 v46, -2.0, v46
	v_fma_f32 v46, v21, v46, 2.0
	v_mul_f32_e32 v46, v46, v172
	v_mul_f32_e32 v46, v46, v168
	v_mul_f32_e32 v134, v13, v46
	v_pk_add_f32 v[46:47], v[134:135], v[136:137]
	v_and_b32_e32 v9, 0xffff0000, v163
	v_add_f32_e32 v2, v47, v2
	v_add_f32_e32 v2, v150, v2
	v_add_f32_e32 v2, v65, v2
	v_add_f32_e32 v2, v64, v2
	v_add_f32_e32 v2, v51, v2
	v_add_f32_e32 v2, v50, v2
	v_add_f32_e32 v2, v59, v2
	v_add_f32_e32 v2, v58, v2
	v_add_f32_e32 v2, v49, v2
	v_add_f32_e32 v2, v48, v2
	s_nop 1
	v_mov_b32_dpp v52, v2 quad_perm:[1,0,3,2] row_mask:0xf bank_mask:0xf
	s_waitcnt lgkmcnt(0)
	v_add_f32_e32 v2, v2, v52
	s_nop 1
	v_mov_b32_dpp v52, v2 quad_perm:[2,3,0,1] row_mask:0xf bank_mask:0xf
	s_waitcnt lgkmcnt(0)
	v_add_f32_e32 v2, v2, v52
	v_mov_b32_dpp v52, v46 quad_perm:[1,0,3,2] row_mask:0xf bank_mask:0xf
	v_mul_f32_e32 v53, 0x3c800000, v2
	v_fmac_f32_e32 v82, 0xbc800000, v2
	v_fmac_f32_e32 v4, 0xbc800000, v2
	v_fmac_f32_e32 v86, 0xbc800000, v2
	s_waitcnt lgkmcnt(0)
	v_pk_add_f32 v[54:55], v[46:47], v[52:53]
	v_pk_add_f32 v[56:57], v[46:47], v[52:53] neg_lo:[0,1] neg_hi:[0,1]
	v_mul_f32_e32 v47, v82, v82
	v_fmac_f32_e32 v47, v4, v4
	v_fmac_f32_e32 v47, v86, v86
	v_fmac_f32_e32 v123, 0xbc800000, v2
	v_fmac_f32_e32 v47, v123, v123
	v_fmac_f32_e32 v125, 0xbc800000, v2
	v_fmac_f32_e32 v47, v125, v125
	v_fmac_f32_e32 v67, 0xbc800000, v2
	v_fmac_f32_e32 v47, v67, v67
	v_fmac_f32_e32 v47, v57, v57
	v_fmac_f32_e32 v150, 0xbc800000, v2
	v_fmac_f32_e32 v47, v150, v150
	v_fmamk_f32 v60, v2, 0xbc800000, v65
	v_fmac_f32_e32 v64, 0xbc800000, v2
	v_mov_b32_e32 v2, v53
	v_fmac_f32_e32 v47, v60, v60
	v_pk_add_f32 v[52:53], v[50:51], v[2:3] op_sel_hi:[1,0] neg_lo:[0,1] neg_hi:[0,1]
	v_fmac_f32_e32 v47, v64, v64
	v_pk_mul_f32 v[50:51], v[52:53], v[52:53]
	v_pk_add_f32 v[48:49], v[48:49], v[2:3] op_sel_hi:[1,0] neg_lo:[0,1] neg_hi:[0,1]
	v_add_f32_e32 v47, v51, v47
	v_add_f32_e32 v47, v50, v47
	v_pk_add_f32 v[50:51], v[58:59], v[2:3] op_sel_hi:[1,0] neg_lo:[0,1] neg_hi:[0,1]
	v_mov_b32_dpp v46, v54 quad_perm:[2,3,0,1] row_mask:0xf bank_mask:0xf
	v_pk_mul_f32 v[58:59], v[50:51], v[50:51]
	s_nop 0
	v_add_f32_e32 v47, v59, v47
	v_add_f32_e32 v47, v58, v47
	v_pk_mul_f32 v[58:59], v[48:49], v[48:49]
	s_nop 0
	v_add_f32_e32 v2, v59, v47
	v_add_f32_e32 v2, v58, v2
	s_nop 1
	v_mov_b32_dpp v47, v2 quad_perm:[1,0,3,2] row_mask:0xf bank_mask:0xf
	s_waitcnt lgkmcnt(0)
	v_add_f32_e32 v2, v2, v47
	s_nop 1
	v_mov_b32_dpp v47, v2 quad_perm:[2,3,0,1] row_mask:0xf bank_mask:0xf
	s_waitcnt lgkmcnt(0)
	v_add_f32_e32 v2, v2, v47
	v_mov_b32_e32 v47, 0x3a27c5ac
	v_fmamk_f32 v2, v2, 0x3c800000, v47
	v_cmp_gt_f32_e32 vcc, s82, v2
	v_mul_f32_e32 v47, 0x4f800000, v2
	s_nop 0
	v_cndmask_b32_e32 v2, v2, v47, vcc
	v_sqrt_f32_e32 v47, v2
	s_nop 0
	v_add_u32_e32 v58, -1, v47
	v_fma_f32 v59, -v58, v47, v2
	v_cmp_ge_f32_e64 s[38:39], 0, v59
	v_add_u32_e32 v59, 1, v47
	s_nop 0
	v_cndmask_b32_e64 v58, v47, v58, s[38:39]
	v_fma_f32 v47, -v59, v47, v2
	v_cmp_lt_f32_e64 s[38:39], 0, v47
	s_nop 1
	v_cndmask_b32_e64 v47, v58, v59, s[38:39]
	v_mul_f32_e32 v58, 0x37800000, v47
	v_cndmask_b32_e32 v47, v47, v58, vcc
	v_cmp_class_f32_e32 vcc, v2, v229
	s_nop 1
	v_cndmask_b32_e32 v2, v47, v2, vcc
	v_div_scale_f32 v47, s[4:5], v2, v2, 1.0
	v_rcp_f32_e32 v58, v47
	s_nop 0
	v_fma_f32 v59, -v47, v58, 1.0
	v_fmac_f32_e32 v58, v59, v58
	v_div_scale_f32 v59, vcc, 1.0, v2, 1.0
	v_mul_f32_e32 v61, v59, v58
	v_fma_f32 v63, -v47, v61, v59
	v_fmac_f32_e32 v61, v63, v58
	v_fma_f32 v47, -v47, v61, v59
	v_div_fmas_f32 v47, v47, v58, v61
	v_div_fixup_f32 v47, v47, v2, 1.0
	v_pk_add_f32 v[54:55], v[54:55], v[46:47]
	v_mul_f32_e32 v133, v4, v47
	v_pk_mul_f32 v[56:57], v[56:57], v[46:47]
	v_mov_b32_e32 v72, v54
	v_mov_b32_e32 v55, v57
	v_pk_mul_f32 v[56:57], v[72:73], v[132:133]
	v_mul_f32_e32 v131, v82, v47
	v_add_f32_e32 v2, v22, v57
	v_add_f32_e32 v2, v56, v2
	v_mul_f32_e32 v58, v2, v179
	v_mov_b32_e32 v2, v54
	v_pk_mul_f32 v[56:57], v[2:3], v[130:131]
	v_mul_f32_e32 v129, v86, v47
	v_add_f32_e32 v2, v23, v57
	v_mov_b32_e32 v82, v54
	v_add_f32_e32 v2, v56, v2
	v_pk_mul_f32 v[56:57], v[82:83], v[128:129]
	v_mul_f32_e32 v127, v123, v47
	v_add_f32_e32 v4, v24, v57
	v_add_f32_e32 v4, v56, v4
	v_mul_f32_e32 v59, v4, v181
	v_mov_b32_e32 v4, v54
	v_pk_mul_f32 v[56:57], v[4:5], v[126:127]
	v_mul_f32_e32 v125, v125, v47
	v_add_f32_e32 v4, v25, v57
	v_mov_b32_e32 v86, v54
	v_add_f32_e32 v4, v56, v4
	v_pk_mul_f32 v[56:57], v[86:87], v[124:125]
	v_mul_f32_e32 v123, v67, v47
	v_add_f32_e32 v46, v26, v57
	v_add_f32_e32 v46, v56, v46
	v_mul_f32_e32 v61, v46, v70
	v_mov_b32_e32 v70, v54
	v_pk_mul_f32 v[56:57], v[70:71], v[122:123]
	v_mul_f32_e32 v2, v2, v180
	v_add_f32_e32 v46, v27, v57
	v_add_f32_e32 v46, v56, v46
	v_pk_mul_f32 v[56:57], v[54:55], v[84:85]
	v_mul_f32_e32 v65, v46, v121
	v_add_f32_e32 v46, v28, v57
	v_mul_f32_e32 v121, v150, v47
	v_mov_b32_e32 v55, v38
	v_add_f32_e32 v46, v56, v46
	v_pk_mul_f32 v[56:57], v[54:55], v[120:121]
	v_mul_f32_e32 v68, v46, v119
	v_add_f32_e32 v46, v29, v57
	v_mul_f32_e32 v119, v60, v47
	v_mov_b32_e32 v55, v39
	v_add_f32_e32 v46, v56, v46
	v_pk_mul_f32 v[56:57], v[54:55], v[118:119]
	v_mul_f32_e32 v69, v46, v117
	v_add_f32_e32 v46, v30, v57
	v_mul_f32_e32 v117, v64, v47
	v_mov_b32_e32 v55, v40
	v_add_f32_e32 v46, v56, v46
	v_pk_mul_f32 v[56:57], v[54:55], v[116:117]
	v_mul_f32_e32 v60, v46, v115
	v_add_f32_e32 v46, v31, v57
	v_mul_f32_e32 v115, v53, v47
	v_mov_b32_e32 v55, v41
	v_add_f32_e32 v46, v56, v46
	v_pk_mul_f32 v[56:57], v[54:55], v[114:115]
	v_mul_f32_e32 v64, v46, v113
	v_add_f32_e32 v46, v32, v57
	v_mul_f32_e32 v113, v52, v47
	v_mov_b32_e32 v55, v42
	v_add_f32_e32 v46, v56, v46
	v_pk_mul_f32 v[52:53], v[54:55], v[112:113]
	v_mul_f32_e32 v70, v46, v111
	v_add_f32_e32 v46, v33, v53
	v_mul_f32_e32 v111, v51, v47
	v_mov_b32_e32 v55, v43
	v_add_f32_e32 v46, v52, v46
	v_pk_mul_f32 v[52:53], v[54:55], v[110:111]
	v_mul_f32_e32 v72, v46, v109
	v_add_f32_e32 v46, v34, v53
	v_mul_f32_e32 v109, v50, v47
	v_mov_b32_e32 v55, v44
	v_add_f32_e32 v46, v52, v46
	v_pk_mul_f32 v[50:51], v[54:55], v[108:109]
	v_mul_f32_e32 v20, v46, v20
	v_add_f32_e32 v46, v35, v51
	v_mul_f32_e32 v67, v49, v47
	v_mov_b32_e32 v55, v45
	v_add_f32_e32 v46, v50, v46
	v_pk_mul_f32 v[50:51], v[54:55], v[66:67]
	v_mul_f32_e32 v56, 0x41000000, v58
	v_mul_f32_e32 v57, 0x41000000, v2
	v_mul_f32_e32 v82, v46, v17
	v_add_f32_e32 v17, v36, v51
	v_mul_f32_e32 v63, v48, v47
	v_mov_b32_e32 v55, v0
	v_mul_f32_e32 v48, 0x41000000, v60
	v_mul_f32_e32 v49, 0x41000000, v64
	v_med3_f32 v58, v56, s33, v233
	v_med3_f32 v57, v57, s33, v233
	v_mov_b32_e32 v56, v1
	v_add_f32_e32 v17, v50, v17
	v_pk_mul_f32 v[46:47], v[54:55], v[62:63]
	v_cvt_pk_fp8_f32 v56, v58, v57
	v_med3_f32 v48, v48, s33, v233
	v_med3_f32 v49, v49, s33, v233
	v_mov_b32_e32 v58, v1
	v_mul_f32_e32 v51, v17, v12
	v_add_f32_e32 v12, v37, v47
	v_cvt_pk_fp8_f32 v58, v48, v49
	v_mul_f32_e32 v4, v4, v182
	v_add_f32_e32 v12, v46, v12
	v_mul_f32_e32 v46, v12, v9
	v_mul_f32_e32 v52, 0x41000000, v59
	v_mul_f32_e32 v9, 0x41000000, v70
	v_mul_f32_e32 v53, 0x41000000, v4
	v_mul_f32_e32 v12, 0x41000000, v72
	v_mul_f32_e32 v54, 0x41000000, v61
	v_mul_f32_e32 v17, 0x41000000, v20
	v_mul_f32_e32 v55, 0x41000000, v65
	v_mul_f32_e32 v20, 0x41000000, v82
	v_med3_f32 v52, v52, s33, v233
	v_med3_f32 v53, v53, s33, v233
	v_med3_f32 v9, v9, s33, v233
	v_med3_f32 v12, v12, s33, v233
	v_cvt_pk_fp8_f32 v56, v52, v53 op_sel:[0,0,1]
	v_med3_f32 v52, v54, s33, v233
	v_med3_f32 v53, v55, s33, v233
	v_mov_b32_e32 v57, v1
	v_cvt_pk_fp8_f32 v58, v9, v12 op_sel:[0,0,1]
	v_med3_f32 v9, v17, s33, v233
	v_med3_f32 v12, v20, s33, v233
	v_mov_b32_e32 v59, v1
	v_cvt_pk_fp8_f32 v57, v52, v53
	v_cvt_pk_fp8_f32 v59, v9, v12
	v_mul_f32_e32 v50, 0x41000000, v68
	v_mul_f32_e32 v2, 0x41000000, v51
	v_mul_f32_e32 v51, 0x41000000, v69
	v_mul_f32_e32 v4, 0x41000000, v46
	v_med3_f32 v50, v50, s33, v233
	v_med3_f32 v51, v51, s33, v233
	v_med3_f32 v2, v2, s33, v233
	v_med3_f32 v4, v4, s33, v233
	v_cvt_pk_fp8_f32 v57, v50, v51 op_sel:[0,0,1]
	v_cvt_pk_fp8_f32 v59, v2, v4 op_sel:[0,0,1]
	v_lshl_add_u64 v[46:47], s[40:41], 0, v[78:79]
	v_add_co_u32_e32 v46, vcc, 0x1d200000, v46
	v_lshl_add_u64 v[78:79], v[78:79], 0, s[22:23]
	s_nop 0
	v_addc_co_u32_e32 v47, vcc, 0, v47, vcc
	global_store_dwordx4 v[46:47], v[56:59], off offset:1024 sc1
	s_cbranch_scc1 .LBB0_1141

.LBB0_1300:
	v_lshl_add_u64 v[2:3], s[58:59], 0, v[60:61]
	v_add_co_u32_e32 v4, vcc, 0x11100000, v2
	v_lshl_add_u64 v[158:159], s[58:59], 0, v[58:59]
	s_nop 0
	v_addc_co_u32_e32 v5, vcc, 0, v3, vcc
	global_load_dwordx2 v[94:95], v[4:5], off nt
	v_add_co_u32_e32 v96, vcc, 0x11101000, v2
	s_nop 1
	v_addc_co_u32_e32 v97, vcc, 0, v3, vcc
	global_load_dwordx2 v[98:99], v[96:97], off nt
	global_load_dwordx2 v[100:101], v[4:5], off offset:512 nt
	global_load_dwordx2 v[106:107], v[96:97], off offset:512 nt
	global_load_dwordx2 v[108:109], v[4:5], off offset:1024 nt
	global_load_dwordx2 v[110:111], v[96:97], off offset:1024 nt
	global_load_dwordx2 v[20:21], v[4:5], off offset:1536 nt
	global_load_dwordx2 v[18:19], v[96:97], off offset:1536 nt
	global_load_dwordx2 v[16:17], v[4:5], off offset:2048 nt
	global_load_dwordx2 v[14:15], v[96:97], off offset:2048 nt
	global_load_dwordx2 v[12:13], v[4:5], off offset:2560 nt
	global_load_dwordx2 v[10:11], v[96:97], off offset:2560 nt
	global_load_dwordx2 v[8:9], v[4:5], off offset:3072 nt
	global_load_dwordx2 v[6:7], v[96:97], off offset:3072 nt
	global_load_dwordx2 v[2:3], v[4:5], off offset:3584 nt
	s_nop 0
	global_load_dwordx2 v[4:5], v[96:97], off offset:3584 nt
	s_waitcnt vmcnt(15)
	v_and_b32_e32 v157, 0xffff0000, v94
	v_and_b32_e32 v155, 0xffff0000, v95
	v_lshlrev_b32_e32 v156, 16, v94
	v_lshlrev_b32_e32 v154, 16, v95
	v_mul_f32_e32 v47, v157, v157
	v_mul_f32_e32 v49, v155, v155
	v_fmac_f32_e32 v47, v156, v156
	v_fmac_f32_e32 v49, v154, v154
	v_add_f32_e32 v47, v47, v49
	s_waitcnt vmcnt(14)
	v_and_b32_e32 v153, 0xffff0000, v98
	v_and_b32_e32 v119, 0xffff0000, v99
	v_lshlrev_b32_e32 v152, 16, v98
	v_lshlrev_b32_e32 v118, 16, v99
	v_mul_f32_e32 v49, v153, v153
	v_mul_f32_e32 v51, v119, v119
	v_fmac_f32_e32 v49, v152, v152
	v_fmac_f32_e32 v51, v118, v118
	s_waitcnt vmcnt(13)
	v_and_b32_e32 v151, 0xffff0000, v100
	v_and_b32_e32 v149, 0xffff0000, v101
	v_add_f32_e32 v49, v49, v51
	v_lshlrev_b32_e32 v150, 16, v100
	v_lshlrev_b32_e32 v148, 16, v101
	v_mul_f32_e32 v51, v151, v151
	v_mul_f32_e32 v53, v149, v149
	v_fmac_f32_e32 v51, v150, v150
	v_fmac_f32_e32 v53, v148, v148
	s_waitcnt vmcnt(12)
	v_and_b32_e32 v147, 0xffff0000, v106
	v_and_b32_e32 v145, 0xffff0000, v107
	v_add_f32_e32 v51, v51, v53
	v_lshlrev_b32_e32 v146, 16, v106
	v_lshlrev_b32_e32 v144, 16, v107
	v_add_f32_e32 v47, v47, v51
	v_mul_f32_e32 v51, v147, v147
	v_mul_f32_e32 v53, v145, v145
	v_fmac_f32_e32 v51, v146, v146
	v_fmac_f32_e32 v53, v144, v144
	v_add_f32_e32 v51, v51, v53
	s_waitcnt vmcnt(11)
	v_and_b32_e32 v143, 0xffff0000, v108
	v_and_b32_e32 v141, 0xffff0000, v109
	v_add_f32_e32 v49, v49, v51
	v_lshlrev_b32_e32 v142, 16, v108
	v_lshlrev_b32_e32 v140, 16, v109
	v_mul_f32_e32 v51, v143, v143
	v_mul_f32_e32 v53, v141, v141
	v_fmac_f32_e32 v51, v142, v142
	v_fmac_f32_e32 v53, v140, v140
	s_waitcnt vmcnt(9)
	v_and_b32_e32 v131, 0xffff0000, v20
	v_and_b32_e32 v129, 0xffff0000, v21
	v_and_b32_e32 v139, 0xffff0000, v110
	v_and_b32_e32 v137, 0xffff0000, v111
	v_add_f32_e32 v51, v51, v53
	v_lshlrev_b32_e32 v130, 16, v20
	v_lshlrev_b32_e32 v128, 16, v21
	s_waitcnt vmcnt(8)
	v_lshlrev_b32_e32 v132, 16, v18
	v_and_b32_e32 v133, 0xffff0000, v18
	v_lshlrev_b32_e32 v134, 16, v19
	v_and_b32_e32 v135, 0xffff0000, v19
	v_mul_f32_e32 v18, v131, v131
	v_mul_f32_e32 v19, v129, v129
	s_waitcnt vmcnt(7)
	v_and_b32_e32 v127, 0xffff0000, v16
	v_and_b32_e32 v125, 0xffff0000, v17
	v_lshlrev_b32_e32 v138, 16, v110
	v_lshlrev_b32_e32 v136, 16, v111
	v_add_f32_e32 v47, v47, v51
	v_mul_f32_e32 v51, v139, v139
	v_mul_f32_e32 v53, v137, v137
	v_fmac_f32_e32 v18, v130, v130
	v_fmac_f32_e32 v19, v128, v128
	v_lshlrev_b32_e32 v126, 16, v16
	v_lshlrev_b32_e32 v124, 16, v17
	s_waitcnt vmcnt(6)
	v_lshlrev_b32_e32 v122, 16, v14
	v_and_b32_e32 v123, 0xffff0000, v14
	v_lshlrev_b32_e32 v120, 16, v15
	v_and_b32_e32 v121, 0xffff0000, v15
	v_mul_f32_e32 v14, v127, v127
	v_mul_f32_e32 v15, v125, v125
	v_fmac_f32_e32 v51, v138, v138
	v_fmac_f32_e32 v53, v136, v136
	v_add_f32_e32 v18, v18, v19
	v_mul_f32_e32 v19, v133, v133
	v_mul_f32_e32 v20, v135, v135
	v_fmac_f32_e32 v14, v126, v126
	v_fmac_f32_e32 v15, v124, v124
	v_add_f32_e32 v51, v51, v53
	v_fmac_f32_e32 v19, v132, v132
	v_fmac_f32_e32 v20, v134, v134
	v_add_f32_e32 v14, v14, v15
	v_mul_f32_e32 v15, v123, v123
	v_mul_f32_e32 v16, v121, v121
	v_add_f32_e32 v49, v49, v51
	v_add_f32_e32 v19, v19, v20
	v_fmac_f32_e32 v15, v122, v122
	v_fmac_f32_e32 v16, v120, v120
	s_waitcnt vmcnt(5)
	v_and_b32_e32 v117, 0xffff0000, v12
	v_and_b32_e32 v115, 0xffff0000, v13
	v_add_f32_e32 v18, v47, v18
	v_add_f32_e32 v19, v49, v19
	v_add_f32_e32 v15, v15, v16
	v_lshlrev_b32_e32 v116, 16, v12
	v_lshlrev_b32_e32 v114, 16, v13
	s_waitcnt vmcnt(4)
	v_lshlrev_b32_e32 v112, 16, v10
	v_and_b32_e32 v113, 0xffff0000, v10
	v_lshlrev_b32_e32 v110, 16, v11
	v_and_b32_e32 v111, 0xffff0000, v11
	v_mul_f32_e32 v10, v117, v117
	v_mul_f32_e32 v11, v115, v115
	s_waitcnt vmcnt(3)
	v_and_b32_e32 v109, 0xffff0000, v8
	v_and_b32_e32 v107, 0xffff0000, v9
	v_add_f32_e32 v14, v18, v14
	v_add_f32_e32 v15, v19, v15
	v_fmac_f32_e32 v10, v116, v116
	v_fmac_f32_e32 v11, v114, v114
	v_lshlrev_b32_e32 v108, 16, v8
	v_lshlrev_b32_e32 v106, 16, v9
	s_waitcnt vmcnt(2)
	v_lshlrev_b32_e32 v20, 16, v6
	v_and_b32_e32 v21, 0xffff0000, v6
	v_lshlrev_b32_e32 v18, 16, v7
	v_and_b32_e32 v19, 0xffff0000, v7
	v_mul_f32_e32 v6, v109, v109
	v_mul_f32_e32 v7, v107, v107
	s_waitcnt vmcnt(1)
	v_and_b32_e32 v101, 0xffff0000, v2
	v_and_b32_e32 v99, 0xffff0000, v3
	v_add_f32_e32 v10, v10, v11
	v_fmac_f32_e32 v6, v108, v108
	v_fmac_f32_e32 v7, v106, v106
	v_lshlrev_b32_e32 v100, 16, v2
	v_lshlrev_b32_e32 v98, 16, v3
	v_mul_f32_e32 v2, v101, v101
	v_mul_f32_e32 v3, v99, v99
	v_add_f32_e32 v10, v14, v10
	v_add_f32_e32 v6, v6, v7
	s_waitcnt vmcnt(0)
	v_and_b32_e32 v97, 0xffff0000, v4
	v_and_b32_e32 v95, 0xffff0000, v5
	v_fmac_f32_e32 v2, v100, v100
	v_fmac_f32_e32 v3, v98, v98
	v_add_f32_e32 v6, v10, v6
	v_lshlrev_b32_e32 v96, 16, v4
	v_lshlrev_b32_e32 v94, 16, v5
	v_add_f32_e32 v2, v2, v3
	v_mul_f32_e32 v3, v97, v97
	v_mul_f32_e32 v4, v95, v95
	v_add_f32_e32 v2, v6, v2
	v_fmac_f32_e32 v3, v96, v96
	v_fmac_f32_e32 v4, v94, v94
	v_add_f32_e32 v3, v3, v4
	v_mov_b32_dpp v4, v2 quad_perm:[1,0,3,2] row_mask:0xf bank_mask:0xf
	v_mul_f32_e32 v11, v113, v113
	v_mul_f32_e32 v12, v111, v111
	v_fmac_f32_e32 v11, v112, v112
	v_fmac_f32_e32 v12, v110, v110
	s_waitcnt lgkmcnt(0)
	v_add_f32_e32 v2, v2, v4
	s_nop 1
	v_mov_b32_dpp v4, v2 quad_perm:[2,3,0,1] row_mask:0xf bank_mask:0xf
	v_mul_f32_e32 v7, v21, v21
	v_mul_f32_e32 v8, v19, v19
	v_add_f32_e32 v11, v11, v12
	v_fmac_f32_e32 v7, v20, v20
	s_waitcnt lgkmcnt(0)
	v_add_f32_e32 v2, v2, v4
	s_nop 1
	v_mov_b32_dpp v4, v2 row_half_mirror row_mask:0xf bank_mask:0xf
	v_fmac_f32_e32 v8, v18, v18
	v_add_f32_e32 v11, v15, v11
	v_add_f32_e32 v7, v7, v8
	v_add_f32_e32 v7, v11, v7
	s_waitcnt lgkmcnt(0)
	v_add_f32_e32 v2, v2, v4
	s_nop 1
	v_mov_b32_dpp v4, v2 row_mirror row_mask:0xf bank_mask:0xf
	v_add_f32_e32 v3, v7, v3
	v_mov_b32_e32 v51, 0
	s_waitcnt lgkmcnt(0)
	v_add_f32_e32 v2, v2, v4
	v_mov_b32_e32 v4, v2
	s_nop 1
	v_permlane16_swap_b32_e32 v2, v4
	v_add_f32_e32 v2, v2, v4
	v_mov_b32_e32 v4, v2
	s_nop 1
	v_permlane32_swap_b32_e32 v2, v4
	v_add_f32_e32 v2, v2, v4
	v_fmamk_f32 v2, v2, 0x3a000000, v228
	v_cmp_gt_f32_e32 vcc, s82, v2
	v_mul_f32_e32 v4, 0x4f800000, v2
	s_nop 0
	v_cndmask_b32_e32 v2, v2, v4, vcc
	v_sqrt_f32_e32 v4, v2
	s_nop 0
	v_add_u32_e32 v5, -1, v4
	v_fma_f32 v6, -v5, v4, v2
	v_cmp_ge_f32_e64 s[44:45], 0, v6
	v_add_u32_e32 v6, 1, v4
	s_nop 0
	v_cndmask_b32_e64 v5, v4, v5, s[44:45]
	v_fma_f32 v4, -v6, v4, v2
	v_cmp_lt_f32_e64 s[44:45], 0, v4
	s_nop 1
	v_cndmask_b32_e64 v4, v5, v6, s[44:45]
	v_mul_f32_e32 v5, 0x37800000, v4
	v_cndmask_b32_e32 v4, v4, v5, vcc
	v_cmp_class_f32_e32 vcc, v2, v229
	s_nop 1
	v_cndmask_b32_e32 v2, v4, v2, vcc
	v_mov_b32_dpp v4, v3 quad_perm:[1,0,3,2] row_mask:0xf bank_mask:0xf
	s_waitcnt lgkmcnt(0)
	v_add_f32_e32 v3, v3, v4
	s_nop 1
	v_mov_b32_dpp v4, v3 quad_perm:[2,3,0,1] row_mask:0xf bank_mask:0xf
	s_waitcnt lgkmcnt(0)
	v_add_f32_e32 v3, v3, v4
	s_nop 1
	v_mov_b32_dpp v4, v3 row_half_mirror row_mask:0xf bank_mask:0xf
	s_waitcnt lgkmcnt(0)
	v_add_f32_e32 v3, v3, v4
	s_nop 1
	v_mov_b32_dpp v4, v3 row_mirror row_mask:0xf bank_mask:0xf
	s_waitcnt lgkmcnt(0)
	v_add_f32_e32 v3, v3, v4
	v_mov_b32_e32 v4, v3
	s_nop 1
	v_permlane16_swap_b32_e32 v3, v4
	v_add_f32_e32 v3, v3, v4
	v_mov_b32_e32 v4, v3
	s_nop 1
	v_permlane32_swap_b32_e32 v3, v4
	v_add_f32_e32 v3, v3, v4
	v_fmamk_f32 v3, v3, 0x3a000000, v228
	v_cmp_gt_f32_e32 vcc, s82, v3
	v_mul_f32_e32 v4, 0x4f800000, v3
	s_nop 0
	v_cndmask_b32_e32 v3, v3, v4, vcc
	v_sqrt_f32_e32 v4, v3
	s_nop 0
	v_add_u32_e32 v5, -1, v4
	v_fma_f32 v6, -v5, v4, v3
	v_cmp_ge_f32_e64 s[44:45], 0, v6
	v_add_u32_e32 v6, 1, v4
	s_nop 0
	v_cndmask_b32_e64 v5, v4, v5, s[44:45]
	v_fma_f32 v4, -v6, v4, v3
	v_cmp_lt_f32_e64 s[44:45], 0, v4
	s_nop 1
	v_cndmask_b32_e64 v4, v5, v6, s[44:45]
	v_mul_f32_e32 v5, 0x37800000, v4
	v_cndmask_b32_e32 v4, v4, v5, vcc
	v_cmp_class_f32_e32 vcc, v3, v229
	s_nop 1
	v_cndmask_b32_e32 v3, v4, v3, vcc
	v_div_scale_f32 v4, s[4:5], v2, v2, 1.0
	v_rcp_f32_e32 v5, v4
	s_nop 0
	v_fma_f32 v6, -v4, v5, 1.0
	v_fmac_f32_e32 v5, v6, v5
	v_div_scale_f32 v6, vcc, 1.0, v2, 1.0
	v_mul_f32_e32 v7, v6, v5
	v_fma_f32 v8, -v4, v7, v6
	v_fmac_f32_e32 v7, v8, v5
	v_fma_f32 v4, -v4, v7, v6
	v_div_fmas_f32 v4, v4, v5, v7
	v_div_fixup_f32 v102, v4, v2, 1.0
	v_div_scale_f32 v2, s[4:5], v3, v3, 1.0
	v_rcp_f32_e32 v4, v2
	v_pk_mul_f32 v[156:157], v[102:103], v[156:157] op_sel_hi:[0,1]
	v_pk_mul_f32 v[154:155], v[102:103], v[154:155] op_sel_hi:[0,1]
	v_fma_f32 v5, -v2, v4, 1.0
	v_fmac_f32_e32 v4, v5, v4
	v_div_scale_f32 v5, vcc, 1.0, v3, 1.0
	v_mul_f32_e32 v6, v5, v4
	v_fma_f32 v7, -v2, v6, v5
	v_fmac_f32_e32 v6, v7, v4
	v_fma_f32 v2, -v2, v6, v5
	v_div_fmas_f32 v2, v2, v4, v6
	v_div_fixup_f32 v104, v2, v3, 1.0
	global_load_dwordx4 v[2:5], v[26:27], off
	global_load_dwordx4 v[6:9], v[62:63], off
	global_load_dwordx4 v[14:17], v[64:65], off
	v_pk_mul_f32 v[152:153], v[104:105], v[152:153] op_sel_hi:[0,1]
	v_pk_mul_f32 v[118:119], v[104:105], v[118:119] op_sel_hi:[0,1]
	s_waitcnt vmcnt(1)
	v_pk_add_f32 v[8:9], v[8:9], 1.0 op_sel_hi:[1,0]
	v_pk_add_f32 v[6:7], v[6:7], 1.0 op_sel_hi:[1,0]
	v_pk_mul_f32 v[160:161], v[4:5], v[8:9]
	v_pk_mul_f32 v[162:163], v[2:3], v[6:7]
	global_load_dwordx4 v[2:5], v[66:67], off
	global_load_dwordx4 v[10:13], v[68:69], off
	global_load_dwordx4 v[6:9], v[28:29], off
	s_waitcnt vmcnt(3)
	v_pk_fma_f32 v[156:157], v[162:163], v[156:157], v[14:15]
	v_pk_fma_f32 v[154:155], v[160:161], v[154:155], v[16:17]
	v_med3_f32 v47, v156, s33, v233
	v_med3_f32 v49, v157, s33, v233
	v_cvt_pk_fp8_f32 v51, v47, v49
	ds_read_b128 v[206:209], v105
	ds_read_b128 v[238:241], v105 offset:2048
	v_med3_f32 v47, v154, s33, v233
	v_med3_f32 v49, v155, s33, v233
	v_cvt_pk_fp8_f32 v51, v47, v49 op_sel:[0,0,1]
	v_pk_fma_f32 v[16:17], v[160:161], v[118:119], v[16:17]
	v_pk_fma_f32 v[14:15], v[162:163], v[152:153], v[14:15]
	v_add_co_u32_e32 v118, vcc, s80, v158
	s_waitcnt lgkmcnt(1)
	v_fma_f32 v224, v156, v206, 0
	v_addc_co_u32_e32 v119, vcc, 0, v159, vcc
	v_fma_f32 v223, v156, v207, 0
	v_fma_f32 v221, v156, v208, 0
	v_fma_f32 v217, v156, v209, 0
	v_fma_f32 v225, v14, v206, 0
	v_fma_f32 v222, v14, v207, 0
	v_fma_f32 v219, v14, v208, 0
	v_fma_f32 v215, v14, v209, 0
	ds_read_b128 v[206:209], v105 offset:1024
	global_store_dword v[118:119], v51, off
	v_med3_f32 v47, v14, s33, v233
	v_med3_f32 v49, v15, s33, v233
	v_mov_b32_e32 v51, 0
	v_cvt_pk_fp8_f32 v51, v47, v49
	v_med3_f32 v47, v16, s33, v233
	v_med3_f32 v49, v17, s33, v233
	s_waitcnt lgkmcnt(0)
	v_fma_f32 v220, v156, v206, 0
	v_fma_f32 v216, v156, v207, 0
	v_fma_f32 v213, v156, v208, 0
	v_fma_f32 v211, v156, v209, 0
	v_fma_f32 v218, v14, v206, 0
	v_fma_f32 v214, v14, v207, 0
	v_fma_f32 v212, v14, v208, 0
	v_fma_f32 v210, v14, v209, 0
	v_fma_f32 v209, v156, v238, 0
	v_fma_f32 v207, v156, v239, 0
	v_fma_f32 v205, v156, v240, 0
	v_fma_f32 v153, v156, v241, 0
	v_fma_f32 v208, v14, v238, 0
	v_fma_f32 v206, v14, v239, 0
	v_fma_f32 v158, v14, v240, 0
	v_fma_f32 v57, v14, v241, 0
	ds_read_b128 v[238:241], v105 offset:3072
	v_cvt_pk_fp8_f32 v51, v47, v49 op_sel:[0,0,1]
	global_store_dword v[118:119], v51, off offset:2048
	s_waitcnt lgkmcnt(0)
	v_fma_f32 v159, v156, v238, 0
	v_fma_f32 v152, v156, v239, 0
	v_fma_f32 v53, v156, v240, 0
	v_fma_f32 v49, v156, v241, 0
	v_fma_f32 v156, v14, v238, 0
	v_fma_f32 v55, v14, v239, 0
	v_fma_f32 v51, v14, v240, 0
	v_fma_f32 v47, v14, v241, 0
	ds_read_b128 v[238:241], v105 offset:4096
	s_waitcnt lgkmcnt(0)
	v_fmac_f32_e32 v224, v157, v238
	v_fmac_f32_e32 v223, v157, v239
	v_fmac_f32_e32 v221, v157, v240
	v_fmac_f32_e32 v217, v157, v241
	v_fmac_f32_e32 v225, v15, v238
	v_fmac_f32_e32 v222, v15, v239
	v_fmac_f32_e32 v219, v15, v240
	v_fmac_f32_e32 v215, v15, v241
	ds_read_b128 v[238:241], v105 offset:5120
	s_waitcnt lgkmcnt(0)
	v_fmac_f32_e32 v220, v157, v238
	v_fmac_f32_e32 v216, v157, v239
	v_fmac_f32_e32 v213, v157, v240
	v_fmac_f32_e32 v211, v157, v241
	v_fmac_f32_e32 v218, v15, v238
	v_fmac_f32_e32 v214, v15, v239
	v_fmac_f32_e32 v212, v15, v240
	v_fmac_f32_e32 v210, v15, v241
	ds_read_b128 v[238:241], v105 offset:6144
	s_waitcnt lgkmcnt(0)
	v_fmac_f32_e32 v209, v157, v238
	v_fmac_f32_e32 v207, v157, v239
	v_fmac_f32_e32 v205, v157, v240
	v_fmac_f32_e32 v153, v157, v241
	v_fmac_f32_e32 v208, v15, v238
	v_fmac_f32_e32 v206, v15, v239
	v_fmac_f32_e32 v158, v15, v240
	v_fmac_f32_e32 v57, v15, v241
	ds_read_b128 v[238:241], v105 offset:7168
	s_waitcnt lgkmcnt(0)
	v_fmac_f32_e32 v159, v157, v238
	v_fmac_f32_e32 v152, v157, v239
	v_fmac_f32_e32 v53, v157, v240
	v_fmac_f32_e32 v49, v157, v241
	v_fmac_f32_e32 v156, v15, v238
	v_fmac_f32_e32 v55, v15, v239
	v_fmac_f32_e32 v51, v15, v240
	v_fmac_f32_e32 v47, v15, v241
	ds_read_b128 v[238:241], v105 offset:8192
	s_waitcnt lgkmcnt(0)
	v_fmac_f32_e32 v224, v154, v238
	v_fmac_f32_e32 v223, v154, v239
	v_fmac_f32_e32 v221, v154, v240
	v_fmac_f32_e32 v217, v154, v241
	v_fmac_f32_e32 v225, v16, v238
	v_fmac_f32_e32 v222, v16, v239
	v_fmac_f32_e32 v219, v16, v240
	v_fmac_f32_e32 v215, v16, v241
	ds_read_b128 v[238:241], v105 offset:9216
	s_waitcnt lgkmcnt(0)
	v_fmac_f32_e32 v220, v154, v238
	v_fmac_f32_e32 v216, v154, v239
	v_fmac_f32_e32 v213, v154, v240
	v_fmac_f32_e32 v211, v154, v241
	v_fmac_f32_e32 v218, v16, v238
	v_fmac_f32_e32 v214, v16, v239
	v_fmac_f32_e32 v212, v16, v240
	v_fmac_f32_e32 v210, v16, v241
	ds_read_b128 v[238:241], v105 offset:10240
	s_waitcnt lgkmcnt(0)
	v_fmac_f32_e32 v209, v154, v238
	v_fmac_f32_e32 v207, v154, v239
	v_fmac_f32_e32 v205, v154, v240
	v_fmac_f32_e32 v153, v154, v241
	v_fmac_f32_e32 v208, v16, v238
	v_fmac_f32_e32 v206, v16, v239
	v_fmac_f32_e32 v158, v16, v240
	v_fmac_f32_e32 v57, v16, v241
	ds_read_b128 v[238:241], v105 offset:11264
	s_waitcnt lgkmcnt(0)
	v_fmac_f32_e32 v159, v154, v238
	v_fmac_f32_e32 v152, v154, v239
	v_fmac_f32_e32 v53, v154, v240
	v_fmac_f32_e32 v49, v154, v241
	v_fmac_f32_e32 v156, v16, v238
	v_fmac_f32_e32 v55, v16, v239
	v_fmac_f32_e32 v51, v16, v240
	v_fmac_f32_e32 v47, v16, v241
	ds_read_b128 v[238:241], v105 offset:12288
	s_waitcnt lgkmcnt(0)
	v_fmac_f32_e32 v224, v155, v238
	v_fmac_f32_e32 v223, v155, v239
	v_fmac_f32_e32 v221, v155, v240
	v_fmac_f32_e32 v217, v155, v241
	v_fmac_f32_e32 v225, v17, v238
	v_fmac_f32_e32 v222, v17, v239
	v_fmac_f32_e32 v219, v17, v240
	v_fmac_f32_e32 v215, v17, v241
	ds_read_b128 v[238:241], v105 offset:13312
	s_waitcnt lgkmcnt(0)
	v_fmac_f32_e32 v220, v155, v238
	v_fmac_f32_e32 v216, v155, v239
	v_fmac_f32_e32 v213, v155, v240
	v_fmac_f32_e32 v211, v155, v241
	v_fmac_f32_e32 v218, v17, v238
	v_fmac_f32_e32 v214, v17, v239
	v_fmac_f32_e32 v212, v17, v240
	v_fmac_f32_e32 v210, v17, v241
	ds_read_b128 v[238:241], v105 offset:14336
	s_waitcnt lgkmcnt(0)
	v_fmac_f32_e32 v209, v155, v238
	v_fmac_f32_e32 v207, v155, v239
	v_fmac_f32_e32 v205, v155, v240
	v_fmac_f32_e32 v153, v155, v241
	v_fmac_f32_e32 v208, v17, v238
	v_fmac_f32_e32 v206, v17, v239
	v_fmac_f32_e32 v158, v17, v240
	v_fmac_f32_e32 v57, v17, v241
	ds_read_b128 v[238:241], v105 offset:15360
	s_waitcnt lgkmcnt(0)
	v_fmac_f32_e32 v53, v155, v240
	v_fmac_f32_e32 v55, v17, v239
	v_fmac_f32_e32 v51, v17, v240
	v_fmac_f32_e32 v159, v155, v238
	v_fmac_f32_e32 v152, v155, v239
	v_fmac_f32_e32 v49, v155, v241
	v_fmac_f32_e32 v156, v17, v238
	v_fmac_f32_e32 v47, v17, v241
	s_waitcnt vmcnt(3)
	v_pk_add_f32 v[10:11], v[10:11], 1.0 op_sel_hi:[1,0]
	v_pk_mul_f32 v[150:151], v[102:103], v[150:151] op_sel_hi:[0,1]
	s_waitcnt vmcnt(2)
	v_pk_mul_f32 v[154:155], v[6:7], v[10:11]
	v_pk_add_f32 v[12:13], v[12:13], 1.0 op_sel_hi:[1,0]
	v_pk_fma_f32 v[160:161], v[150:151], v[154:155], v[2:3]
	v_pk_mul_f32 v[146:147], v[104:105], v[146:147] op_sel_hi:[0,1]
	v_pk_mul_f32 v[16:17], v[8:9], v[12:13]
	v_pk_mul_f32 v[14:15], v[102:103], v[148:149] op_sel_hi:[0,1]
	v_pk_mul_f32 v[144:145], v[104:105], v[144:145] op_sel_hi:[0,1]
	v_pk_fma_f32 v[154:155], v[154:155], v[146:147], v[2:3]
	v_med3_f32 v2, v160, s33, v233
	v_med3_f32 v3, v161, s33, v233
	v_mov_b32_e32 v148, 0
	v_pk_fma_f32 v[14:15], v[14:15], v[16:17], v[4:5]
	v_pk_fma_f32 v[16:17], v[16:17], v[144:145], v[4:5]
	v_cvt_pk_fp8_f32 v148, v2, v3
	v_med3_f32 v4, v154, s33, v233
	v_med3_f32 v5, v155, s33, v233
	v_mov_b32_e32 v149, 0
	v_cvt_pk_fp8_f32 v149, v4, v5
	v_med3_f32 v2, v14, s33, v233
	v_med3_f32 v3, v15, s33, v233
	v_cvt_pk_fp8_f32 v148, v2, v3 op_sel:[0,0,1]
	v_med3_f32 v2, v16, s33, v233
	v_med3_f32 v3, v17, s33, v233
	global_load_dwordx4 v[6:9], v[70:71], off
	global_load_dwordx4 v[10:13], v[72:73], off
	v_cvt_pk_fp8_f32 v149, v2, v3 op_sel:[0,0,1]
	global_load_dwordx4 v[2:5], v[30:31], off
	ds_read_b128 v[144:147], v105 offset:16384
	global_store_dword v[118:119], v148, off offset:256
	global_store_dword v[118:119], v149, off offset:2304
	ds_read_b128 v[148:151], v105 offset:17408
	s_waitcnt lgkmcnt(1)
	v_fmac_f32_e32 v224, v160, v144
	v_fmac_f32_e32 v223, v160, v145
	v_fmac_f32_e32 v221, v160, v146
	v_fmac_f32_e32 v217, v160, v147
	v_fmac_f32_e32 v225, v154, v144
	v_fmac_f32_e32 v222, v154, v145
	v_fmac_f32_e32 v219, v154, v146
	v_fmac_f32_e32 v215, v154, v147
	ds_read_b128 v[144:147], v105 offset:18432
	s_waitcnt lgkmcnt(1)
	v_fmac_f32_e32 v220, v160, v148
	v_fmac_f32_e32 v216, v160, v149
	v_fmac_f32_e32 v213, v160, v150
	v_fmac_f32_e32 v211, v160, v151
	v_fmac_f32_e32 v218, v154, v148
	v_fmac_f32_e32 v214, v154, v149
	v_fmac_f32_e32 v212, v154, v150
	v_fmac_f32_e32 v210, v154, v151
	ds_read_b128 v[148:151], v105 offset:19456
	s_waitcnt lgkmcnt(1)
	v_fmac_f32_e32 v209, v160, v144
	v_fmac_f32_e32 v207, v160, v145
	v_fmac_f32_e32 v205, v160, v146
	v_fmac_f32_e32 v153, v160, v147
	v_fmac_f32_e32 v208, v154, v144
	v_fmac_f32_e32 v206, v154, v145
	v_fmac_f32_e32 v158, v154, v146
	v_fmac_f32_e32 v57, v154, v147
	ds_read_b128 v[144:147], v105 offset:20480
	s_waitcnt lgkmcnt(1)
	v_fmac_f32_e32 v159, v160, v148
	v_fmac_f32_e32 v152, v160, v149
	v_fmac_f32_e32 v53, v160, v150
	v_fmac_f32_e32 v49, v160, v151
	v_fmac_f32_e32 v156, v154, v148
	v_fmac_f32_e32 v55, v154, v149
	v_fmac_f32_e32 v51, v154, v150
	v_fmac_f32_e32 v47, v154, v151
	ds_read_b128 v[148:151], v105 offset:21504
	s_waitcnt lgkmcnt(1)
	v_fmac_f32_e32 v224, v161, v144
	v_fmac_f32_e32 v223, v161, v145
	v_fmac_f32_e32 v221, v161, v146
	v_fmac_f32_e32 v217, v161, v147
	v_fmac_f32_e32 v225, v155, v144
	v_fmac_f32_e32 v222, v155, v145
	v_fmac_f32_e32 v219, v155, v146
	v_fmac_f32_e32 v215, v155, v147
	ds_read_b128 v[144:147], v105 offset:22528
	s_waitcnt lgkmcnt(1)
	v_fmac_f32_e32 v220, v161, v148
	v_fmac_f32_e32 v216, v161, v149
	v_fmac_f32_e32 v213, v161, v150
	v_fmac_f32_e32 v211, v161, v151
	v_fmac_f32_e32 v218, v155, v148
	v_fmac_f32_e32 v214, v155, v149
	v_fmac_f32_e32 v212, v155, v150
	v_fmac_f32_e32 v210, v155, v151
	ds_read_b128 v[148:151], v105 offset:23552
	s_waitcnt lgkmcnt(1)
	v_fmac_f32_e32 v209, v161, v144
	v_fmac_f32_e32 v207, v161, v145
	v_fmac_f32_e32 v205, v161, v146
	v_fmac_f32_e32 v153, v161, v147
	v_fmac_f32_e32 v208, v155, v144
	v_fmac_f32_e32 v206, v155, v145
	v_fmac_f32_e32 v158, v155, v146
	v_fmac_f32_e32 v57, v155, v147
	ds_read_b128 v[144:147], v105 offset:24576
	s_waitcnt lgkmcnt(1)
	v_fmac_f32_e32 v159, v161, v148
	v_fmac_f32_e32 v152, v161, v149
	v_fmac_f32_e32 v53, v161, v150
	v_fmac_f32_e32 v49, v161, v151
	v_fmac_f32_e32 v156, v155, v148
	v_fmac_f32_e32 v55, v155, v149
	v_fmac_f32_e32 v51, v155, v150
	v_fmac_f32_e32 v47, v155, v151
	ds_read_b128 v[148:151], v105 offset:25600
	s_waitcnt lgkmcnt(1)
	v_fmac_f32_e32 v224, v14, v144
	v_fmac_f32_e32 v223, v14, v145
	v_fmac_f32_e32 v221, v14, v146
	v_fmac_f32_e32 v217, v14, v147
	v_fmac_f32_e32 v225, v16, v144
	v_fmac_f32_e32 v222, v16, v145
	v_fmac_f32_e32 v219, v16, v146
	v_fmac_f32_e32 v215, v16, v147
	ds_read_b128 v[144:147], v105 offset:26624
	s_waitcnt lgkmcnt(1)
	v_fmac_f32_e32 v220, v14, v148
	v_fmac_f32_e32 v216, v14, v149
	v_fmac_f32_e32 v213, v14, v150
	v_fmac_f32_e32 v211, v14, v151
	v_fmac_f32_e32 v218, v16, v148
	v_fmac_f32_e32 v214, v16, v149
	v_fmac_f32_e32 v212, v16, v150
	v_fmac_f32_e32 v210, v16, v151
	ds_read_b128 v[148:151], v105 offset:27648
	s_waitcnt lgkmcnt(1)
	v_fmac_f32_e32 v209, v14, v144
	v_fmac_f32_e32 v207, v14, v145
	v_fmac_f32_e32 v205, v14, v146
	v_fmac_f32_e32 v153, v14, v147
	v_fmac_f32_e32 v208, v16, v144
	v_fmac_f32_e32 v206, v16, v145
	v_fmac_f32_e32 v158, v16, v146
	v_fmac_f32_e32 v57, v16, v147
	ds_read_b128 v[144:147], v105 offset:28672
	s_waitcnt lgkmcnt(1)
	v_fmac_f32_e32 v159, v14, v148
	v_fmac_f32_e32 v152, v14, v149
	v_fmac_f32_e32 v53, v14, v150
	v_fmac_f32_e32 v49, v14, v151
	v_fmac_f32_e32 v156, v16, v148
	v_fmac_f32_e32 v55, v16, v149
	v_fmac_f32_e32 v51, v16, v150
	v_fmac_f32_e32 v47, v16, v151
	ds_read_b128 v[148:151], v105 offset:29696
	s_waitcnt lgkmcnt(1)
	v_fmac_f32_e32 v224, v15, v144
	v_fmac_f32_e32 v223, v15, v145
	v_fmac_f32_e32 v221, v15, v146
	v_fmac_f32_e32 v217, v15, v147
	v_fmac_f32_e32 v225, v17, v144
	v_fmac_f32_e32 v222, v17, v145
	v_fmac_f32_e32 v219, v17, v146
	v_fmac_f32_e32 v215, v17, v147
	ds_read_b128 v[144:147], v105 offset:30720
	s_waitcnt lgkmcnt(1)
	v_fmac_f32_e32 v220, v15, v148
	v_fmac_f32_e32 v216, v15, v149
	v_fmac_f32_e32 v213, v15, v150
	v_fmac_f32_e32 v211, v15, v151
	v_fmac_f32_e32 v218, v17, v148
	v_fmac_f32_e32 v214, v17, v149
	v_fmac_f32_e32 v212, v17, v150
	v_fmac_f32_e32 v210, v17, v151
	ds_read_b128 v[148:151], v105 offset:31744
	s_waitcnt lgkmcnt(1)
	v_fmac_f32_e32 v57, v17, v147
	v_fmac_f32_e32 v209, v15, v144
	v_fmac_f32_e32 v207, v15, v145
	v_fmac_f32_e32 v205, v15, v146
	s_waitcnt lgkmcnt(0)
	v_fmac_f32_e32 v53, v15, v150
	v_fmac_f32_e32 v55, v17, v149
	v_fmac_f32_e32 v51, v17, v150
	v_fmac_f32_e32 v153, v15, v147
	v_fmac_f32_e32 v208, v17, v144
	v_fmac_f32_e32 v206, v17, v145
	v_fmac_f32_e32 v158, v17, v146
	v_fmac_f32_e32 v159, v15, v148
	v_fmac_f32_e32 v152, v15, v149
	v_fmac_f32_e32 v49, v15, v151
	v_fmac_f32_e32 v156, v17, v148
	v_fmac_f32_e32 v47, v17, v151
	s_waitcnt vmcnt(3)
	v_pk_add_f32 v[10:11], v[10:11], 1.0 op_sel_hi:[1,0]
	v_pk_mul_f32 v[142:143], v[102:103], v[142:143] op_sel_hi:[0,1]
	s_waitcnt vmcnt(2)
	v_pk_mul_f32 v[144:145], v[2:3], v[10:11]
	v_pk_add_f32 v[12:13], v[12:13], 1.0 op_sel_hi:[1,0]
	v_pk_fma_f32 v[146:147], v[142:143], v[144:145], v[6:7]
	v_pk_mul_f32 v[138:139], v[104:105], v[138:139] op_sel_hi:[0,1]
	v_pk_mul_f32 v[16:17], v[4:5], v[12:13]
	v_pk_mul_f32 v[14:15], v[102:103], v[140:141] op_sel_hi:[0,1]
	v_pk_mul_f32 v[136:137], v[104:105], v[136:137] op_sel_hi:[0,1]
	v_pk_fma_f32 v[144:145], v[138:139], v[144:145], v[6:7]
	v_med3_f32 v6, v146, s33, v233
	v_med3_f32 v7, v147, s33, v233
	v_mov_b32_e32 v140, 0
	v_pk_fma_f32 v[14:15], v[14:15], v[16:17], v[8:9]
	v_pk_fma_f32 v[16:17], v[136:137], v[16:17], v[8:9]
	v_cvt_pk_fp8_f32 v140, v6, v7
	v_med3_f32 v8, v144, s33, v233
	v_med3_f32 v9, v145, s33, v233
	v_mov_b32_e32 v141, 0
	v_cvt_pk_fp8_f32 v141, v8, v9
	v_med3_f32 v6, v14, s33, v233
	v_med3_f32 v7, v15, s33, v233
	v_cvt_pk_fp8_f32 v140, v6, v7 op_sel:[0,0,1]
	v_med3_f32 v6, v16, s33, v233
	v_med3_f32 v7, v17, s33, v233
	global_load_dwordx4 v[2:5], v[74:75], off
	global_load_dwordx4 v[10:13], v[76:77], off
	v_cvt_pk_fp8_f32 v141, v6, v7 op_sel:[0,0,1]
	global_load_dwordx4 v[6:9], v[32:33], off
	ds_read_b128 v[136:139], v105 offset:32768
	global_store_dword v[118:119], v140, off offset:512
	global_store_dword v[118:119], v141, off offset:2560
	ds_read_b128 v[140:143], v105 offset:33792
	s_waitcnt lgkmcnt(1)
	v_fmac_f32_e32 v224, v146, v136
	v_fmac_f32_e32 v223, v146, v137
	v_fmac_f32_e32 v221, v146, v138
	v_fmac_f32_e32 v217, v146, v139
	v_fmac_f32_e32 v225, v144, v136
	v_fmac_f32_e32 v222, v144, v137
	v_fmac_f32_e32 v219, v144, v138
	v_fmac_f32_e32 v215, v144, v139
	ds_read_b128 v[136:139], v105 offset:34816
	s_waitcnt lgkmcnt(1)
	v_fmac_f32_e32 v220, v146, v140
	v_fmac_f32_e32 v216, v146, v141
	v_fmac_f32_e32 v213, v146, v142
	v_fmac_f32_e32 v211, v146, v143
	v_fmac_f32_e32 v218, v144, v140
	v_fmac_f32_e32 v214, v144, v141
	v_fmac_f32_e32 v212, v144, v142
	v_fmac_f32_e32 v210, v144, v143
	ds_read_b128 v[140:143], v105 offset:35840
	s_waitcnt lgkmcnt(1)
	v_fmac_f32_e32 v209, v146, v136
	v_fmac_f32_e32 v207, v146, v137
	v_fmac_f32_e32 v205, v146, v138
	v_fmac_f32_e32 v153, v146, v139
	v_fmac_f32_e32 v208, v144, v136
	v_fmac_f32_e32 v206, v144, v137
	v_fmac_f32_e32 v158, v144, v138
	v_fmac_f32_e32 v57, v144, v139
	ds_read_b128 v[136:139], v105 offset:36864
	s_waitcnt lgkmcnt(1)
	v_fmac_f32_e32 v159, v146, v140
	v_fmac_f32_e32 v152, v146, v141
	v_fmac_f32_e32 v53, v146, v142
	v_fmac_f32_e32 v49, v146, v143
	v_fmac_f32_e32 v156, v144, v140
	v_fmac_f32_e32 v55, v144, v141
	v_fmac_f32_e32 v51, v144, v142
	v_fmac_f32_e32 v47, v144, v143
	ds_read_b128 v[140:143], v105 offset:37888
	s_waitcnt lgkmcnt(1)
	v_fmac_f32_e32 v224, v147, v136
	v_fmac_f32_e32 v223, v147, v137
	v_fmac_f32_e32 v221, v147, v138
	v_fmac_f32_e32 v217, v147, v139
	v_fmac_f32_e32 v225, v145, v136
	v_fmac_f32_e32 v222, v145, v137
	v_fmac_f32_e32 v219, v145, v138
	v_fmac_f32_e32 v215, v145, v139
	ds_read_b128 v[136:139], v105 offset:38912
	s_waitcnt lgkmcnt(1)
	v_fmac_f32_e32 v220, v147, v140
	v_fmac_f32_e32 v216, v147, v141
	v_fmac_f32_e32 v213, v147, v142
	v_fmac_f32_e32 v211, v147, v143
	v_fmac_f32_e32 v218, v145, v140
	v_fmac_f32_e32 v214, v145, v141
	v_fmac_f32_e32 v212, v145, v142
	v_fmac_f32_e32 v210, v145, v143
	ds_read_b128 v[140:143], v105 offset:39936
	s_waitcnt lgkmcnt(1)
	v_fmac_f32_e32 v209, v147, v136
	v_fmac_f32_e32 v207, v147, v137
	v_fmac_f32_e32 v205, v147, v138
	v_fmac_f32_e32 v153, v147, v139
	v_fmac_f32_e32 v208, v145, v136
	v_fmac_f32_e32 v206, v145, v137
	v_fmac_f32_e32 v158, v145, v138
	v_fmac_f32_e32 v57, v145, v139
	ds_read_b128 v[136:139], v105 offset:40960
	s_waitcnt lgkmcnt(1)
	v_fmac_f32_e32 v159, v147, v140
	v_fmac_f32_e32 v152, v147, v141
	v_fmac_f32_e32 v53, v147, v142
	v_fmac_f32_e32 v49, v147, v143
	v_fmac_f32_e32 v156, v145, v140
	v_fmac_f32_e32 v55, v145, v141
	v_fmac_f32_e32 v51, v145, v142
	v_fmac_f32_e32 v47, v145, v143
	ds_read_b128 v[140:143], v105 offset:41984
	s_waitcnt lgkmcnt(1)
	v_fmac_f32_e32 v224, v14, v136
	v_fmac_f32_e32 v223, v14, v137
	v_fmac_f32_e32 v221, v14, v138
	v_fmac_f32_e32 v217, v14, v139
	v_fmac_f32_e32 v225, v16, v136
	v_fmac_f32_e32 v222, v16, v137
	v_fmac_f32_e32 v219, v16, v138
	v_fmac_f32_e32 v215, v16, v139
	ds_read_b128 v[136:139], v105 offset:43008
	s_waitcnt lgkmcnt(1)
	v_fmac_f32_e32 v220, v14, v140
	v_fmac_f32_e32 v216, v14, v141
	v_fmac_f32_e32 v213, v14, v142
	v_fmac_f32_e32 v211, v14, v143
	v_fmac_f32_e32 v218, v16, v140
	v_fmac_f32_e32 v214, v16, v141
	v_fmac_f32_e32 v212, v16, v142
	v_fmac_f32_e32 v210, v16, v143
	ds_read_b128 v[140:143], v105 offset:44032
	s_waitcnt lgkmcnt(1)
	v_fmac_f32_e32 v209, v14, v136
	v_fmac_f32_e32 v207, v14, v137
	v_fmac_f32_e32 v205, v14, v138
	v_fmac_f32_e32 v153, v14, v139
	v_fmac_f32_e32 v208, v16, v136
	v_fmac_f32_e32 v206, v16, v137
	v_fmac_f32_e32 v158, v16, v138
	v_fmac_f32_e32 v57, v16, v139
	ds_read_b128 v[136:139], v105 offset:45056
	s_waitcnt lgkmcnt(1)
	v_fmac_f32_e32 v159, v14, v140
	v_fmac_f32_e32 v152, v14, v141
	v_fmac_f32_e32 v53, v14, v142
	v_fmac_f32_e32 v49, v14, v143
	v_fmac_f32_e32 v156, v16, v140
	v_fmac_f32_e32 v55, v16, v141
	v_fmac_f32_e32 v51, v16, v142
	v_fmac_f32_e32 v47, v16, v143
	ds_read_b128 v[140:143], v105 offset:46080
	s_waitcnt lgkmcnt(1)
	v_fmac_f32_e32 v224, v15, v136
	v_fmac_f32_e32 v223, v15, v137
	v_fmac_f32_e32 v221, v15, v138
	v_fmac_f32_e32 v217, v15, v139
	v_fmac_f32_e32 v225, v17, v136
	v_fmac_f32_e32 v222, v17, v137
	v_fmac_f32_e32 v219, v17, v138
	v_fmac_f32_e32 v215, v17, v139
	ds_read_b128 v[136:139], v105 offset:47104
	s_waitcnt lgkmcnt(1)
	v_fmac_f32_e32 v220, v15, v140
	v_fmac_f32_e32 v216, v15, v141
	v_fmac_f32_e32 v213, v15, v142
	v_fmac_f32_e32 v211, v15, v143
	v_fmac_f32_e32 v218, v17, v140
	v_fmac_f32_e32 v214, v17, v141
	v_fmac_f32_e32 v212, v17, v142
	v_fmac_f32_e32 v210, v17, v143
	ds_read_b128 v[140:143], v105 offset:48128
	s_waitcnt lgkmcnt(1)
	v_fmac_f32_e32 v57, v17, v139
	v_fmac_f32_e32 v209, v15, v136
	v_fmac_f32_e32 v207, v15, v137
	v_fmac_f32_e32 v205, v15, v138
	s_waitcnt lgkmcnt(0)
	v_fmac_f32_e32 v53, v15, v142
	v_fmac_f32_e32 v55, v17, v141
	v_fmac_f32_e32 v51, v17, v142
	v_fmac_f32_e32 v153, v15, v139
	v_fmac_f32_e32 v208, v17, v136
	v_fmac_f32_e32 v206, v17, v137
	v_fmac_f32_e32 v158, v17, v138
	v_fmac_f32_e32 v159, v15, v140
	v_fmac_f32_e32 v152, v15, v141
	v_fmac_f32_e32 v49, v15, v143
	v_fmac_f32_e32 v156, v17, v140
	v_fmac_f32_e32 v47, v17, v143
	s_waitcnt vmcnt(3)
	v_pk_add_f32 v[10:11], v[10:11], 1.0 op_sel_hi:[1,0]
	v_pk_mul_f32 v[130:131], v[102:103], v[130:131] op_sel_hi:[0,1]
	s_waitcnt vmcnt(2)
	v_pk_mul_f32 v[136:137], v[6:7], v[10:11]
	v_pk_add_f32 v[12:13], v[12:13], 1.0 op_sel_hi:[1,0]
	v_pk_mul_f32 v[14:15], v[102:103], v[128:129] op_sel_hi:[0,1]
	v_pk_fma_f32 v[138:139], v[130:131], v[136:137], v[2:3]
	v_pk_mul_f32 v[128:129], v[104:105], v[132:133] op_sel_hi:[0,1]
	v_pk_mul_f32 v[16:17], v[8:9], v[12:13]
	v_pk_mul_f32 v[130:131], v[104:105], v[134:135] op_sel_hi:[0,1]
	v_pk_fma_f32 v[136:137], v[128:129], v[136:137], v[2:3]
	v_med3_f32 v2, v138, s33, v233
	v_med3_f32 v3, v139, s33, v233
	v_mov_b32_e32 v132, 0
	v_pk_fma_f32 v[14:15], v[14:15], v[16:17], v[4:5]
	v_pk_fma_f32 v[16:17], v[130:131], v[16:17], v[4:5]
	v_cvt_pk_fp8_f32 v132, v2, v3
	v_med3_f32 v4, v136, s33, v233
	v_med3_f32 v5, v137, s33, v233
	v_mov_b32_e32 v133, 0
	v_cvt_pk_fp8_f32 v133, v4, v5
	v_med3_f32 v2, v14, s33, v233
	v_med3_f32 v3, v15, s33, v233
	v_cvt_pk_fp8_f32 v132, v2, v3 op_sel:[0,0,1]
	v_med3_f32 v2, v16, s33, v233
	v_med3_f32 v3, v17, s33, v233
	global_load_dwordx4 v[10:13], v[78:79], off
	global_load_dwordx4 v[6:9], v[80:81], off
	v_cvt_pk_fp8_f32 v133, v2, v3 op_sel:[0,0,1]
	global_load_dwordx4 v[2:5], v[34:35], off
	ds_read_b128 v[128:131], v105 offset:49152
	global_store_dword v[118:119], v132, off offset:768
	global_store_dword v[118:119], v133, off offset:2816
	ds_read_b128 v[132:135], v105 offset:50176
	s_waitcnt lgkmcnt(1)
	v_fmac_f32_e32 v224, v138, v128
	v_fmac_f32_e32 v223, v138, v129
	v_fmac_f32_e32 v221, v138, v130
	v_fmac_f32_e32 v217, v138, v131
	v_fmac_f32_e32 v225, v136, v128
	v_fmac_f32_e32 v222, v136, v129
	v_fmac_f32_e32 v219, v136, v130
	v_fmac_f32_e32 v215, v136, v131
	ds_read_b128 v[128:131], v105 offset:51200
	s_waitcnt lgkmcnt(1)
	v_fmac_f32_e32 v220, v138, v132
	v_fmac_f32_e32 v216, v138, v133
	v_fmac_f32_e32 v213, v138, v134
	v_fmac_f32_e32 v211, v138, v135
	v_fmac_f32_e32 v218, v136, v132
	v_fmac_f32_e32 v214, v136, v133
	v_fmac_f32_e32 v212, v136, v134
	v_fmac_f32_e32 v210, v136, v135
	ds_read_b128 v[132:135], v105 offset:52224
	s_waitcnt lgkmcnt(1)
	v_fmac_f32_e32 v209, v138, v128
	v_fmac_f32_e32 v207, v138, v129
	v_fmac_f32_e32 v205, v138, v130
	v_fmac_f32_e32 v153, v138, v131
	v_fmac_f32_e32 v208, v136, v128
	v_fmac_f32_e32 v206, v136, v129
	v_fmac_f32_e32 v158, v136, v130
	v_fmac_f32_e32 v57, v136, v131
	ds_read_b128 v[128:131], v105 offset:53248
	s_waitcnt lgkmcnt(1)
	v_fmac_f32_e32 v159, v138, v132
	v_fmac_f32_e32 v152, v138, v133
	v_fmac_f32_e32 v53, v138, v134
	v_fmac_f32_e32 v49, v138, v135
	v_fmac_f32_e32 v156, v136, v132
	v_fmac_f32_e32 v55, v136, v133
	v_fmac_f32_e32 v51, v136, v134
	v_fmac_f32_e32 v47, v136, v135
	ds_read_b128 v[132:135], v105 offset:54272
	s_waitcnt lgkmcnt(1)
	v_fmac_f32_e32 v224, v139, v128
	v_fmac_f32_e32 v223, v139, v129
	v_fmac_f32_e32 v221, v139, v130
	v_fmac_f32_e32 v217, v139, v131
	v_fmac_f32_e32 v225, v137, v128
	v_fmac_f32_e32 v222, v137, v129
	v_fmac_f32_e32 v219, v137, v130
	v_fmac_f32_e32 v215, v137, v131
	ds_read_b128 v[128:131], v105 offset:55296
	s_waitcnt lgkmcnt(1)
	v_fmac_f32_e32 v220, v139, v132
	v_fmac_f32_e32 v216, v139, v133
	v_fmac_f32_e32 v213, v139, v134
	v_fmac_f32_e32 v211, v139, v135
	v_fmac_f32_e32 v218, v137, v132
	v_fmac_f32_e32 v214, v137, v133
	v_fmac_f32_e32 v212, v137, v134
	v_fmac_f32_e32 v210, v137, v135
	ds_read_b128 v[132:135], v105 offset:56320
	s_waitcnt lgkmcnt(1)
	v_fmac_f32_e32 v209, v139, v128
	v_fmac_f32_e32 v207, v139, v129
	v_fmac_f32_e32 v205, v139, v130
	v_fmac_f32_e32 v153, v139, v131
	v_fmac_f32_e32 v208, v137, v128
	v_fmac_f32_e32 v206, v137, v129
	v_fmac_f32_e32 v158, v137, v130
	v_fmac_f32_e32 v57, v137, v131
	ds_read_b128 v[128:131], v105 offset:57344
	s_waitcnt lgkmcnt(1)
	v_fmac_f32_e32 v159, v139, v132
	v_fmac_f32_e32 v152, v139, v133
	v_fmac_f32_e32 v53, v139, v134
	v_fmac_f32_e32 v49, v139, v135
	v_fmac_f32_e32 v156, v137, v132
	v_fmac_f32_e32 v55, v137, v133
	v_fmac_f32_e32 v51, v137, v134
	v_fmac_f32_e32 v47, v137, v135
	ds_read_b128 v[132:135], v105 offset:58368
	s_waitcnt lgkmcnt(1)
	v_fmac_f32_e32 v224, v14, v128
	v_fmac_f32_e32 v223, v14, v129
	v_fmac_f32_e32 v221, v14, v130
	v_fmac_f32_e32 v217, v14, v131
	v_fmac_f32_e32 v225, v16, v128
	v_fmac_f32_e32 v222, v16, v129
	v_fmac_f32_e32 v219, v16, v130
	v_fmac_f32_e32 v215, v16, v131
	ds_read_b128 v[128:131], v105 offset:59392
	s_waitcnt lgkmcnt(1)
	v_fmac_f32_e32 v220, v14, v132
	v_fmac_f32_e32 v216, v14, v133
	v_fmac_f32_e32 v213, v14, v134
	v_fmac_f32_e32 v211, v14, v135
	v_fmac_f32_e32 v218, v16, v132
	v_fmac_f32_e32 v214, v16, v133
	v_fmac_f32_e32 v212, v16, v134
	v_fmac_f32_e32 v210, v16, v135
	ds_read_b128 v[132:135], v105 offset:60416
	s_waitcnt lgkmcnt(1)
	v_fmac_f32_e32 v209, v14, v128
	v_fmac_f32_e32 v207, v14, v129
	v_fmac_f32_e32 v205, v14, v130
	v_fmac_f32_e32 v153, v14, v131
	v_fmac_f32_e32 v208, v16, v128
	v_fmac_f32_e32 v206, v16, v129
	v_fmac_f32_e32 v158, v16, v130
	v_fmac_f32_e32 v57, v16, v131
	ds_read_b128 v[128:131], v105 offset:61440
	s_waitcnt lgkmcnt(1)
	v_fmac_f32_e32 v159, v14, v132
	v_fmac_f32_e32 v152, v14, v133
	v_fmac_f32_e32 v53, v14, v134
	v_fmac_f32_e32 v49, v14, v135
	v_fmac_f32_e32 v156, v16, v132
	v_fmac_f32_e32 v55, v16, v133
	v_fmac_f32_e32 v51, v16, v134
	v_fmac_f32_e32 v47, v16, v135
	ds_read_b128 v[132:135], v105 offset:62464
	s_waitcnt lgkmcnt(1)
	v_fmac_f32_e32 v224, v15, v128
	v_fmac_f32_e32 v223, v15, v129
	v_fmac_f32_e32 v221, v15, v130
	v_fmac_f32_e32 v217, v15, v131
	v_fmac_f32_e32 v225, v17, v128
	v_fmac_f32_e32 v222, v17, v129
	v_fmac_f32_e32 v219, v17, v130
	v_fmac_f32_e32 v215, v17, v131
	ds_read_b128 v[128:131], v105 offset:63488
	s_waitcnt lgkmcnt(1)
	v_fmac_f32_e32 v220, v15, v132
	v_fmac_f32_e32 v216, v15, v133
	v_fmac_f32_e32 v213, v15, v134
	v_fmac_f32_e32 v211, v15, v135
	v_fmac_f32_e32 v218, v17, v132
	v_fmac_f32_e32 v214, v17, v133
	v_fmac_f32_e32 v212, v17, v134
	v_fmac_f32_e32 v210, v17, v135
	ds_read_b128 v[132:135], v105 offset:64512
	s_waitcnt lgkmcnt(1)
	v_fmac_f32_e32 v57, v17, v131
	v_fmac_f32_e32 v209, v15, v128
	v_fmac_f32_e32 v207, v15, v129
	v_fmac_f32_e32 v205, v15, v130
	s_waitcnt lgkmcnt(0)
	v_fmac_f32_e32 v53, v15, v134
	v_fmac_f32_e32 v55, v17, v133
	v_fmac_f32_e32 v51, v17, v134
	v_fmac_f32_e32 v153, v15, v131
	v_fmac_f32_e32 v208, v17, v128
	v_fmac_f32_e32 v206, v17, v129
	v_fmac_f32_e32 v158, v17, v130
	v_fmac_f32_e32 v159, v15, v132
	v_fmac_f32_e32 v152, v15, v133
	v_fmac_f32_e32 v49, v15, v135
	v_fmac_f32_e32 v156, v17, v132
	v_fmac_f32_e32 v47, v17, v135
	s_waitcnt vmcnt(3)
	v_pk_add_f32 v[6:7], v[6:7], 1.0 op_sel_hi:[1,0]
	v_pk_mul_f32 v[126:127], v[102:103], v[126:127] op_sel_hi:[0,1]
	s_waitcnt vmcnt(2)
	v_pk_mul_f32 v[128:129], v[2:3], v[6:7]
	v_pk_add_f32 v[8:9], v[8:9], 1.0 op_sel_hi:[1,0]
	v_pk_fma_f32 v[130:131], v[126:127], v[128:129], v[10:11]
	v_pk_mul_f32 v[122:123], v[104:105], v[122:123] op_sel_hi:[0,1]
	v_pk_mul_f32 v[16:17], v[4:5], v[8:9]
	v_pk_mul_f32 v[14:15], v[102:103], v[124:125] op_sel_hi:[0,1]
	v_pk_mul_f32 v[120:121], v[104:105], v[120:121] op_sel_hi:[0,1]
	v_pk_fma_f32 v[128:129], v[122:123], v[128:129], v[10:11]
	v_med3_f32 v10, v130, s33, v233
	v_med3_f32 v11, v131, s33, v233
	v_mov_b32_e32 v124, 0
	v_pk_fma_f32 v[14:15], v[14:15], v[16:17], v[12:13]
	v_pk_fma_f32 v[16:17], v[120:121], v[16:17], v[12:13]
	v_cvt_pk_fp8_f32 v124, v10, v11
	v_med3_f32 v12, v128, s33, v233
	v_med3_f32 v13, v129, s33, v233
	v_mov_b32_e32 v125, 0
	v_cvt_pk_fp8_f32 v125, v12, v13
	v_med3_f32 v10, v14, s33, v233
	v_med3_f32 v11, v15, s33, v233
	v_cvt_pk_fp8_f32 v124, v10, v11 op_sel:[0,0,1]
	v_med3_f32 v10, v16, s33, v233
	v_med3_f32 v11, v17, s33, v233
	global_load_dwordx4 v[6:9], v[82:83], off
	global_load_dwordx4 v[2:5], v[84:85], off
	v_cvt_pk_fp8_f32 v125, v10, v11 op_sel:[0,0,1]
	v_add_u32_e32 v10, 0x10000, v105
	ds_read_b128 v[120:123], v10
	global_load_dwordx4 v[10:13], v[36:37], off
	s_nop 0
	global_store_dword v[118:119], v124, off offset:1024
	global_store_dword v[118:119], v125, off offset:3072
	v_add_u32_e32 v124, 0x10400, v105
	ds_read_b128 v[124:127], v124
	s_waitcnt lgkmcnt(1)
	v_fmac_f32_e32 v224, v130, v120
	v_fmac_f32_e32 v225, v128, v120
	v_add_u32_e32 v120, 0x10800, v105
	v_fmac_f32_e32 v223, v130, v121
	v_fmac_f32_e32 v221, v130, v122
	v_fmac_f32_e32 v217, v130, v123
	v_fmac_f32_e32 v222, v128, v121
	v_fmac_f32_e32 v219, v128, v122
	v_fmac_f32_e32 v215, v128, v123
	ds_read_b128 v[120:123], v120
	s_waitcnt lgkmcnt(1)
	v_fmac_f32_e32 v220, v130, v124
	v_fmac_f32_e32 v218, v128, v124
	v_add_u32_e32 v124, 0x10c00, v105
	v_fmac_f32_e32 v216, v130, v125
	v_fmac_f32_e32 v213, v130, v126
	v_fmac_f32_e32 v211, v130, v127
	v_fmac_f32_e32 v214, v128, v125
	v_fmac_f32_e32 v212, v128, v126
	v_fmac_f32_e32 v210, v128, v127
	ds_read_b128 v[124:127], v124
	s_waitcnt lgkmcnt(1)
	v_fmac_f32_e32 v209, v130, v120
	v_fmac_f32_e32 v208, v128, v120
	v_add_u32_e32 v120, 0x11000, v105
	v_fmac_f32_e32 v207, v130, v121
	v_fmac_f32_e32 v205, v130, v122
	v_fmac_f32_e32 v153, v130, v123
	v_fmac_f32_e32 v206, v128, v121
	v_fmac_f32_e32 v158, v128, v122
	v_fmac_f32_e32 v57, v128, v123
	ds_read_b128 v[120:123], v120
	s_waitcnt lgkmcnt(1)
	v_fmac_f32_e32 v159, v130, v124
	v_fmac_f32_e32 v156, v128, v124
	v_add_u32_e32 v124, 0x11400, v105
	v_fmac_f32_e32 v152, v130, v125
	v_fmac_f32_e32 v53, v130, v126
	v_fmac_f32_e32 v49, v130, v127
	v_fmac_f32_e32 v55, v128, v125
	v_fmac_f32_e32 v51, v128, v126
	v_fmac_f32_e32 v47, v128, v127
	ds_read_b128 v[124:127], v124
	s_waitcnt lgkmcnt(1)
	v_fmac_f32_e32 v224, v131, v120
	v_fmac_f32_e32 v225, v129, v120
	v_add_u32_e32 v120, 0x11800, v105
	v_fmac_f32_e32 v223, v131, v121
	v_fmac_f32_e32 v221, v131, v122
	v_fmac_f32_e32 v217, v131, v123
	v_fmac_f32_e32 v222, v129, v121
	v_fmac_f32_e32 v219, v129, v122
	v_fmac_f32_e32 v215, v129, v123
	ds_read_b128 v[120:123], v120
	s_waitcnt lgkmcnt(1)
	v_fmac_f32_e32 v220, v131, v124
	v_fmac_f32_e32 v218, v129, v124
	v_add_u32_e32 v124, 0x11c00, v105
	v_fmac_f32_e32 v216, v131, v125
	v_fmac_f32_e32 v213, v131, v126
	v_fmac_f32_e32 v211, v131, v127
	v_fmac_f32_e32 v214, v129, v125
	v_fmac_f32_e32 v212, v129, v126
	v_fmac_f32_e32 v210, v129, v127
	ds_read_b128 v[124:127], v124
	s_waitcnt lgkmcnt(1)
	v_fmac_f32_e32 v209, v131, v120
	v_fmac_f32_e32 v208, v129, v120
	v_add_u32_e32 v120, 0x12000, v105
	v_fmac_f32_e32 v207, v131, v121
	v_fmac_f32_e32 v205, v131, v122
	v_fmac_f32_e32 v153, v131, v123
	v_fmac_f32_e32 v206, v129, v121
	v_fmac_f32_e32 v158, v129, v122
	v_fmac_f32_e32 v57, v129, v123
	ds_read_b128 v[120:123], v120
	s_waitcnt lgkmcnt(1)
	v_fmac_f32_e32 v159, v131, v124
	v_fmac_f32_e32 v156, v129, v124
	v_add_u32_e32 v124, 0x12400, v105
	v_fmac_f32_e32 v152, v131, v125
	v_fmac_f32_e32 v53, v131, v126
	v_fmac_f32_e32 v49, v131, v127
	v_fmac_f32_e32 v55, v129, v125
	v_fmac_f32_e32 v51, v129, v126
	v_fmac_f32_e32 v47, v129, v127
	ds_read_b128 v[124:127], v124
	s_waitcnt lgkmcnt(1)
	v_fmac_f32_e32 v224, v14, v120
	v_fmac_f32_e32 v225, v16, v120
	v_add_u32_e32 v120, 0x12800, v105
	v_fmac_f32_e32 v223, v14, v121
	v_fmac_f32_e32 v221, v14, v122
	v_fmac_f32_e32 v217, v14, v123
	v_fmac_f32_e32 v222, v16, v121
	v_fmac_f32_e32 v219, v16, v122
	v_fmac_f32_e32 v215, v16, v123
	ds_read_b128 v[120:123], v120
	s_waitcnt lgkmcnt(1)
	v_fmac_f32_e32 v220, v14, v124
	v_fmac_f32_e32 v218, v16, v124
	v_add_u32_e32 v124, 0x12c00, v105
	v_fmac_f32_e32 v216, v14, v125
	v_fmac_f32_e32 v213, v14, v126
	v_fmac_f32_e32 v211, v14, v127
	v_fmac_f32_e32 v214, v16, v125
	v_fmac_f32_e32 v212, v16, v126
	v_fmac_f32_e32 v210, v16, v127
	ds_read_b128 v[124:127], v124
	s_waitcnt lgkmcnt(1)
	v_fmac_f32_e32 v209, v14, v120
	v_fmac_f32_e32 v207, v14, v121
	v_fmac_f32_e32 v205, v14, v122
	v_fmac_f32_e32 v153, v14, v123
	s_waitcnt lgkmcnt(0)
	v_fmac_f32_e32 v159, v14, v124
	v_fmac_f32_e32 v152, v14, v125
	v_fmac_f32_e32 v53, v14, v126
	v_fmac_f32_e32 v49, v14, v127
	v_add_u32_e32 v14, 0x13000, v105
	v_fmac_f32_e32 v208, v16, v120
	v_fmac_f32_e32 v206, v16, v121
	v_fmac_f32_e32 v158, v16, v122
	v_fmac_f32_e32 v57, v16, v123
	ds_read_b128 v[120:123], v14
	v_add_u32_e32 v14, 0x13400, v105
	v_fmac_f32_e32 v156, v16, v124
	v_fmac_f32_e32 v55, v16, v125
	v_fmac_f32_e32 v51, v16, v126
	v_fmac_f32_e32 v47, v16, v127
	ds_read_b128 v[124:127], v14
	v_add_u32_e32 v14, 0x13800, v105
	s_waitcnt lgkmcnt(1)
	v_fmac_f32_e32 v224, v15, v120
	v_fmac_f32_e32 v223, v15, v121
	v_fmac_f32_e32 v221, v15, v122
	v_fmac_f32_e32 v217, v15, v123
	v_fmac_f32_e32 v225, v17, v120
	v_fmac_f32_e32 v222, v17, v121
	v_fmac_f32_e32 v219, v17, v122
	v_fmac_f32_e32 v215, v17, v123
	ds_read_b128 v[120:123], v14
	v_add_u32_e32 v14, 0x13c00, v105
	s_waitcnt lgkmcnt(1)
	v_fmac_f32_e32 v220, v15, v124
	v_fmac_f32_e32 v216, v15, v125
	v_fmac_f32_e32 v213, v15, v126
	v_fmac_f32_e32 v211, v15, v127
	v_fmac_f32_e32 v218, v17, v124
	v_fmac_f32_e32 v214, v17, v125
	v_fmac_f32_e32 v212, v17, v126
	v_fmac_f32_e32 v210, v17, v127
	ds_read_b128 v[124:127], v14
	s_waitcnt lgkmcnt(1)
	v_fmac_f32_e32 v57, v17, v123
	v_fmac_f32_e32 v209, v15, v120
	v_fmac_f32_e32 v207, v15, v121
	v_fmac_f32_e32 v205, v15, v122
	s_waitcnt lgkmcnt(0)
	v_fmac_f32_e32 v53, v15, v126
	v_fmac_f32_e32 v55, v17, v125
	v_fmac_f32_e32 v51, v17, v126
	v_fmac_f32_e32 v153, v15, v123
	v_fmac_f32_e32 v208, v17, v120
	v_fmac_f32_e32 v206, v17, v121
	v_fmac_f32_e32 v158, v17, v122
	v_fmac_f32_e32 v159, v15, v124
	v_fmac_f32_e32 v152, v15, v125
	v_fmac_f32_e32 v49, v15, v127
	v_fmac_f32_e32 v156, v17, v124
	v_fmac_f32_e32 v47, v17, v127
	s_waitcnt vmcnt(3)
	v_pk_add_f32 v[2:3], v[2:3], 1.0 op_sel_hi:[1,0]
	v_pk_mul_f32 v[116:117], v[102:103], v[116:117] op_sel_hi:[0,1]
	s_waitcnt vmcnt(2)
	v_pk_mul_f32 v[120:121], v[10:11], v[2:3]
	v_pk_add_f32 v[4:5], v[4:5], 1.0 op_sel_hi:[1,0]
	v_pk_fma_f32 v[122:123], v[116:117], v[120:121], v[6:7]
	v_pk_mul_f32 v[112:113], v[104:105], v[112:113] op_sel_hi:[0,1]
	v_pk_mul_f32 v[16:17], v[12:13], v[4:5]
	v_pk_mul_f32 v[14:15], v[102:103], v[114:115] op_sel_hi:[0,1]
	v_pk_mul_f32 v[110:111], v[104:105], v[110:111] op_sel_hi:[0,1]
	v_pk_fma_f32 v[120:121], v[112:113], v[120:121], v[6:7]
	v_med3_f32 v6, v122, s33, v233
	v_med3_f32 v7, v123, s33, v233
	v_mov_b32_e32 v114, 0
	v_pk_fma_f32 v[14:15], v[14:15], v[16:17], v[8:9]
	v_pk_fma_f32 v[16:17], v[110:111], v[16:17], v[8:9]
	v_cvt_pk_fp8_f32 v114, v6, v7
	v_med3_f32 v8, v120, s33, v233
	v_med3_f32 v9, v121, s33, v233
	v_mov_b32_e32 v115, 0
	v_cvt_pk_fp8_f32 v115, v8, v9
	v_med3_f32 v6, v14, s33, v233
	v_med3_f32 v7, v15, s33, v233
	v_cvt_pk_fp8_f32 v114, v6, v7 op_sel:[0,0,1]
	v_med3_f32 v6, v16, s33, v233
	v_med3_f32 v7, v17, s33, v233
	v_cvt_pk_fp8_f32 v115, v6, v7 op_sel:[0,0,1]
	v_add_u32_e32 v6, 0x14000, v105
	global_load_dwordx4 v[2:5], v[86:87], off
	global_load_dwordx4 v[10:13], v[88:89], off
	ds_read_b128 v[110:113], v6
	global_load_dwordx4 v[6:9], v[38:39], off
	s_nop 0
	global_store_dword v[118:119], v114, off offset:1280
	global_store_dword v[118:119], v115, off offset:3328
	v_add_u32_e32 v114, 0x14400, v105
	ds_read_b128 v[114:117], v114
	s_waitcnt lgkmcnt(1)
	v_fmac_f32_e32 v224, v122, v110
	v_fmac_f32_e32 v225, v120, v110
	v_add_u32_e32 v110, 0x14800, v105
	v_fmac_f32_e32 v223, v122, v111
	v_fmac_f32_e32 v221, v122, v112
	v_fmac_f32_e32 v217, v122, v113
	v_fmac_f32_e32 v222, v120, v111
	v_fmac_f32_e32 v219, v120, v112
	v_fmac_f32_e32 v215, v120, v113
	ds_read_b128 v[110:113], v110
	s_waitcnt lgkmcnt(1)
	v_fmac_f32_e32 v220, v122, v114
	v_fmac_f32_e32 v218, v120, v114
	v_add_u32_e32 v114, 0x14c00, v105
	v_fmac_f32_e32 v216, v122, v115
	v_fmac_f32_e32 v213, v122, v116
	v_fmac_f32_e32 v211, v122, v117
	v_fmac_f32_e32 v214, v120, v115
	v_fmac_f32_e32 v212, v120, v116
	v_fmac_f32_e32 v210, v120, v117
	ds_read_b128 v[114:117], v114
	s_waitcnt lgkmcnt(1)
	v_fmac_f32_e32 v209, v122, v110
	v_fmac_f32_e32 v208, v120, v110
	v_add_u32_e32 v110, 0x15000, v105
	v_fmac_f32_e32 v207, v122, v111
	v_fmac_f32_e32 v205, v122, v112
	v_fmac_f32_e32 v153, v122, v113
	v_fmac_f32_e32 v206, v120, v111
	v_fmac_f32_e32 v158, v120, v112
	v_fmac_f32_e32 v57, v120, v113
	ds_read_b128 v[110:113], v110
	s_waitcnt lgkmcnt(1)
	v_fmac_f32_e32 v159, v122, v114
	v_fmac_f32_e32 v152, v122, v115
	v_fmac_f32_e32 v53, v122, v116
	v_fmac_f32_e32 v49, v122, v117
	v_fmac_f32_e32 v156, v120, v114
	v_fmac_f32_e32 v55, v120, v115
	v_fmac_f32_e32 v51, v120, v116
	v_fmac_f32_e32 v47, v120, v117
	ds_read_b128 v[114:117], v230
	s_waitcnt lgkmcnt(1)
	v_fmac_f32_e32 v224, v123, v110
	v_fmac_f32_e32 v223, v123, v111
	v_fmac_f32_e32 v221, v123, v112
	v_fmac_f32_e32 v217, v123, v113
	v_fmac_f32_e32 v225, v121, v110
	v_fmac_f32_e32 v222, v121, v111
	v_fmac_f32_e32 v219, v121, v112
	v_fmac_f32_e32 v215, v121, v113
	ds_read_b128 v[110:113], v250
	s_waitcnt lgkmcnt(1)
	v_fmac_f32_e32 v220, v123, v114
	v_fmac_f32_e32 v216, v123, v115
	v_fmac_f32_e32 v213, v123, v116
	v_fmac_f32_e32 v211, v123, v117
	v_fmac_f32_e32 v218, v121, v114
	v_fmac_f32_e32 v214, v121, v115
	v_fmac_f32_e32 v212, v121, v116
	v_fmac_f32_e32 v210, v121, v117
	ds_read_b128 v[114:117], v251
	s_waitcnt lgkmcnt(1)
	v_fmac_f32_e32 v209, v123, v110
	v_fmac_f32_e32 v207, v123, v111
	v_fmac_f32_e32 v205, v123, v112
	v_fmac_f32_e32 v153, v123, v113
	v_fmac_f32_e32 v208, v121, v110
	v_fmac_f32_e32 v206, v121, v111
	v_fmac_f32_e32 v158, v121, v112
	v_fmac_f32_e32 v57, v121, v113
	s_waitcnt lgkmcnt(0)
	v_fmac_f32_e32 v159, v123, v114
	v_fmac_f32_e32 v152, v123, v115
	v_fmac_f32_e32 v53, v123, v116
	v_fmac_f32_e32 v49, v123, v117
	v_fmac_f32_e32 v156, v121, v114
	ds_read_b128 v[110:113], v164
	v_fmac_f32_e32 v55, v121, v115
	v_fmac_f32_e32 v51, v121, v116
	v_fmac_f32_e32 v47, v121, v117
	ds_read_b128 v[114:117], v165
	s_waitcnt lgkmcnt(1)
	v_fmac_f32_e32 v224, v14, v110
	v_fmac_f32_e32 v223, v14, v111
	v_fmac_f32_e32 v221, v14, v112
	v_fmac_f32_e32 v217, v14, v113
	v_fmac_f32_e32 v225, v16, v110
	v_fmac_f32_e32 v222, v16, v111
	v_fmac_f32_e32 v219, v16, v112
	v_fmac_f32_e32 v215, v16, v113
	s_waitcnt lgkmcnt(0)
	v_fmac_f32_e32 v220, v14, v114
	v_fmac_f32_e32 v216, v14, v115
	v_fmac_f32_e32 v213, v14, v116
	v_fmac_f32_e32 v211, v14, v117
	v_fmac_f32_e32 v218, v16, v114
	ds_read_b128 v[110:113], v166
	v_fmac_f32_e32 v214, v16, v115
	v_fmac_f32_e32 v212, v16, v116
	v_fmac_f32_e32 v210, v16, v117
	ds_read_b128 v[114:117], v167
	s_waitcnt lgkmcnt(1)
	v_fmac_f32_e32 v209, v14, v110
	v_fmac_f32_e32 v207, v14, v111
	v_fmac_f32_e32 v205, v14, v112
	v_fmac_f32_e32 v153, v14, v113
	v_fmac_f32_e32 v208, v16, v110
	v_fmac_f32_e32 v206, v16, v111
	v_fmac_f32_e32 v158, v16, v112
	v_fmac_f32_e32 v57, v16, v113
	s_waitcnt lgkmcnt(0)
	v_fmac_f32_e32 v159, v14, v114
	v_fmac_f32_e32 v152, v14, v115
	v_fmac_f32_e32 v53, v14, v116
	v_fmac_f32_e32 v49, v14, v117
	v_fmac_f32_e32 v156, v16, v114
	ds_read_b128 v[110:113], v168
	v_fmac_f32_e32 v55, v16, v115
	v_fmac_f32_e32 v51, v16, v116
	v_fmac_f32_e32 v47, v16, v117
	ds_read_b128 v[114:117], v169
	s_waitcnt lgkmcnt(1)
	v_fmac_f32_e32 v224, v15, v110
	v_fmac_f32_e32 v223, v15, v111
	v_fmac_f32_e32 v221, v15, v112
	v_fmac_f32_e32 v217, v15, v113
	v_fmac_f32_e32 v225, v17, v110
	v_fmac_f32_e32 v222, v17, v111
	v_fmac_f32_e32 v219, v17, v112
	v_fmac_f32_e32 v215, v17, v113
	s_waitcnt lgkmcnt(0)
	v_fmac_f32_e32 v220, v15, v114
	v_fmac_f32_e32 v216, v15, v115
	v_fmac_f32_e32 v213, v15, v116
	v_fmac_f32_e32 v211, v15, v117
	v_fmac_f32_e32 v218, v17, v114
	ds_read_b128 v[110:113], v170
	v_fmac_f32_e32 v214, v17, v115
	v_fmac_f32_e32 v212, v17, v116
	v_fmac_f32_e32 v210, v17, v117
	ds_read_b128 v[114:117], v171
	s_waitcnt lgkmcnt(1)
	v_fmac_f32_e32 v57, v17, v113
	v_fmac_f32_e32 v209, v15, v110
	v_fmac_f32_e32 v207, v15, v111
	v_fmac_f32_e32 v205, v15, v112
	s_waitcnt lgkmcnt(0)
	v_fmac_f32_e32 v53, v15, v116
	v_fmac_f32_e32 v55, v17, v115
	v_fmac_f32_e32 v51, v17, v116
	v_fmac_f32_e32 v153, v15, v113
	v_fmac_f32_e32 v208, v17, v110
	v_fmac_f32_e32 v206, v17, v111
	v_fmac_f32_e32 v158, v17, v112
	v_fmac_f32_e32 v159, v15, v114
	v_fmac_f32_e32 v152, v15, v115
	v_fmac_f32_e32 v49, v15, v117
	v_fmac_f32_e32 v156, v17, v114
	v_fmac_f32_e32 v47, v17, v117
	s_waitcnt vmcnt(3)
	v_pk_add_f32 v[12:13], v[12:13], 1.0 op_sel_hi:[1,0]
	v_pk_add_f32 v[10:11], v[10:11], 1.0 op_sel_hi:[1,0]
	s_waitcnt vmcnt(2)
	v_pk_mul_f32 v[12:13], v[8:9], v[12:13]
	v_pk_mul_f32 v[10:11], v[6:7], v[10:11]
	global_load_dwordx4 v[6:9], v[90:91], off
	global_load_dwordx4 v[114:117], v[92:93], off
	global_load_dwordx4 v[120:123], v[40:41], off
	v_pk_mul_f32 v[14:15], v[102:103], v[108:109] op_sel_hi:[0,1]
	v_pk_mul_f32 v[16:17], v[102:103], v[106:107] op_sel_hi:[0,1]
	v_pk_fma_f32 v[106:107], v[16:17], v[12:13], v[4:5]
	v_pk_fma_f32 v[108:109], v[14:15], v[10:11], v[2:3]
	v_pk_mul_f32 v[14:15], v[104:105], v[20:21] op_sel_hi:[0,1]
	v_pk_mul_f32 v[16:17], v[104:105], v[18:19] op_sel_hi:[0,1]
	v_pk_fma_f32 v[110:111], v[16:17], v[12:13], v[4:5]
	v_pk_fma_f32 v[112:113], v[14:15], v[10:11], v[2:3]
	v_med3_f32 v2, v108, s33, v233
	v_med3_f32 v3, v109, s33, v233
	v_mov_b32_e32 v4, 0
	v_cvt_pk_fp8_f32 v4, v2, v3
	v_med3_f32 v2, v106, s33, v233
	v_med3_f32 v3, v107, s33, v233
	v_cvt_pk_fp8_f32 v4, v2, v3 op_sel:[0,0,1]
	v_med3_f32 v2, v112, s33, v233
	v_med3_f32 v3, v113, s33, v233
	global_store_dword v[118:119], v4, off offset:1536
	v_mov_b32_e32 v4, 0
	v_cvt_pk_fp8_f32 v4, v2, v3
	v_med3_f32 v2, v110, s33, v233
	v_med3_f32 v3, v111, s33, v233
	v_cvt_pk_fp8_f32 v4, v2, v3 op_sel:[0,0,1]
	global_store_dword v[118:119], v4, off offset:3584
	ds_read_b128 v[10:13], v172
	ds_read_b128 v[124:127], v173
	ds_read_b128 v[128:131], v174
	ds_read_b128 v[132:135], v175
	ds_read_b128 v[14:17], v176
	ds_read_b128 v[136:139], v177
	ds_read_b128 v[140:143], v178
	ds_read_b128 v[144:147], v179
	ds_read_b128 v[18:21], v180
	ds_read_b128 v[148:151], v181
	ds_read_b128 v[238:241], v182
	ds_read_b128 v[242:245], v183
	ds_read_b128 v[2:5], v184
	ds_read_b128 v[246:249], v185
	ds_read_b128 v[234:237], v186
	ds_read_b128 v[160:163], v187
	s_waitcnt vmcnt(3)
	v_pk_add_f32 v[116:117], v[116:117], 1.0 op_sel_hi:[1,0]
	v_pk_add_f32 v[154:155], v[114:115], 1.0 op_sel_hi:[1,0]
	s_waitcnt lgkmcnt(14)
	v_fmac_f32_e32 v215, v112, v13
	v_fmac_f32_e32 v219, v112, v12
	v_fmac_f32_e32 v222, v112, v11
	v_fmac_f32_e32 v225, v112, v10
	v_fmac_f32_e32 v217, v108, v13
	v_fmac_f32_e32 v221, v108, v12
	v_fmac_f32_e32 v223, v108, v11
	v_fmac_f32_e32 v224, v108, v10
	s_waitcnt vmcnt(2)
	v_pk_mul_f32 v[114:115], v[122:123], v[116:117]
	v_pk_mul_f32 v[116:117], v[120:121], v[154:155]
	s_waitcnt lgkmcnt(11)
	v_fmac_f32_e32 v215, v113, v17
	v_fmac_f32_e32 v219, v113, v16
	v_fmac_f32_e32 v222, v113, v15
	v_fmac_f32_e32 v225, v113, v14
	v_fmac_f32_e32 v217, v109, v17
	v_fmac_f32_e32 v221, v109, v16
	v_fmac_f32_e32 v223, v109, v15
	v_fmac_f32_e32 v224, v109, v14
	v_pk_mul_f32 v[10:11], v[102:103], v[100:101] op_sel_hi:[0,1]
	s_waitcnt lgkmcnt(7)
	v_fmac_f32_e32 v215, v110, v21
	v_fmac_f32_e32 v219, v110, v20
	v_fmac_f32_e32 v222, v110, v19
	v_fmac_f32_e32 v225, v110, v18
	v_fmac_f32_e32 v217, v106, v21
	v_fmac_f32_e32 v221, v106, v20
	v_fmac_f32_e32 v223, v106, v19
	v_fmac_f32_e32 v224, v106, v18
	v_pk_fma_f32 v[18:19], v[10:11], v[116:117], v[6:7]
	v_pk_mul_f32 v[10:11], v[104:105], v[96:97] op_sel_hi:[0,1]
	s_waitcnt lgkmcnt(3)
	v_fmac_f32_e32 v215, v111, v5
	v_fmac_f32_e32 v219, v111, v4
	v_fmac_f32_e32 v222, v111, v3
	v_fmac_f32_e32 v217, v107, v5
	v_fmac_f32_e32 v221, v107, v4
	v_fmac_f32_e32 v223, v107, v3
	v_pk_mul_f32 v[4:5], v[102:103], v[98:99] op_sel_hi:[0,1]
	v_pk_mul_f32 v[12:13], v[104:105], v[94:95] op_sel_hi:[0,1]
	v_pk_fma_f32 v[6:7], v[10:11], v[116:117], v[6:7]
	v_med3_f32 v3, v18, s33, v233
	v_med3_f32 v10, v19, s33, v233
	v_mov_b32_e32 v14, 0
	v_pk_fma_f32 v[4:5], v[4:5], v[114:115], v[8:9]
	v_pk_fma_f32 v[8:9], v[12:13], v[114:115], v[8:9]
	v_cvt_pk_fp8_f32 v14, v3, v10
	v_med3_f32 v11, v6, s33, v233
	v_med3_f32 v12, v7, s33, v233
	v_mov_b32_e32 v15, 0
	v_cvt_pk_fp8_f32 v15, v11, v12
	v_med3_f32 v3, v4, s33, v233
	v_med3_f32 v10, v5, s33, v233
	v_cvt_pk_fp8_f32 v14, v3, v10 op_sel:[0,0,1]
	v_med3_f32 v3, v8, s33, v233
	v_med3_f32 v10, v9, s33, v233
	v_cvt_pk_fp8_f32 v15, v3, v10 op_sel:[0,0,1]
	ds_read_b128 v[10:13], v188
	global_store_dword v[118:119], v14, off offset:1792
	global_store_dword v[118:119], v15, off offset:3840
	ds_read_b128 v[14:17], v189
	v_fmac_f32_e32 v210, v112, v127
	v_fmac_f32_e32 v212, v112, v126
	v_fmac_f32_e32 v214, v112, v125
	v_fmac_f32_e32 v218, v112, v124
	v_fmac_f32_e32 v211, v108, v127
	v_fmac_f32_e32 v213, v108, v126
	v_fmac_f32_e32 v216, v108, v125
	v_fmac_f32_e32 v220, v108, v124
	v_fmac_f32_e32 v210, v113, v139
	v_fmac_f32_e32 v212, v113, v138
	v_fmac_f32_e32 v214, v113, v137
	v_fmac_f32_e32 v218, v113, v136
	v_fmac_f32_e32 v211, v109, v139
	v_fmac_f32_e32 v213, v109, v138
	v_fmac_f32_e32 v216, v109, v137
	v_fmac_f32_e32 v220, v109, v136
	v_fmac_f32_e32 v210, v110, v151
	v_fmac_f32_e32 v212, v110, v150
	v_fmac_f32_e32 v214, v110, v149
	v_fmac_f32_e32 v218, v110, v148
	v_fmac_f32_e32 v211, v106, v151
	v_fmac_f32_e32 v213, v106, v150
	v_fmac_f32_e32 v216, v106, v149
	v_fmac_f32_e32 v220, v106, v148
	s_waitcnt lgkmcnt(4)
	v_fmac_f32_e32 v210, v111, v249
	v_fmac_f32_e32 v212, v111, v248
	v_fmac_f32_e32 v214, v111, v247
	v_fmac_f32_e32 v218, v111, v246
	v_fmac_f32_e32 v211, v107, v249
	v_fmac_f32_e32 v213, v107, v248
	v_fmac_f32_e32 v216, v107, v247
	v_fmac_f32_e32 v220, v107, v246
	v_fmac_f32_e32 v225, v111, v2
	v_fmac_f32_e32 v224, v107, v2
	s_waitcnt lgkmcnt(1)
	v_fmac_f32_e32 v224, v18, v10
	v_fmac_f32_e32 v223, v18, v11
	v_fmac_f32_e32 v221, v18, v12
	v_fmac_f32_e32 v217, v18, v13
	v_fmac_f32_e32 v225, v6, v10
	v_fmac_f32_e32 v222, v6, v11
	v_fmac_f32_e32 v219, v6, v12
	v_fmac_f32_e32 v215, v6, v13
	ds_read_b128 v[10:13], v190
	s_waitcnt lgkmcnt(1)
	v_fmac_f32_e32 v220, v18, v14
	v_fmac_f32_e32 v216, v18, v15
	v_fmac_f32_e32 v213, v18, v16
	v_fmac_f32_e32 v211, v18, v17
	v_fmac_f32_e32 v218, v6, v14
	v_fmac_f32_e32 v214, v6, v15
	v_fmac_f32_e32 v212, v6, v16
	v_fmac_f32_e32 v210, v6, v17
	ds_read_b128 v[14:17], v191
	v_fmac_f32_e32 v47, v112, v135
	v_fmac_f32_e32 v51, v112, v134
	v_fmac_f32_e32 v55, v112, v133
	v_fmac_f32_e32 v156, v112, v132
	v_fmac_f32_e32 v49, v108, v135
	v_fmac_f32_e32 v53, v108, v134
	v_fmac_f32_e32 v152, v108, v133
	v_fmac_f32_e32 v159, v108, v132
	v_fmac_f32_e32 v57, v112, v131
	v_fmac_f32_e32 v158, v112, v130
	v_fmac_f32_e32 v206, v112, v129
	v_fmac_f32_e32 v208, v112, v128
	v_fmac_f32_e32 v153, v108, v131
	v_fmac_f32_e32 v205, v108, v130
	v_fmac_f32_e32 v207, v108, v129
	v_fmac_f32_e32 v209, v108, v128
	v_fmac_f32_e32 v47, v113, v147
	v_fmac_f32_e32 v51, v113, v146
	v_fmac_f32_e32 v55, v113, v145
	v_fmac_f32_e32 v156, v113, v144
	v_fmac_f32_e32 v49, v109, v147
	v_fmac_f32_e32 v53, v109, v146
	v_fmac_f32_e32 v152, v109, v145
	v_fmac_f32_e32 v159, v109, v144
	v_fmac_f32_e32 v57, v113, v143
	v_fmac_f32_e32 v158, v113, v142
	v_fmac_f32_e32 v206, v113, v141
	v_fmac_f32_e32 v208, v113, v140
	v_fmac_f32_e32 v153, v109, v143
	v_fmac_f32_e32 v205, v109, v142
	v_fmac_f32_e32 v207, v109, v141
	v_fmac_f32_e32 v209, v109, v140
	v_fmac_f32_e32 v47, v110, v245
	v_fmac_f32_e32 v51, v110, v244
	v_fmac_f32_e32 v55, v110, v243
	v_fmac_f32_e32 v156, v110, v242
	v_fmac_f32_e32 v49, v106, v245
	v_fmac_f32_e32 v53, v106, v244
	v_fmac_f32_e32 v152, v106, v243
	v_fmac_f32_e32 v159, v106, v242
	v_fmac_f32_e32 v57, v110, v241
	v_fmac_f32_e32 v158, v110, v240
	v_fmac_f32_e32 v206, v110, v239
	v_fmac_f32_e32 v208, v110, v238
	v_fmac_f32_e32 v153, v106, v241
	v_fmac_f32_e32 v205, v106, v240
	v_fmac_f32_e32 v207, v106, v239
	v_fmac_f32_e32 v209, v106, v238
	v_fmac_f32_e32 v47, v111, v163
	v_fmac_f32_e32 v51, v111, v162
	v_fmac_f32_e32 v55, v111, v161
	v_fmac_f32_e32 v156, v111, v160
	v_fmac_f32_e32 v49, v107, v163
	v_fmac_f32_e32 v53, v107, v162
	v_fmac_f32_e32 v152, v107, v161
	v_fmac_f32_e32 v159, v107, v160
	v_fmac_f32_e32 v57, v111, v237
	v_fmac_f32_e32 v158, v111, v236
	v_fmac_f32_e32 v206, v111, v235
	v_fmac_f32_e32 v208, v111, v234
	v_fmac_f32_e32 v153, v107, v237
	v_fmac_f32_e32 v205, v107, v236
	v_fmac_f32_e32 v207, v107, v235
	v_fmac_f32_e32 v209, v107, v234
	s_waitcnt lgkmcnt(1)
	v_fmac_f32_e32 v209, v18, v10
	v_fmac_f32_e32 v207, v18, v11
	v_fmac_f32_e32 v205, v18, v12
	v_fmac_f32_e32 v153, v18, v13
	v_fmac_f32_e32 v208, v6, v10
	v_fmac_f32_e32 v206, v6, v11
	v_fmac_f32_e32 v158, v6, v12
	v_fmac_f32_e32 v57, v6, v13
	ds_read_b128 v[10:13], v192
	s_waitcnt lgkmcnt(1)
	v_fmac_f32_e32 v159, v18, v14
	v_fmac_f32_e32 v152, v18, v15
	v_fmac_f32_e32 v53, v18, v16
	v_fmac_f32_e32 v49, v18, v17
	v_fmac_f32_e32 v156, v6, v14
	v_fmac_f32_e32 v55, v6, v15
	v_fmac_f32_e32 v51, v6, v16
	v_fmac_f32_e32 v47, v6, v17
	ds_read_b128 v[14:17], v193
	s_waitcnt lgkmcnt(1)
	v_fmac_f32_e32 v224, v19, v10
	v_fmac_f32_e32 v223, v19, v11
	v_fmac_f32_e32 v221, v19, v12
	v_fmac_f32_e32 v217, v19, v13
	v_fmac_f32_e32 v225, v7, v10
	v_fmac_f32_e32 v222, v7, v11
	v_fmac_f32_e32 v219, v7, v12
	v_fmac_f32_e32 v215, v7, v13
	ds_read_b128 v[10:13], v194
	s_waitcnt lgkmcnt(1)
	v_fmac_f32_e32 v220, v19, v14
	v_fmac_f32_e32 v216, v19, v15
	v_fmac_f32_e32 v213, v19, v16
	v_fmac_f32_e32 v211, v19, v17
	v_fmac_f32_e32 v218, v7, v14
	v_fmac_f32_e32 v214, v7, v15
	v_fmac_f32_e32 v212, v7, v16
	v_fmac_f32_e32 v210, v7, v17
	ds_read_b128 v[14:17], v195
	s_waitcnt lgkmcnt(1)
	v_fmac_f32_e32 v209, v19, v10
	v_fmac_f32_e32 v207, v19, v11
	v_fmac_f32_e32 v205, v19, v12
	v_fmac_f32_e32 v153, v19, v13
	v_fmac_f32_e32 v208, v7, v10
	v_fmac_f32_e32 v206, v7, v11
	v_fmac_f32_e32 v158, v7, v12
	v_fmac_f32_e32 v57, v7, v13
	ds_read_b128 v[10:13], v196
	s_waitcnt lgkmcnt(1)
	v_fmac_f32_e32 v159, v19, v14
	v_fmac_f32_e32 v152, v19, v15
	v_fmac_f32_e32 v53, v19, v16
	v_fmac_f32_e32 v49, v19, v17
	v_fmac_f32_e32 v156, v7, v14
	v_fmac_f32_e32 v55, v7, v15
	v_fmac_f32_e32 v51, v7, v16
	v_fmac_f32_e32 v47, v7, v17
	ds_read_b128 v[14:17], v197
	s_waitcnt lgkmcnt(1)
	v_fmac_f32_e32 v224, v4, v10
	v_fmac_f32_e32 v223, v4, v11
	v_fmac_f32_e32 v221, v4, v12
	v_fmac_f32_e32 v217, v4, v13
	v_fmac_f32_e32 v225, v8, v10
	v_fmac_f32_e32 v222, v8, v11
	v_fmac_f32_e32 v219, v8, v12
	v_fmac_f32_e32 v215, v8, v13
	ds_read_b128 v[10:13], v198
	s_waitcnt lgkmcnt(1)
	v_fmac_f32_e32 v220, v4, v14
	v_fmac_f32_e32 v216, v4, v15
	v_fmac_f32_e32 v213, v4, v16
	v_fmac_f32_e32 v211, v4, v17
	v_fmac_f32_e32 v218, v8, v14
	v_fmac_f32_e32 v214, v8, v15
	v_fmac_f32_e32 v212, v8, v16
	v_fmac_f32_e32 v210, v8, v17
	ds_read_b128 v[14:17], v199
	s_waitcnt lgkmcnt(1)
	v_fmac_f32_e32 v209, v4, v10
	v_fmac_f32_e32 v207, v4, v11
	v_fmac_f32_e32 v205, v4, v12
	v_fmac_f32_e32 v153, v4, v13
	v_fmac_f32_e32 v208, v8, v10
	v_fmac_f32_e32 v206, v8, v11
	v_fmac_f32_e32 v158, v8, v12
	v_fmac_f32_e32 v57, v8, v13
	ds_read_b128 v[10:13], v200
	s_waitcnt lgkmcnt(1)
	v_fmac_f32_e32 v159, v4, v14
	v_fmac_f32_e32 v152, v4, v15
	v_fmac_f32_e32 v53, v4, v16
	v_fmac_f32_e32 v49, v4, v17
	v_fmac_f32_e32 v156, v8, v14
	v_fmac_f32_e32 v55, v8, v15
	v_fmac_f32_e32 v51, v8, v16
	v_fmac_f32_e32 v47, v8, v17
	ds_read_b128 v[14:17], v201
	s_waitcnt lgkmcnt(1)
	v_fmac_f32_e32 v224, v5, v10
	v_fmac_f32_e32 v223, v5, v11
	v_fmac_f32_e32 v221, v5, v12
	v_fmac_f32_e32 v217, v5, v13
	v_fmac_f32_e32 v225, v9, v10
	v_fmac_f32_e32 v222, v9, v11
	v_fmac_f32_e32 v219, v9, v12
	v_fmac_f32_e32 v215, v9, v13
	ds_read_b128 v[10:13], v202
	s_waitcnt lgkmcnt(1)
	v_fmac_f32_e32 v220, v5, v14
	v_fmac_f32_e32 v216, v5, v15
	v_fmac_f32_e32 v213, v5, v16
	v_fmac_f32_e32 v211, v5, v17
	v_fmac_f32_e32 v218, v9, v14
	v_fmac_f32_e32 v214, v9, v15
	v_fmac_f32_e32 v212, v9, v16
	v_fmac_f32_e32 v210, v9, v17
	ds_read_b128 v[14:17], v203
	s_waitcnt lgkmcnt(1)
	v_fmac_f32_e32 v57, v9, v13
	v_fmac_f32_e32 v209, v5, v10
	v_fmac_f32_e32 v207, v5, v11
	v_fmac_f32_e32 v205, v5, v12
	s_waitcnt lgkmcnt(0)
	v_fmac_f32_e32 v53, v5, v16
	v_fmac_f32_e32 v55, v9, v15
	v_fmac_f32_e32 v51, v9, v16
	v_fmac_f32_e32 v153, v5, v13
	v_fmac_f32_e32 v208, v9, v10
	v_fmac_f32_e32 v206, v9, v11
	v_fmac_f32_e32 v158, v9, v12
	v_fmac_f32_e32 v159, v5, v14
	v_fmac_f32_e32 v152, v5, v15
	v_fmac_f32_e32 v49, v5, v17
	v_fmac_f32_e32 v156, v9, v14
	v_fmac_f32_e32 v47, v9, v17
	v_mov_b32_dpp v10, v221 quad_perm:[1,0,3,2] row_mask:0xf bank_mask:0xf
	v_mov_b32_dpp v12, v219 quad_perm:[1,0,3,2] row_mask:0xf bank_mask:0xf
	v_mov_b32_dpp v14, v217 quad_perm:[1,0,3,2] row_mask:0xf bank_mask:0xf
	v_mov_b32_dpp v2, v224 quad_perm:[1,0,3,2] row_mask:0xf bank_mask:0xf
	v_mov_b32_dpp v3, v225 quad_perm:[1,0,3,2] row_mask:0xf bank_mask:0xf
	s_waitcnt lgkmcnt(4)
	v_add_f32_e32 v10, v221, v10
	s_nop 1
	v_mov_b32_dpp v11, v10 quad_perm:[2,3,0,1] row_mask:0xf bank_mask:0xf
	s_waitcnt lgkmcnt(4)
	v_add_f32_e32 v12, v219, v12
	s_nop 1
	v_mov_b32_dpp v13, v12 quad_perm:[2,3,0,1] row_mask:0xf bank_mask:0xf
	v_mov_b32_dpp v6, v223 quad_perm:[1,0,3,2] row_mask:0xf bank_mask:0xf
	v_mov_b32_dpp v8, v222 quad_perm:[1,0,3,2] row_mask:0xf bank_mask:0xf
	s_waitcnt lgkmcnt(3)
	v_add_f32_e32 v10, v10, v11
	s_nop 1
	v_mov_b32_dpp v11, v10 row_half_mirror row_mask:0xf bank_mask:0xf
	s_waitcnt lgkmcnt(3)
	v_add_f32_e32 v12, v12, v13
	s_nop 1
	v_mov_b32_dpp v13, v12 row_half_mirror row_mask:0xf bank_mask:0xf
	v_add_f32_e32 v2, v224, v2
	v_add_f32_e32 v3, v225, v3
	s_waitcnt lgkmcnt(1)
	v_add_f32_e32 v10, v10, v11
	s_nop 1
	v_mov_b32_dpp v11, v10 row_mirror row_mask:0xf bank_mask:0xf
	v_add_f32_e32 v6, v223, v6
	v_add_f32_e32 v8, v222, v8
	v_mov_b32_dpp v4, v2 quad_perm:[2,3,0,1] row_mask:0xf bank_mask:0xf
	v_mov_b32_dpp v5, v3 quad_perm:[2,3,0,1] row_mask:0xf bank_mask:0xf
	s_waitcnt lgkmcnt(2)
	v_add_f32_e32 v10, v10, v11
	v_mov_b32_e32 v11, v10
	s_nop 1
	v_permlane16_swap_b32_e32 v10, v11
	v_add_f32_e32 v19, v10, v11
	v_add_f32_e32 v10, v12, v13
	v_add_f32_e32 v12, v217, v14
	s_nop 1
	v_mov_b32_dpp v13, v12 quad_perm:[2,3,0,1] row_mask:0xf bank_mask:0xf
	v_mov_b32_dpp v11, v10 row_mirror row_mask:0xf bank_mask:0xf
	v_mov_b32_dpp v14, v215 quad_perm:[1,0,3,2] row_mask:0xf bank_mask:0xf
	v_mov_b32_dpp v7, v6 quad_perm:[2,3,0,1] row_mask:0xf bank_mask:0xf
	v_mov_b32_dpp v9, v8 quad_perm:[2,3,0,1] row_mask:0xf bank_mask:0xf
	s_waitcnt lgkmcnt(4)
	v_add_f32_e32 v12, v12, v13
	s_nop 1
	v_mov_b32_dpp v13, v12 row_half_mirror row_mask:0xf bank_mask:0xf
	s_waitcnt lgkmcnt(4)
	v_add_f32_e32 v10, v10, v11
	v_mov_b32_e32 v11, v10
	s_nop 1
	v_permlane16_swap_b32_e32 v10, v11
	v_add_f32_e32 v97, v10, v11
	s_waitcnt lgkmcnt(0)
	v_add_f32_e32 v10, v12, v13
	v_add_f32_e32 v12, v215, v14
	s_nop 1
	v_mov_b32_dpp v13, v12 quad_perm:[2,3,0,1] row_mask:0xf bank_mask:0xf
	v_mov_b32_dpp v11, v10 row_mirror row_mask:0xf bank_mask:0xf
	v_mov_b32_dpp v14, v220 quad_perm:[1,0,3,2] row_mask:0xf bank_mask:0xf
	v_add_f32_e32 v2, v2, v4
	v_add_f32_e32 v3, v3, v5
	s_waitcnt lgkmcnt(2)
	v_add_f32_e32 v12, v12, v13
	s_nop 1
	v_mov_b32_dpp v13, v12 row_half_mirror row_mask:0xf bank_mask:0xf
	s_waitcnt lgkmcnt(2)
	v_add_f32_e32 v10, v10, v11
	v_mov_b32_e32 v11, v10
	s_nop 1
	v_permlane16_swap_b32_e32 v10, v11
	v_add_f32_e32 v21, v10, v11
	s_waitcnt lgkmcnt(0)
	v_add_f32_e32 v10, v12, v13
	v_add_f32_e32 v12, v220, v14
	s_nop 1
	v_mov_b32_dpp v13, v12 quad_perm:[2,3,0,1] row_mask:0xf bank_mask:0xf
	v_mov_b32_dpp v11, v10 row_mirror row_mask:0xf bank_mask:0xf
	v_mov_b32_dpp v14, v218 quad_perm:[1,0,3,2] row_mask:0xf bank_mask:0xf
	v_add_f32_e32 v6, v6, v7
	v_add_f32_e32 v8, v8, v9
	s_waitcnt lgkmcnt(2)
	v_add_f32_e32 v12, v12, v13
	s_nop 1
	v_mov_b32_dpp v13, v12 row_half_mirror row_mask:0xf bank_mask:0xf
	s_waitcnt lgkmcnt(2)
	v_add_f32_e32 v10, v10, v11
	v_mov_b32_e32 v11, v10
	s_nop 1
	v_permlane16_swap_b32_e32 v10, v11
	v_add_f32_e32 v99, v10, v11
	s_waitcnt lgkmcnt(0)
	v_add_f32_e32 v10, v12, v13
	v_add_f32_e32 v12, v218, v14
	s_nop 1
	v_mov_b32_dpp v13, v12 quad_perm:[2,3,0,1] row_mask:0xf bank_mask:0xf
	v_mov_b32_dpp v11, v10 row_mirror row_mask:0xf bank_mask:0xf
	v_mov_b32_dpp v14, v216 quad_perm:[1,0,3,2] row_mask:0xf bank_mask:0xf
	v_mov_b32_dpp v4, v2 row_half_mirror row_mask:0xf bank_mask:0xf
	v_mov_b32_dpp v5, v3 row_half_mirror row_mask:0xf bank_mask:0xf
	s_waitcnt lgkmcnt(4)
	v_add_f32_e32 v12, v12, v13
	s_nop 1
	v_mov_b32_dpp v13, v12 row_half_mirror row_mask:0xf bank_mask:0xf
	s_waitcnt lgkmcnt(4)
	v_add_f32_e32 v10, v10, v11
	v_mov_b32_e32 v11, v10
	s_nop 1
	v_permlane16_swap_b32_e32 v10, v11
	v_add_f32_e32 v95, v10, v11
	s_waitcnt lgkmcnt(0)
	v_add_f32_e32 v10, v12, v13
	v_add_f32_e32 v12, v216, v14
	s_nop 1
	v_mov_b32_dpp v13, v12 quad_perm:[2,3,0,1] row_mask:0xf bank_mask:0xf
	v_mov_b32_dpp v11, v10 row_mirror row_mask:0xf bank_mask:0xf
	v_mov_b32_dpp v14, v214 quad_perm:[1,0,3,2] row_mask:0xf bank_mask:0xf
	v_mov_b32_dpp v7, v6 row_half_mirror row_mask:0xf bank_mask:0xf
	v_mov_b32_dpp v9, v8 row_half_mirror row_mask:0xf bank_mask:0xf
	s_waitcnt lgkmcnt(4)
	v_add_f32_e32 v12, v12, v13
	s_nop 1
	v_mov_b32_dpp v13, v12 row_half_mirror row_mask:0xf bank_mask:0xf
	s_waitcnt lgkmcnt(4)
	v_add_f32_e32 v10, v10, v11
	v_mov_b32_e32 v11, v10
	s_nop 1
	v_permlane16_swap_b32_e32 v10, v11
	v_add_f32_e32 v101, v10, v11
	s_waitcnt lgkmcnt(0)
	v_add_f32_e32 v10, v12, v13
	v_add_f32_e32 v12, v214, v14
	s_nop 1
	v_mov_b32_dpp v13, v12 quad_perm:[2,3,0,1] row_mask:0xf bank_mask:0xf
	v_mov_b32_dpp v11, v10 row_mirror row_mask:0xf bank_mask:0xf
	v_mov_b32_dpp v14, v213 quad_perm:[1,0,3,2] row_mask:0xf bank_mask:0xf
	v_add_f32_e32 v2, v2, v4
	v_add_f32_e32 v3, v3, v5
	s_waitcnt lgkmcnt(2)
	v_add_f32_e32 v12, v12, v13
	s_nop 1
	v_mov_b32_dpp v13, v12 row_half_mirror row_mask:0xf bank_mask:0xf
	s_waitcnt lgkmcnt(2)
	v_add_f32_e32 v10, v10, v11
	v_mov_b32_e32 v11, v10
	s_nop 1
	v_permlane16_swap_b32_e32 v10, v11
	v_add_f32_e32 v107, v10, v11
	s_waitcnt lgkmcnt(0)
	v_add_f32_e32 v10, v12, v13
	v_add_f32_e32 v12, v213, v14
	s_nop 1
	v_mov_b32_dpp v13, v12 quad_perm:[2,3,0,1] row_mask:0xf bank_mask:0xf
	v_mov_b32_dpp v11, v10 row_mirror row_mask:0xf bank_mask:0xf
	v_mov_b32_dpp v14, v212 quad_perm:[1,0,3,2] row_mask:0xf bank_mask:0xf
	v_add_f32_e32 v6, v6, v7
	v_add_f32_e32 v8, v8, v9
	s_waitcnt lgkmcnt(2)
	v_add_f32_e32 v12, v12, v13
	s_nop 1
	v_mov_b32_dpp v13, v12 row_half_mirror row_mask:0xf bank_mask:0xf
	s_waitcnt lgkmcnt(2)
	v_add_f32_e32 v10, v10, v11
	v_mov_b32_e32 v11, v10
	s_nop 1
	v_permlane16_swap_b32_e32 v10, v11
	v_add_f32_e32 v115, v10, v11
	s_waitcnt lgkmcnt(0)
	v_add_f32_e32 v10, v12, v13
	v_add_f32_e32 v12, v212, v14
	s_nop 1
	v_mov_b32_dpp v13, v12 quad_perm:[2,3,0,1] row_mask:0xf bank_mask:0xf
	v_mov_b32_dpp v11, v10 row_mirror row_mask:0xf bank_mask:0xf
	v_mov_b32_dpp v14, v211 quad_perm:[1,0,3,2] row_mask:0xf bank_mask:0xf
	v_mov_b32_dpp v4, v2 row_mirror row_mask:0xf bank_mask:0xf
	v_mov_b32_dpp v5, v3 row_mirror row_mask:0xf bank_mask:0xf
	s_waitcnt lgkmcnt(4)
	v_add_f32_e32 v12, v12, v13
	s_nop 1
	v_mov_b32_dpp v13, v12 row_half_mirror row_mask:0xf bank_mask:0xf
	s_waitcnt lgkmcnt(4)
	v_add_f32_e32 v10, v10, v11
	v_mov_b32_e32 v11, v10
	s_nop 1
	v_permlane16_swap_b32_e32 v10, v11
	v_add_f32_e32 v104, v10, v11
	s_waitcnt lgkmcnt(0)
	v_add_f32_e32 v10, v12, v13
	v_add_f32_e32 v12, v211, v14
	s_nop 1
	v_mov_b32_dpp v13, v12 quad_perm:[2,3,0,1] row_mask:0xf bank_mask:0xf
	v_mov_b32_dpp v11, v10 row_mirror row_mask:0xf bank_mask:0xf
	v_mov_b32_dpp v14, v210 quad_perm:[1,0,3,2] row_mask:0xf bank_mask:0xf
	v_mov_b32_dpp v7, v6 row_mirror row_mask:0xf bank_mask:0xf
	v_mov_b32_dpp v9, v8 row_mirror row_mask:0xf bank_mask:0xf
	s_waitcnt lgkmcnt(4)
	v_add_f32_e32 v12, v12, v13
	s_nop 1
	v_mov_b32_dpp v13, v12 row_half_mirror row_mask:0xf bank_mask:0xf
	s_waitcnt lgkmcnt(4)
	v_add_f32_e32 v10, v10, v11
	v_mov_b32_e32 v11, v10
	s_nop 1
	v_permlane16_swap_b32_e32 v10, v11
	v_add_f32_e32 v113, v10, v11
	s_waitcnt lgkmcnt(0)
	v_add_f32_e32 v10, v12, v13
	v_add_f32_e32 v12, v210, v14
	s_nop 1
	v_mov_b32_dpp v13, v12 quad_perm:[2,3,0,1] row_mask:0xf bank_mask:0xf
	v_mov_b32_dpp v11, v10 row_mirror row_mask:0xf bank_mask:0xf
	v_mov_b32_dpp v14, v209 quad_perm:[1,0,3,2] row_mask:0xf bank_mask:0xf
	v_add_f32_e32 v2, v2, v4
	v_add_f32_e32 v4, v3, v5
	s_waitcnt lgkmcnt(2)
	v_add_f32_e32 v12, v12, v13
	s_nop 1
	v_mov_b32_dpp v13, v12 row_half_mirror row_mask:0xf bank_mask:0xf
	s_waitcnt lgkmcnt(2)
	v_add_f32_e32 v10, v10, v11
	v_mov_b32_e32 v11, v10
	s_nop 1
	v_permlane16_swap_b32_e32 v10, v11
	v_add_f32_e32 v109, v10, v11
	s_waitcnt lgkmcnt(0)
	v_add_f32_e32 v10, v12, v13
	v_add_f32_e32 v12, v209, v14
	s_nop 1
	v_mov_b32_dpp v13, v12 quad_perm:[2,3,0,1] row_mask:0xf bank_mask:0xf
	v_mov_b32_dpp v11, v10 row_mirror row_mask:0xf bank_mask:0xf
	v_mov_b32_dpp v14, v208 quad_perm:[1,0,3,2] row_mask:0xf bank_mask:0xf
	v_add_f32_e32 v6, v6, v7
	v_add_f32_e32 v8, v8, v9
	s_waitcnt lgkmcnt(2)
	v_add_f32_e32 v12, v12, v13
	s_nop 1
	v_mov_b32_dpp v13, v12 row_half_mirror row_mask:0xf bank_mask:0xf
	s_waitcnt lgkmcnt(2)
	v_add_f32_e32 v10, v10, v11
	v_mov_b32_e32 v11, v10
	s_nop 1
	v_permlane16_swap_b32_e32 v10, v11
	v_add_f32_e32 v117, v10, v11
	s_waitcnt lgkmcnt(0)
	v_add_f32_e32 v10, v12, v13
	v_add_f32_e32 v12, v208, v14
	s_nop 1
	v_mov_b32_dpp v13, v12 quad_perm:[2,3,0,1] row_mask:0xf bank_mask:0xf
	v_mov_b32_dpp v11, v10 row_mirror row_mask:0xf bank_mask:0xf
	v_mov_b32_dpp v14, v207 quad_perm:[1,0,3,2] row_mask:0xf bank_mask:0xf
	v_mov_b32_e32 v3, v2
	v_mov_b32_e32 v5, v4
	s_waitcnt lgkmcnt(2)
	v_add_f32_e32 v12, v12, v13
	s_nop 1
	v_mov_b32_dpp v13, v12 row_half_mirror row_mask:0xf bank_mask:0xf
	s_waitcnt lgkmcnt(2)
	v_add_f32_e32 v10, v10, v11
	v_mov_b32_e32 v11, v10
	s_nop 1
	v_permlane16_swap_b32_e32 v10, v11
	v_add_f32_e32 v111, v10, v11
	s_waitcnt lgkmcnt(0)
	v_add_f32_e32 v10, v12, v13
	v_add_f32_e32 v12, v207, v14
	s_nop 1
	v_mov_b32_dpp v13, v12 quad_perm:[2,3,0,1] row_mask:0xf bank_mask:0xf
	v_mov_b32_dpp v11, v10 row_mirror row_mask:0xf bank_mask:0xf
	v_mov_b32_dpp v14, v206 quad_perm:[1,0,3,2] row_mask:0xf bank_mask:0xf
	v_mov_b32_e32 v7, v6
	v_mov_b32_e32 v9, v8
	s_waitcnt lgkmcnt(2)
	v_add_f32_e32 v12, v12, v13
	s_nop 1
	v_mov_b32_dpp v13, v12 row_half_mirror row_mask:0xf bank_mask:0xf
	s_waitcnt lgkmcnt(2)
	v_add_f32_e32 v10, v10, v11
	v_mov_b32_e32 v11, v10
	s_nop 1
	v_permlane16_swap_b32_e32 v10, v11
	v_add_f32_e32 v119, v10, v11
	s_waitcnt lgkmcnt(0)
	v_add_f32_e32 v10, v12, v13
	v_add_f32_e32 v12, v206, v14
	s_nop 1
	v_mov_b32_dpp v13, v12 quad_perm:[2,3,0,1] row_mask:0xf bank_mask:0xf
	v_mov_b32_dpp v11, v10 row_mirror row_mask:0xf bank_mask:0xf
	v_mov_b32_dpp v14, v205 quad_perm:[1,0,3,2] row_mask:0xf bank_mask:0xf
	v_permlane16_swap_b32_e32 v2, v3
	s_waitcnt lgkmcnt(2)
	v_add_f32_e32 v12, v12, v13
	s_nop 1
	v_mov_b32_dpp v13, v12 row_half_mirror row_mask:0xf bank_mask:0xf
	s_waitcnt lgkmcnt(2)
	v_add_f32_e32 v10, v10, v11
	v_mov_b32_e32 v11, v10
	s_nop 1
	v_permlane16_swap_b32_e32 v10, v11
	v_add_f32_e32 v123, v10, v11
	s_waitcnt lgkmcnt(0)
	v_add_f32_e32 v10, v12, v13
	v_add_f32_e32 v12, v205, v14
	s_nop 1
	v_mov_b32_dpp v13, v12 quad_perm:[2,3,0,1] row_mask:0xf bank_mask:0xf
	v_mov_b32_dpp v11, v10 row_mirror row_mask:0xf bank_mask:0xf
	v_mov_b32_dpp v14, v158 quad_perm:[1,0,3,2] row_mask:0xf bank_mask:0xf
	v_permlane16_swap_b32_e32 v4, v5
	s_waitcnt lgkmcnt(2)
	v_add_f32_e32 v12, v12, v13
	s_nop 1
	v_mov_b32_dpp v13, v12 row_half_mirror row_mask:0xf bank_mask:0xf
	s_waitcnt lgkmcnt(2)
	v_add_f32_e32 v10, v10, v11
	v_mov_b32_e32 v11, v10
	s_nop 1
	v_permlane16_swap_b32_e32 v10, v11
	v_add_f32_e32 v130, v10, v11
	s_waitcnt lgkmcnt(0)
	v_add_f32_e32 v10, v12, v13
	v_add_f32_e32 v12, v158, v14
	s_nop 1
	v_mov_b32_dpp v13, v12 quad_perm:[2,3,0,1] row_mask:0xf bank_mask:0xf
	v_mov_b32_dpp v11, v10 row_mirror row_mask:0xf bank_mask:0xf
	v_mov_b32_dpp v14, v153 quad_perm:[1,0,3,2] row_mask:0xf bank_mask:0xf
	v_permlane16_swap_b32_e32 v6, v7
	s_waitcnt lgkmcnt(2)
	v_add_f32_e32 v12, v12, v13
	s_nop 1
	v_mov_b32_dpp v13, v12 row_half_mirror row_mask:0xf bank_mask:0xf
	s_waitcnt lgkmcnt(2)
	v_add_f32_e32 v10, v10, v11
	v_mov_b32_e32 v11, v10
	s_nop 1
	v_permlane16_swap_b32_e32 v10, v11
	v_add_f32_e32 v121, v10, v11
	s_waitcnt lgkmcnt(0)
	v_add_f32_e32 v10, v12, v13
	v_add_f32_e32 v12, v153, v14
	s_nop 1
	v_mov_b32_dpp v13, v12 quad_perm:[2,3,0,1] row_mask:0xf bank_mask:0xf
	v_mov_b32_dpp v11, v10 row_mirror row_mask:0xf bank_mask:0xf
	v_mov_b32_dpp v14, v57 quad_perm:[1,0,3,2] row_mask:0xf bank_mask:0xf
	v_permlane16_swap_b32_e32 v8, v9
	s_waitcnt lgkmcnt(2)
	v_add_f32_e32 v12, v12, v13
	s_nop 1
	v_mov_b32_dpp v13, v12 row_half_mirror row_mask:0xf bank_mask:0xf
	s_waitcnt lgkmcnt(2)
	v_add_f32_e32 v10, v10, v11
	v_mov_b32_e32 v11, v10
	s_nop 1
	v_permlane16_swap_b32_e32 v10, v11
	v_add_f32_e32 v128, v10, v11
	s_waitcnt lgkmcnt(0)
	v_add_f32_e32 v10, v12, v13
	v_add_f32_e32 v12, v57, v14
	s_nop 1
	v_mov_b32_dpp v13, v12 quad_perm:[2,3,0,1] row_mask:0xf bank_mask:0xf
	v_mov_b32_dpp v11, v10 row_mirror row_mask:0xf bank_mask:0xf
	v_mov_b32_dpp v14, v159 quad_perm:[1,0,3,2] row_mask:0xf bank_mask:0xf
	v_add_f32_e32 v2, v2, v3
	v_add_f32_e32 v4, v4, v5
	s_waitcnt lgkmcnt(2)
	v_add_f32_e32 v12, v12, v13
	s_nop 1
	v_mov_b32_dpp v13, v12 row_half_mirror row_mask:0xf bank_mask:0xf
	s_waitcnt lgkmcnt(2)
	v_add_f32_e32 v10, v10, v11
	v_mov_b32_e32 v11, v10
	s_nop 1
	v_permlane16_swap_b32_e32 v10, v11
	v_add_f32_e32 v57, v10, v11
	s_waitcnt lgkmcnt(0)
	v_add_f32_e32 v10, v12, v13
	v_add_f32_e32 v12, v159, v14
	s_nop 1
	v_mov_b32_dpp v13, v12 quad_perm:[2,3,0,1] row_mask:0xf bank_mask:0xf
	v_mov_b32_dpp v11, v10 row_mirror row_mask:0xf bank_mask:0xf
	v_mov_b32_dpp v14, v156 quad_perm:[1,0,3,2] row_mask:0xf bank_mask:0xf
	v_add_f32_e32 v6, v6, v7
	v_add_f32_e32 v8, v8, v9
	s_waitcnt lgkmcnt(2)
	v_add_f32_e32 v12, v12, v13
	s_nop 1
	v_mov_b32_dpp v13, v12 row_half_mirror row_mask:0xf bank_mask:0xf
	s_waitcnt lgkmcnt(2)
	v_add_f32_e32 v10, v10, v11
	v_mov_b32_e32 v11, v10
	s_nop 1
	v_permlane16_swap_b32_e32 v10, v11
	v_add_f32_e32 v132, v10, v11
	s_waitcnt lgkmcnt(0)
	v_add_f32_e32 v10, v12, v13
	v_add_f32_e32 v12, v156, v14
	s_nop 1
	v_mov_b32_dpp v13, v12 quad_perm:[2,3,0,1] row_mask:0xf bank_mask:0xf
	v_mov_b32_dpp v11, v10 row_mirror row_mask:0xf bank_mask:0xf
	v_mov_b32_dpp v14, v152 quad_perm:[1,0,3,2] row_mask:0xf bank_mask:0xf
	v_mov_b32_e32 v3, v2
	v_mov_b32_e32 v5, v4
	s_waitcnt lgkmcnt(2)
	v_add_f32_e32 v12, v12, v13
	s_nop 1
	v_mov_b32_dpp v13, v12 row_half_mirror row_mask:0xf bank_mask:0xf
	s_waitcnt lgkmcnt(2)
	v_add_f32_e32 v10, v10, v11
	v_mov_b32_e32 v11, v10
	s_nop 1
	v_permlane16_swap_b32_e32 v10, v11
	v_add_f32_e32 v126, v10, v11
	s_waitcnt lgkmcnt(0)
	v_add_f32_e32 v10, v12, v13
	v_add_f32_e32 v12, v152, v14
	s_nop 1
	v_mov_b32_dpp v13, v12 quad_perm:[2,3,0,1] row_mask:0xf bank_mask:0xf
	v_mov_b32_dpp v11, v10 row_mirror row_mask:0xf bank_mask:0xf
	v_mov_b32_dpp v14, v55 quad_perm:[1,0,3,2] row_mask:0xf bank_mask:0xf
	v_mov_b32_e32 v7, v6
	v_mov_b32_e32 v9, v8
	s_waitcnt lgkmcnt(2)
	v_add_f32_e32 v12, v12, v13
	s_nop 1
	v_mov_b32_dpp v13, v12 row_half_mirror row_mask:0xf bank_mask:0xf
	s_waitcnt lgkmcnt(2)
	v_add_f32_e32 v10, v10, v11
	v_mov_b32_e32 v11, v10
	s_nop 1
	v_permlane16_swap_b32_e32 v10, v11
	v_add_f32_e32 v134, v10, v11
	s_waitcnt lgkmcnt(0)
	v_add_f32_e32 v10, v12, v13
	v_add_f32_e32 v12, v55, v14
	s_nop 1
	v_mov_b32_dpp v13, v12 quad_perm:[2,3,0,1] row_mask:0xf bank_mask:0xf
	v_mov_b32_dpp v11, v10 row_mirror row_mask:0xf bank_mask:0xf
	v_mov_b32_dpp v14, v53 quad_perm:[1,0,3,2] row_mask:0xf bank_mask:0xf
	v_mov_b32_e32 v20, v19
	v_mov_b32_e32 v98, v97
	s_waitcnt lgkmcnt(2)
	v_add_f32_e32 v12, v12, v13
	s_nop 1
	v_mov_b32_dpp v13, v12 row_half_mirror row_mask:0xf bank_mask:0xf
	s_waitcnt lgkmcnt(2)
	v_add_f32_e32 v10, v10, v11
	v_mov_b32_e32 v11, v10
	s_nop 1
	v_permlane16_swap_b32_e32 v10, v11
	v_add_f32_e32 v55, v10, v11
	s_waitcnt lgkmcnt(0)
	v_add_f32_e32 v10, v12, v13
	v_add_f32_e32 v12, v53, v14
	s_nop 1
	v_mov_b32_dpp v13, v12 quad_perm:[2,3,0,1] row_mask:0xf bank_mask:0xf
	v_mov_b32_dpp v11, v10 row_mirror row_mask:0xf bank_mask:0xf
	v_mov_b32_dpp v14, v51 quad_perm:[1,0,3,2] row_mask:0xf bank_mask:0xf
	v_mov_b32_e32 v94, v21
	v_mov_b32_e32 v100, v99
	s_waitcnt lgkmcnt(2)
	v_add_f32_e32 v12, v12, v13
	s_nop 1
	v_mov_b32_dpp v13, v12 row_half_mirror row_mask:0xf bank_mask:0xf
	s_waitcnt lgkmcnt(2)
	v_add_f32_e32 v10, v10, v11
	v_mov_b32_e32 v11, v10
	s_nop 1
	v_permlane16_swap_b32_e32 v10, v11
	v_add_f32_e32 v143, v10, v11
	s_waitcnt lgkmcnt(0)
	v_add_f32_e32 v10, v12, v13
	v_add_f32_e32 v12, v51, v14
	s_nop 0
	v_mov_b32_dpp v11, v10 row_mirror row_mask:0xf bank_mask:0xf
	s_nop 0
	v_mov_b32_dpp v13, v12 quad_perm:[2,3,0,1] row_mask:0xf bank_mask:0xf
	v_mov_b32_dpp v14, v47 quad_perm:[1,0,3,2] row_mask:0xf bank_mask:0xf
	v_mov_b32_e32 v96, v95
	v_mov_b32_e32 v102, v101
	s_waitcnt lgkmcnt(2)
	v_add_f32_e32 v10, v10, v11
	s_waitcnt lgkmcnt(1)
	v_add_f32_e32 v11, v12, v13
	s_nop 1
	v_mov_b32_dpp v12, v11 row_half_mirror row_mask:0xf bank_mask:0xf
	v_mov_b32_e32 v13, v10
	s_nop 1
	v_permlane16_swap_b32_e32 v10, v13
	v_add_f32_e32 v51, v10, v13
	s_waitcnt lgkmcnt(0)
	v_add_f32_e32 v10, v11, v12
	s_nop 1
	v_mov_b32_dpp v11, v10 row_mirror row_mask:0xf bank_mask:0xf
	v_mov_b32_dpp v12, v49 quad_perm:[1,0,3,2] row_mask:0xf bank_mask:0xf
	v_mov_b32_e32 v108, v107
	v_mov_b32_e32 v116, v115
	v_mov_b32_e32 v106, v104
	s_waitcnt lgkmcnt(1)
	v_add_f32_e32 v10, v10, v11
	s_waitcnt lgkmcnt(0)
	v_add_f32_e32 v11, v49, v12
	v_mov_b32_e32 v13, v10
	s_nop 0
	v_mov_b32_dpp v12, v11 quad_perm:[2,3,0,1] row_mask:0xf bank_mask:0xf
	s_nop 0
	v_permlane16_swap_b32_e32 v10, v13
	v_add_f32_e32 v141, v10, v13
	v_add_f32_e32 v10, v47, v14
	s_nop 1
	v_mov_b32_dpp v13, v10 quad_perm:[2,3,0,1] row_mask:0xf bank_mask:0xf
	s_waitcnt lgkmcnt(1)
	v_add_f32_e32 v11, v11, v12
	s_nop 1
	v_mov_b32_dpp v12, v11 row_half_mirror row_mask:0xf bank_mask:0xf
	v_mov_b32_e32 v114, v113
	v_mov_b32_e32 v110, v109
	s_waitcnt lgkmcnt(1)
	v_add_f32_e32 v10, v10, v13
	s_nop 1
	v_mov_b32_dpp v13, v10 row_half_mirror row_mask:0xf bank_mask:0xf
	s_waitcnt lgkmcnt(1)
	v_add_f32_e32 v11, v11, v12
	s_nop 1
	v_mov_b32_dpp v12, v11 row_mirror row_mask:0xf bank_mask:0xf
	v_mov_b32_e32 v118, v117
	v_mov_b32_e32 v112, v111
	s_waitcnt lgkmcnt(1)
	v_add_f32_e32 v10, v10, v13
	s_nop 1
	v_mov_b32_dpp v13, v10 row_mirror row_mask:0xf bank_mask:0xf
	s_waitcnt lgkmcnt(1)
	v_add_f32_e32 v11, v11, v12
	v_mov_b32_e32 v12, v11
	s_nop 1
	v_permlane16_swap_b32_e32 v11, v12
	s_waitcnt lgkmcnt(0)
	v_add_f32_e32 v10, v10, v13
	v_add_f32_e32 v136, v11, v12
	v_mov_b32_e32 v11, v10
	s_nop 1
	v_permlane16_swap_b32_e32 v10, v11
	v_add_f32_e32 v139, v10, v11
	v_mov_b32_e32 v120, v119
	v_mov_b32_e32 v124, v123
	v_mov_b32_e32 v131, v130
	v_mov_b32_e32 v122, v121
	v_mov_b32_e32 v129, v128
	v_mov_b32_e32 v125, v57
	v_mov_b32_e32 v133, v132
	v_mov_b32_e32 v127, v126
	v_mov_b32_e32 v135, v134
	v_mov_b32_e32 v137, v55
	v_mov_b32_e32 v144, v143
	v_mov_b32_e32 v53, v51
	v_mov_b32_e32 v142, v141
	v_mov_b32_e32 v138, v136
	v_mov_b32_e32 v140, v139
	v_permlane32_swap_b32_e32 v2, v3
	v_permlane32_swap_b32_e32 v4, v5
	v_permlane32_swap_b32_e32 v6, v7
	v_permlane32_swap_b32_e32 v8, v9
	v_permlane32_swap_b32_e32 v19, v20
	v_permlane32_swap_b32_e32 v97, v98
	v_permlane32_swap_b32_e32 v21, v94
	v_permlane32_swap_b32_e32 v99, v100
	v_permlane32_swap_b32_e32 v95, v96
	v_permlane32_swap_b32_e32 v101, v102
	v_permlane32_swap_b32_e32 v107, v108
	v_permlane32_swap_b32_e32 v115, v116
	v_permlane32_swap_b32_e32 v104, v106
	v_permlane32_swap_b32_e32 v113, v114
	v_permlane32_swap_b32_e32 v109, v110
	v_permlane32_swap_b32_e32 v117, v118
	v_permlane32_swap_b32_e32 v111, v112
	v_permlane32_swap_b32_e32 v119, v120
	v_permlane32_swap_b32_e32 v123, v124
	v_permlane32_swap_b32_e32 v130, v131
	v_permlane32_swap_b32_e32 v121, v122
	v_permlane32_swap_b32_e32 v128, v129
	v_permlane32_swap_b32_e32 v57, v125
	v_permlane32_swap_b32_e32 v132, v133
	v_permlane32_swap_b32_e32 v126, v127
	v_permlane32_swap_b32_e32 v134, v135
	v_permlane32_swap_b32_e32 v55, v137
	v_permlane32_swap_b32_e32 v143, v144
	v_permlane32_swap_b32_e32 v51, v53
	v_permlane32_swap_b32_e32 v141, v142
	v_permlane32_swap_b32_e32 v136, v138
	v_permlane32_swap_b32_e32 v139, v140
	s_and_saveexec_b64 s[4:5], s[42:43]
	s_cbranch_execz .LBB0_1299
	v_add_f32_e32 v4, v4, v5
	v_add_f32_e32 v2, v2, v3
	v_cndmask_b32_e64 v2, v2, v4, s[40:41]
	v_mul_f32_e32 v2, 0xbfb8aa3b, v2
	s_load_dwordx2 s[6:7], s[56:57], 0xd0
	v_exp_f32_e32 v2, v2
	v_add_f32_e32 v8, v8, v9
	v_add_f32_e32 v6, v6, v7
	v_cndmask_b32_e64 v49, v6, v8, s[40:41]
	v_add_f32_e32 v2, 1.0, v2
	v_rcp_f32_e32 v18, v2
	s_waitcnt lgkmcnt(0)
	global_load_dwordx4 v[2:5], v1, s[6:7] offset:48
	global_load_dwordx4 v[6:9], v1, s[6:7] offset:32
	global_load_dwordx4 v[10:13], v1, s[6:7] offset:16
	global_load_dwordx4 v[14:17], v1, s[6:7]
	s_mov_b32 s6, 0xf149f2ca
	s_waitcnt vmcnt(0)
	v_add_f32_e32 v47, v18, v14
	v_mul_f32_e32 v14, 0xbfb8aa3b, v49
	v_exp_f32_e32 v14, v14
	v_cmp_nlt_f32_e32 vcc, s6, v47
	v_add_f32_e32 v14, 1.0, v14
	v_rcp_f32_e32 v14, v14
	s_nop 0
	v_add_f32_e32 v49, v14, v15
	v_mov_b32_e32 v15, 0xf149f2ca
	v_cndmask_b32_e32 v145, v47, v15, vcc
	v_cmp_gt_f32_e64 s[44:45], v49, v145
	v_cmp_ngt_f32_e64 s[46:47], v49, v145
	v_mov_b32_e32 v148, v49
	v_mov_b32_e32 v147, v145
	s_and_saveexec_b64 s[6:7], s[46:47]
	s_cbranch_execz .LBB0_1305
	v_mov_b32_e32 v147, 0xf149f2ca
	v_cmp_gt_f32_e64 s[46:47], v49, v147
	s_and_saveexec_b64 s[8:9], s[46:47]
	v_mov_b32_e32 v147, v49
	s_or_b64 exec, exec, s[8:9]
	v_mov_b32_e32 v148, v145

.LBB0_1613:
	s_add_u32 s2, s0, s17
	s_addc_u32 s3, s1, s18
	global_load_dwordx4 v[106:109], v65, s[2:3] nt
	v_add_co_u32_e32 v84, vcc, s13, v80
	v_lshl_add_u64 v[82:83], s[0:1], 0, v[78:79]
	s_nop 0
	v_addc_co_u32_e32 v85, vcc, -1, v81, vcc
	v_add_co_u32_e32 v82, vcc, 0x11100000, v82
	s_add_i32 s15, s15, s66
	s_nop 0
	v_addc_co_u32_e32 v83, vcc, 0, v83, vcc
	global_load_dwordx2 v[110:111], v[82:83], off nt
	global_load_dwordx2 v[112:113], v[82:83], off offset:512 nt
	global_load_dwordx2 v[114:115], v[82:83], off offset:1024 nt
	global_load_dwordx2 v[116:117], v[82:83], off offset:1536 nt
	global_load_dwordx2 v[118:119], v[82:83], off offset:2048 nt
	global_load_dwordx2 v[120:121], v[82:83], off offset:2560 nt
	global_load_dwordx2 v[122:123], v[82:83], off offset:3072 nt
	global_load_dwordx2 v[124:125], v[82:83], off offset:3584 nt
	v_lshl_add_u64 v[78:79], v[78:79], 0, s[94:95]
	s_waitcnt vmcnt(8)
	v_readfirstlane_b32 s2, v106
	v_readfirstlane_b32 s3, v107
	s_lshr_b32 s4, s2, 18
	s_lshl_b32 s2, s2, 11
	s_lshr_b32 s11, s3, 18
	s_and_b32 s19, s4, 0x3ffc
	s_and_b32 s4, s2, 0x7ffff800
	s_and_b32 s2, s11, 0x3ffc
	s_add_i32 s11, s81, s19
	s_add_i32 s2, s81, s2
	v_mov_b32_e32 v105, s11
	v_mov_b32_e32 v139, s2
	ds_read_b32 v138, v105
	ds_read_b32 v140, v139
	s_lshl_b32 s3, s3, 11
	v_pk_mul_f32 v[82:83], v[108:109], s[8:9] op_sel_hi:[1,0]
	s_waitcnt vmcnt(7)
	v_lshlrev_b32_e32 v106, 16, v110
	s_waitcnt lgkmcnt(1)
	v_ashrrev_i32_e32 v139, 31, v138
	s_waitcnt lgkmcnt(0)
	v_ashrrev_i32_e32 v141, 31, v140
	v_lshlrev_b64 v[138:139], 19, v[138:139]
	v_lshlrev_b64 v[140:141], 19, v[140:141]
	v_lshl_add_u64 v[138:139], s[6:7], 0, v[138:139]
	v_lshl_add_u64 v[140:141], s[6:7], 0, v[140:141]
	v_lshl_add_u64 v[138:139], v[138:139], 0, s[4:5]
	s_and_b32 s4, s3, 0x7ffff800
	v_lshl_add_u64 v[140:141], v[140:141], 0, s[4:5]
	v_readfirstlane_b32 s2, v138
	v_readfirstlane_b32 s3, v139
	s_nop 4
	global_load_dword v105, v93, s[2:3] nt
	global_load_dword v139, v93, s[2:3] offset:256 nt
	global_load_dword v143, v93, s[2:3] offset:512 nt
	global_load_dword v145, v93, s[2:3] offset:768 nt
	global_load_dword v147, v93, s[2:3] offset:1024 nt
	global_load_dword v149, v93, s[2:3] offset:1280 nt
	global_load_dword v151, v93, s[2:3] offset:1536 nt
	global_load_dword v153, v93, s[2:3] offset:1792 nt
	v_readfirstlane_b32 s2, v140
	v_readfirstlane_b32 s3, v141
	s_nop 4
	global_load_dword v155, v93, s[2:3] nt
	global_load_dword v157, v93, s[2:3] offset:256 nt
	global_load_dword v159, v93, s[2:3] offset:512 nt
	global_load_dword v167, v93, s[2:3] offset:768 nt
	global_load_dword v175, v93, s[2:3] offset:1024 nt
	global_load_dword v183, v93, s[2:3] offset:1280 nt
	global_load_dword v191, v93, s[2:3] offset:1536 nt
	global_load_dword v199, v93, s[2:3] offset:1792 nt
	v_and_b32_e32 v107, 0xffff0000, v110
	v_lshlrev_b32_e32 v108, 16, v111
	v_and_b32_e32 v109, 0xffff0000, v111
	s_waitcnt vmcnt(22)
	v_lshlrev_b32_e32 v110, 16, v112
	v_and_b32_e32 v111, 0xffff0000, v112
	v_lshlrev_b32_e32 v112, 16, v113
	v_and_b32_e32 v113, 0xffff0000, v113
	s_waitcnt vmcnt(21)
	v_lshlrev_b32_e32 v126, 16, v114
	v_and_b32_e32 v127, 0xffff0000, v114
	v_lshlrev_b32_e32 v114, 16, v115
	v_and_b32_e32 v115, 0xffff0000, v115
	s_waitcnt vmcnt(16)
	v_lshlrev_b32_e32 v136, 16, v124
	v_and_b32_e32 v137, 0xffff0000, v124
	v_lshlrev_b32_e32 v124, 16, v125
	v_and_b32_e32 v125, 0xffff0000, v125
	v_lshlrev_b32_e32 v128, 16, v116
	v_and_b32_e32 v129, 0xffff0000, v116
	v_lshlrev_b32_e32 v116, 16, v117
	v_and_b32_e32 v117, 0xffff0000, v117
	v_lshlrev_b32_e32 v130, 16, v118
	v_and_b32_e32 v131, 0xffff0000, v118
	v_lshlrev_b32_e32 v118, 16, v119
	v_and_b32_e32 v119, 0xffff0000, v119
	v_lshlrev_b32_e32 v132, 16, v120
	v_and_b32_e32 v133, 0xffff0000, v120
	v_lshlrev_b32_e32 v120, 16, v121
	v_and_b32_e32 v121, 0xffff0000, v121
	v_lshlrev_b32_e32 v134, 16, v122
	v_and_b32_e32 v135, 0xffff0000, v122
	v_lshlrev_b32_e32 v122, 16, v123
	v_and_b32_e32 v123, 0xffff0000, v123
	s_add_u32 s17, s17, s68
	s_addc_u32 s18, s18, s69
	s_cmp_ge_i32 s15, s16
	s_waitcnt vmcnt(15)
	v_cvt_f32_fp8_sdwa v140, v105 src0_sel:BYTE_1
	v_cvt_f32_fp8_sdwa v144, v105 src0_sel:BYTE_3
	s_waitcnt vmcnt(14)
	v_cvt_f32_fp8_sdwa v148, v139 src0_sel:BYTE_1
	v_cvt_f32_fp8_sdwa v152, v139 src0_sel:BYTE_3
	s_waitcnt vmcnt(12)
	v_cvt_f32_fp8_e32 v162, v145
	v_cvt_f32_fp8_sdwa v164, v145 src0_sel:BYTE_1
	v_cvt_f32_fp8_sdwa v166, v145 src0_sel:BYTE_2
	v_cvt_f32_fp8_sdwa v168, v145 src0_sel:BYTE_3
	s_waitcnt vmcnt(10)
	v_cvt_f32_fp8_e32 v178, v149
	v_cvt_f32_fp8_sdwa v180, v149 src0_sel:BYTE_1
	v_cvt_f32_fp8_sdwa v182, v149 src0_sel:BYTE_2
	v_cvt_f32_fp8_sdwa v184, v149 src0_sel:BYTE_3
	s_waitcnt vmcnt(8)
	v_cvt_f32_fp8_e32 v194, v153
	v_cvt_f32_fp8_sdwa v196, v153 src0_sel:BYTE_1
	v_cvt_f32_fp8_sdwa v198, v153 src0_sel:BYTE_2
	v_cvt_f32_fp8_sdwa v200, v153 src0_sel:BYTE_3
	s_waitcnt vmcnt(7)
	v_cvt_f32_fp8_e32 v141, v155
	v_cvt_f32_fp8_sdwa v145, v155 src0_sel:BYTE_2
	s_waitcnt vmcnt(6)
	v_cvt_f32_fp8_e32 v149, v157
	v_cvt_f32_fp8_sdwa v153, v157 src0_sel:BYTE_2
	v_cvt_f32_fp8_e32 v138, v105
	v_cvt_f32_fp8_sdwa v142, v105 src0_sel:BYTE_2
	v_cvt_f32_fp8_e32 v146, v139
	v_cvt_f32_fp8_sdwa v150, v139 src0_sel:BYTE_2
	v_cvt_f32_fp8_e32 v154, v143
	v_cvt_f32_fp8_sdwa v156, v143 src0_sel:BYTE_1
	v_cvt_f32_fp8_sdwa v158, v143 src0_sel:BYTE_2
	v_cvt_f32_fp8_sdwa v160, v143 src0_sel:BYTE_3
	v_cvt_f32_fp8_e32 v170, v147
	v_cvt_f32_fp8_sdwa v172, v147 src0_sel:BYTE_1
	v_cvt_f32_fp8_sdwa v174, v147 src0_sel:BYTE_2
	v_cvt_f32_fp8_sdwa v176, v147 src0_sel:BYTE_3
	v_cvt_f32_fp8_e32 v186, v151
	v_cvt_f32_fp8_sdwa v188, v151 src0_sel:BYTE_1
	v_cvt_f32_fp8_sdwa v190, v151 src0_sel:BYTE_2
	v_cvt_f32_fp8_sdwa v192, v151 src0_sel:BYTE_3
	v_cvt_f32_fp8_sdwa v139, v155 src0_sel:BYTE_1
	v_cvt_f32_fp8_sdwa v143, v155 src0_sel:BYTE_3
	v_cvt_f32_fp8_sdwa v147, v157 src0_sel:BYTE_1
	v_cvt_f32_fp8_sdwa v151, v157 src0_sel:BYTE_3
	s_waitcnt vmcnt(5)
	v_cvt_f32_fp8_e32 v157, v159
	v_cvt_f32_fp8_sdwa v161, v159 src0_sel:BYTE_2
	s_waitcnt vmcnt(4)
	v_cvt_f32_fp8_e32 v165, v167
	v_cvt_f32_fp8_sdwa v169, v167 src0_sel:BYTE_2
	s_waitcnt vmcnt(3)
	v_cvt_f32_fp8_e32 v173, v175
	v_cvt_f32_fp8_sdwa v177, v175 src0_sel:BYTE_2
	s_waitcnt vmcnt(2)
	v_cvt_f32_fp8_e32 v181, v183
	v_cvt_f32_fp8_sdwa v185, v183 src0_sel:BYTE_2
	s_waitcnt vmcnt(1)
	v_cvt_f32_fp8_e32 v189, v191
	v_cvt_f32_fp8_sdwa v193, v191 src0_sel:BYTE_2
	s_waitcnt vmcnt(0)
	v_cvt_f32_fp8_e32 v197, v199
	v_cvt_f32_fp8_sdwa v201, v199 src0_sel:BYTE_2
	v_cvt_f32_fp8_sdwa v155, v159 src0_sel:BYTE_1
	v_cvt_f32_fp8_sdwa v159, v159 src0_sel:BYTE_3
	v_cvt_f32_fp8_sdwa v163, v167 src0_sel:BYTE_1
	v_cvt_f32_fp8_sdwa v167, v167 src0_sel:BYTE_3
	v_cvt_f32_fp8_sdwa v171, v175 src0_sel:BYTE_1
	v_cvt_f32_fp8_sdwa v175, v175 src0_sel:BYTE_3
	v_cvt_f32_fp8_sdwa v179, v183 src0_sel:BYTE_1
	v_cvt_f32_fp8_sdwa v183, v183 src0_sel:BYTE_3
	v_cvt_f32_fp8_sdwa v187, v191 src0_sel:BYTE_1
	v_cvt_f32_fp8_sdwa v191, v191 src0_sel:BYTE_3
	v_cvt_f32_fp8_sdwa v195, v199 src0_sel:BYTE_1
	v_cvt_f32_fp8_sdwa v199, v199 src0_sel:BYTE_3
	v_pk_mul_f32 v[140:141], v[82:83], v[140:141]
	v_pk_mul_f32 v[144:145], v[82:83], v[144:145]
	v_pk_mul_f32 v[148:149], v[82:83], v[148:149]
	v_pk_mul_f32 v[152:153], v[82:83], v[152:153]
	v_pk_mul_f32 v[156:157], v[82:83], v[156:157]
	v_pk_mul_f32 v[160:161], v[82:83], v[160:161]
	v_pk_mul_f32 v[164:165], v[82:83], v[164:165]
	v_pk_mul_f32 v[168:169], v[82:83], v[168:169]
	v_pk_mul_f32 v[172:173], v[82:83], v[172:173]
	v_pk_mul_f32 v[176:177], v[82:83], v[176:177]
	v_pk_mul_f32 v[180:181], v[82:83], v[180:181]
	v_pk_mul_f32 v[184:185], v[82:83], v[184:185]
	v_pk_mul_f32 v[188:189], v[82:83], v[188:189]
	v_pk_mul_f32 v[192:193], v[82:83], v[192:193]
	v_pk_mul_f32 v[196:197], v[82:83], v[196:197]
	v_pk_mul_f32 v[200:201], v[82:83], v[200:201]
	v_pk_fma_f32 v[138:139], v[82:83], v[138:139], v[140:141] op_sel:[0,0,1] op_sel_hi:[1,1,0]
	v_pk_fma_f32 v[140:141], v[82:83], v[142:143], v[144:145] op_sel:[0,0,1] op_sel_hi:[1,1,0]
	v_pk_fma_f32 v[142:143], v[82:83], v[146:147], v[148:149] op_sel:[0,0,1] op_sel_hi:[1,1,0]
	v_pk_fma_f32 v[144:145], v[82:83], v[150:151], v[152:153] op_sel:[0,0,1] op_sel_hi:[1,1,0]
	v_pk_fma_f32 v[146:147], v[82:83], v[154:155], v[156:157] op_sel:[0,0,1] op_sel_hi:[1,1,0]
	v_pk_fma_f32 v[148:149], v[82:83], v[158:159], v[160:161] op_sel:[0,0,1] op_sel_hi:[1,1,0]
	v_pk_fma_f32 v[150:151], v[82:83], v[162:163], v[164:165] op_sel:[0,0,1] op_sel_hi:[1,1,0]
	v_pk_fma_f32 v[152:153], v[82:83], v[166:167], v[168:169] op_sel:[0,0,1] op_sel_hi:[1,1,0]
	v_pk_fma_f32 v[154:155], v[82:83], v[170:171], v[172:173] op_sel:[0,0,1] op_sel_hi:[1,1,0]
	v_pk_fma_f32 v[156:157], v[82:83], v[174:175], v[176:177] op_sel:[0,0,1] op_sel_hi:[1,1,0]
	v_pk_fma_f32 v[158:159], v[82:83], v[178:179], v[180:181] op_sel:[0,0,1] op_sel_hi:[1,1,0]
	v_pk_fma_f32 v[160:161], v[82:83], v[182:183], v[184:185] op_sel:[0,0,1] op_sel_hi:[1,1,0]
	v_pk_fma_f32 v[162:163], v[82:83], v[186:187], v[188:189] op_sel:[0,0,1] op_sel_hi:[1,1,0]
	v_pk_fma_f32 v[164:165], v[82:83], v[190:191], v[192:193] op_sel:[0,0,1] op_sel_hi:[1,1,0]
	v_pk_fma_f32 v[166:167], v[82:83], v[194:195], v[196:197] op_sel:[0,0,1] op_sel_hi:[1,1,0]
	v_pk_fma_f32 v[82:83], v[82:83], v[198:199], v[200:201] op_sel:[0,0,1] op_sel_hi:[1,1,0]
	v_pk_fma_f32 v[108:109], v[10:11], v[140:141], v[108:109]
	v_pk_fma_f32 v[106:107], v[8:9], v[138:139], v[106:107]
	v_pk_fma_f32 v[112:113], v[14:15], v[144:145], v[112:113]
	v_pk_fma_f32 v[110:111], v[12:13], v[142:143], v[110:111]
	v_pk_fma_f32 v[114:115], v[26:27], v[148:149], v[114:115]
	v_pk_fma_f32 v[126:127], v[24:25], v[146:147], v[126:127]
	v_pk_fma_f32 v[82:83], v[62:63], v[82:83], v[124:125]
	v_pk_fma_f32 v[124:125], v[60:61], v[166:167], v[136:137]
	v_mul_f32_e32 v105, v107, v107
	v_mul_f32_e32 v136, v109, v109
	v_mul_f32_e32 v137, v111, v111
	v_mul_f32_e32 v138, v113, v113
	v_pk_fma_f32 v[116:117], v[30:31], v[152:153], v[116:117]
	v_pk_fma_f32 v[128:129], v[28:29], v[150:151], v[128:129]
	v_mul_f32_e32 v139, v127, v127
	v_mul_f32_e32 v140, v115, v115
	v_fmac_f32_e32 v105, v106, v106
	v_fmac_f32_e32 v136, v108, v108
	v_fmac_f32_e32 v137, v110, v110
	v_fmac_f32_e32 v138, v112, v112
	v_pk_fma_f32 v[118:119], v[42:43], v[156:157], v[118:119]
	v_pk_fma_f32 v[130:131], v[40:41], v[154:155], v[130:131]
	v_mul_f32_e32 v141, v129, v129
	v_mul_f32_e32 v142, v117, v117
	v_fmac_f32_e32 v139, v126, v126
	v_fmac_f32_e32 v140, v114, v114
	v_add_f32_e32 v105, v105, v136
	v_add_f32_e32 v136, v137, v138
	v_pk_fma_f32 v[120:121], v[46:47], v[160:161], v[120:121]
	v_pk_fma_f32 v[132:133], v[44:45], v[158:159], v[132:133]
	v_mul_f32_e32 v143, v131, v131
	v_mul_f32_e32 v144, v119, v119
	v_fmac_f32_e32 v141, v128, v128
	v_fmac_f32_e32 v142, v116, v116
	v_add_f32_e32 v137, v139, v140
	v_add_f32_e32 v105, v105, v136
	v_pk_fma_f32 v[122:123], v[58:59], v[164:165], v[122:123]
	v_pk_fma_f32 v[134:135], v[56:57], v[162:163], v[134:135]
	v_mul_f32_e32 v145, v133, v133
	v_mul_f32_e32 v146, v121, v121
	v_fmac_f32_e32 v143, v130, v130
	v_fmac_f32_e32 v144, v118, v118
	v_add_f32_e32 v138, v141, v142
	v_add_f32_e32 v105, v105, v137
	v_mul_f32_e32 v147, v135, v135
	v_mul_f32_e32 v148, v123, v123
	v_fmac_f32_e32 v145, v132, v132
	v_fmac_f32_e32 v146, v120, v120
	v_add_f32_e32 v139, v143, v144
	v_add_f32_e32 v105, v105, v138
	v_mul_f32_e32 v149, v125, v125
	v_mul_f32_e32 v150, v83, v83
	v_fmac_f32_e32 v147, v134, v134
	v_fmac_f32_e32 v148, v122, v122
	v_add_f32_e32 v140, v145, v146
	v_add_f32_e32 v105, v105, v139
	v_fmac_f32_e32 v149, v124, v124
	v_fmac_f32_e32 v150, v82, v82
	v_add_f32_e32 v141, v147, v148
	v_add_f32_e32 v105, v105, v140
	v_add_f32_e32 v142, v149, v150
	v_add_f32_e32 v105, v105, v141
	v_add_f32_e32 v105, v105, v142
	s_nop 1
	v_mov_b32_dpp v136, v105 quad_perm:[1,0,3,2] row_mask:0xf bank_mask:0xf
	s_waitcnt lgkmcnt(0)
	v_add_f32_e32 v105, v105, v136
	s_nop 1
	v_mov_b32_dpp v136, v105 quad_perm:[2,3,0,1] row_mask:0xf bank_mask:0xf
	s_waitcnt lgkmcnt(0)
	v_add_f32_e32 v105, v105, v136
	s_nop 1
	v_mov_b32_dpp v136, v105 row_half_mirror row_mask:0xf bank_mask:0xf
	s_waitcnt lgkmcnt(0)
	v_add_f32_e32 v105, v105, v136
	s_nop 1
	v_mov_b32_dpp v136, v105 row_mirror row_mask:0xf bank_mask:0xf
	s_waitcnt lgkmcnt(0)
	v_add_f32_e32 v105, v105, v136
	v_mov_b32_e32 v136, v105
	s_nop 1
	v_permlane16_swap_b32_e32 v105, v136
	v_add_f32_e32 v105, v105, v136
	v_mov_b32_e32 v136, v105
	s_nop 1
	v_permlane32_swap_b32_e32 v105, v136
	v_add_f32_e32 v105, v105, v136
	v_fmamk_f32 v105, v105, 0x3a000000, v94
	v_mul_f32_e32 v136, 0x4f800000, v105
	v_cmp_gt_f32_e32 vcc, s12, v105
	s_nop 1
	v_cndmask_b32_e32 v105, v105, v136, vcc
	v_sqrt_f32_e32 v136, v105
	s_nop 0
	v_add_u32_e32 v137, -1, v136
	v_add_u32_e32 v138, 1, v136
	v_fma_f32 v139, -v137, v136, v105
	v_fma_f32 v140, -v138, v136, v105
	v_cmp_ge_f32_e64 s[2:3], 0, v139
	s_nop 1
	v_cndmask_b32_e64 v136, v136, v137, s[2:3]
	v_cmp_lt_f32_e64 s[2:3], 0, v140
	s_nop 1
	v_cndmask_b32_e64 v136, v136, v138, s[2:3]
	v_mul_f32_e32 v137, 0x37800000, v136
	v_cndmask_b32_e32 v136, v136, v137, vcc
	v_cmp_class_f32_e32 vcc, v105, v95
	s_nop 1
	v_cndmask_b32_e32 v105, v136, v105, vcc
	v_div_scale_f32 v136, s[2:3], v105, v105, 1.0
	v_rcp_f32_e32 v138, v136
	v_div_scale_f32 v137, vcc, 1.0, v105, 1.0
	v_fma_f32 v139, -v136, v138, 1.0
	v_fmac_f32_e32 v138, v139, v138
	v_mul_f32_e32 v139, v137, v138
	v_fma_f32 v140, -v136, v139, v137
	v_fmac_f32_e32 v139, v140, v138
	v_fma_f32 v136, -v136, v139, v137
	v_div_fmas_f32 v136, v136, v138, v139
	v_div_fixup_f32 v136, v136, v105, 1.0
	v_pk_mul_f32 v[106:107], v[106:107], v[136:137] op_sel_hi:[1,0]
	v_pk_mul_f32 v[108:109], v[108:109], v[136:137] op_sel_hi:[1,0]
	v_pk_mul_f32 v[110:111], v[110:111], v[136:137] op_sel_hi:[1,0]
	v_pk_mul_f32 v[112:113], v[112:113], v[136:137] op_sel_hi:[1,0]
	v_pk_mul_f32 v[126:127], v[126:127], v[136:137] op_sel_hi:[1,0]
	v_pk_mul_f32 v[114:115], v[114:115], v[136:137] op_sel_hi:[1,0]
	v_pk_mul_f32 v[128:129], v[128:129], v[136:137] op_sel_hi:[1,0]
	v_pk_mul_f32 v[138:139], v[116:117], v[136:137] op_sel_hi:[1,0]
	v_pk_mul_f32 v[130:131], v[130:131], v[136:137] op_sel_hi:[1,0]
	v_pk_mul_f32 v[140:141], v[118:119], v[136:137] op_sel_hi:[1,0]
	v_pk_mul_f32 v[132:133], v[132:133], v[136:137] op_sel_hi:[1,0]
	v_pk_mul_f32 v[142:143], v[120:121], v[136:137] op_sel_hi:[1,0]
	v_pk_mul_f32 v[134:135], v[134:135], v[136:137] op_sel_hi:[1,0]
	v_pk_mul_f32 v[144:145], v[122:123], v[136:137] op_sel_hi:[1,0]
	v_pk_mul_f32 v[146:147], v[124:125], v[136:137] op_sel_hi:[1,0]
	v_pk_mul_f32 v[82:83], v[82:83], v[136:137] op_sel_hi:[1,0]
	v_pk_mul_f32 v[108:109], v[2:3], v[108:109]
	v_pk_mul_f32 v[106:107], v[0:1], v[106:107]
	v_pk_mul_f32 v[112:113], v[6:7], v[112:113]
	v_pk_mul_f32 v[110:111], v[4:5], v[110:111]
	v_pk_mul_f32 v[116:117], v[18:19], v[114:115]
	v_pk_mul_f32 v[114:115], v[16:17], v[126:127]
	v_pk_mul_f32 v[120:121], v[22:23], v[138:139]
	v_pk_mul_f32 v[118:119], v[20:21], v[128:129]
	v_pk_mul_f32 v[124:125], v[34:35], v[140:141]
	v_pk_mul_f32 v[122:123], v[32:33], v[130:131]
	v_pk_mul_f32 v[128:129], v[38:39], v[142:143]
	v_pk_mul_f32 v[126:127], v[36:37], v[132:133]
	v_pk_mul_f32 v[132:133], v[50:51], v[144:145]
	v_pk_mul_f32 v[130:131], v[48:49], v[134:135]
	v_pk_mul_f32 v[136:137], v[54:55], v[82:83]
	v_pk_mul_f32 v[134:135], v[52:53], v[146:147]
	global_store_dwordx4 v[84:85], v[106:109], off offset:-3072 sc1
	global_store_dwordx4 v[84:85], v[110:113], off offset:-2048 sc1
	global_store_dwordx4 v[84:85], v[114:117], off offset:-1024 sc1
	global_store_dwordx4 v[80:81], v[118:121], off offset:-4096 sc1
	global_store_dwordx4 v[80:81], v[122:125], off offset:-3072 sc1
	global_store_dwordx4 v[80:81], v[126:129], off offset:-2048 sc1
	global_store_dwordx4 v[80:81], v[130:133], off offset:-1024 sc1
	global_store_dwordx4 v[80:81], v[134:137], off sc1
	v_lshl_add_u64 v[80:81], v[80:81], 0, s[24:25]
	s_cbranch_scc0 .LBB0_1613
	s_branch .LBB0_1610
